# GEMM segment edges: MMA-segment cleanup plus merged load-segment closing waits, on top of the SWA prefetch / z_setup merge version
# baseline (speedup 1.0000x reference)
; #define PG8_STAGE(bufoff, gbase, voff) do { _Pragma("unroll") for (int _i = 0; _i < 2; ++_i) \
;         __builtin_amdgcn_global_load_lds((const unsigned*)((const char*)(gbase) + (voff)[_i]), (LAS unsigned*)(lds + (bufoff) + ldsw + _i * 8192), 16, 0, 0); } while (0)
; #define PG8_LDA(dst, b, h) do { _Pragma("unroll") for (int m = 0; m < 4; ++m) dst[m] = PG8_LD32(lds + PG8_SA(b, h) + aoff + m * 2048); } while (0)
; #define PG8_LDB(dst, b, h) do { _Pragma("unroll") for (int n = 0; n < 2; ++n) dst[n] = PG8_LD32(lds + PG8_SB(b, h) + boff + n * 2048); } while (0)
; #define PG8_WAIT_V(n) asm volatile("s_waitcnt vmcnt(" #n ")" ::: "memory")
; #define PG8_WAIT_L(n) asm volatile("s_waitcnt lgkmcnt(" #n ")" ::: "memory")
; #define PG8_BAR __builtin_amdgcn_s_barrier()
; #define PG8_SCHED __builtin_amdgcn_sched_barrier(0)
; #define PG8_STA(bufoff, nextflag, h, koff) do { if constexpr (Sched::GATHER) { unsigned _o[2]; _o[0] = (nextflag) ? nxtA[h][0] : curA[h][0]; _o[1] = (nextflag) ? nxtA[h][1] : curA[h][1]; PG8_STAGE(bufoff, Ab + (koff), _o); } \
;         else { PG8_STAGE(bufoff, ((nextflag) ? nA : cA) + (size_t)(h) * hstep + (koff), voffA); } } while (0)
; template <class Epi, class Sched, bool ALIGN_EPI, int DT>
; __device__ __forceinline__ void gemm_phase(LAS unsigned char* lds, const int KB, const Sched& S, const Epi& E) {
;     ...
;             PG8_LDB(B0, 0, 0); PG8_LDB(B1, 0, 1); PG8_SCHED; PG8_LDA(At, 0, 0); PG8_STA(PG8_SA(1, 1), false, 1, k1);
;             PG8_WAIT_V(8); PG8_WAIT_L(0); PG8_BAR; PG8_MMA(0, 0, At, B0); PG8_MMA(0, 1, At, B1); PG8_BAR; PG8_SCHED;
;             PG8_LDA(At, 0, 1); PG8_STAGE(PG8_SB(0, 0), b2, voffB); PG8_STAGE(PG8_SB(0, 1), b2 + hstep, voffB); PG8_STA(PG8_SA(0, 0), last, 0, k2);
;             PG8_WAIT_V(8); PG8_WAIT_L(0); PG8_BAR; PG8_MMA(1, 0, At, B0); PG8_MMA(1, 1, At, B1); PG8_BAR; PG8_SCHED;
.LBB0_193:
	ds_read_b128 v[152:155], v175
	ds_read_b128 v[156:159], v175 offset:1024
	ds_read_b128 v[160:163], v175 offset:2048
	ds_read_b128 v[164:167], v175 offset:3072
	ds_read_b128 v[168:171], v176
	ds_read_b128 v[182:185], v176 offset:1024
	ds_read_b128 v[186:189], v176 offset:2048
	ds_read_b128 v[190:193], v176 offset:3072
	s_add_u32 s38, s36, 0x100
	s_addc_u32 s39, s37, 0
	s_add_u32 s68, s25, s36
	s_addc_u32 s69, s66, s37
	s_cmp_eq_u32 s67, 12
	s_cselect_b64 s[42:43], -1, 0
	s_and_b64 s[40:41], s[42:43], exec
	s_cselect_b32 s70, 0, s38
	s_cselect_b32 s41, s0, s69
	s_cselect_b32 s40, s23, s68
	v_lshl_add_u64 v[228:229], v[148:149], 0, s[36:37]
	s_add_i32 m0, s45, 0xc000
	ds_read_b128 v[196:199], v177
	ds_read_b128 v[200:203], v177 offset:1024
	ds_read_b128 v[204:207], v177 offset:2048
	ds_read_b128 v[208:211], v177 offset:3072
	ds_read_b128 v[212:215], v177 offset:4096
	ds_read_b128 v[216:219], v177 offset:5120
	ds_read_b128 v[220:223], v177 offset:6144
	ds_read_b128 v[224:227], v177 offset:7168
	global_load_lds_dwordx4 v[228:229], off
	v_lshl_add_u64 v[228:229], v[150:151], 0, s[36:37]
	s_add_i32 m0, s45, 0xe000
	s_nop 0
	global_load_lds_dwordx4 v[228:229], off
	s_waitcnt vmcnt(8) lgkmcnt(0)
	s_barrier
	s_setprio 1
	v_mfma_i32_16x16x64_i8 v[126:129], v[152:155], v[196:199], v[126:129]
	v_mfma_i32_16x16x64_i8 v[122:125], v[160:163], v[196:199], v[122:125]
	v_mfma_i32_16x16x64_i8 v[110:113], v[152:155], v[204:207], v[110:113]
	v_mfma_i32_16x16x64_i8 v[106:109], v[160:163], v[204:207], v[106:109]
	v_mfma_i32_16x16x64_i8 v[94:97], v[152:155], v[212:215], v[94:97]
	v_mfma_i32_16x16x64_i8 v[90:93], v[160:163], v[212:215], v[90:93]
	v_mfma_i32_16x16x64_i8 v[78:81], v[152:155], v[220:223], v[78:81]
	v_mfma_i32_16x16x64_i8 v[74:77], v[160:163], v[220:223], v[74:77]
	v_mfma_i32_16x16x64_i8 v[126:129], v[156:159], v[200:203], v[126:129]
	v_mfma_i32_16x16x64_i8 v[122:125], v[164:167], v[200:203], v[122:125]
	v_mfma_i32_16x16x64_i8 v[110:113], v[156:159], v[208:211], v[110:113]
	v_mfma_i32_16x16x64_i8 v[106:109], v[164:167], v[208:211], v[106:109]
	v_mfma_i32_16x16x64_i8 v[94:97], v[156:159], v[216:219], v[94:97]
	v_mfma_i32_16x16x64_i8 v[90:93], v[164:167], v[216:219], v[90:93]
	v_mfma_i32_16x16x64_i8 v[78:81], v[156:159], v[224:227], v[78:81]
	v_mfma_i32_16x16x64_i8 v[74:77], v[164:167], v[224:227], v[74:77]
	v_mfma_i32_16x16x64_i8 v[118:121], v[168:171], v[196:199], v[118:121]
	v_mfma_i32_16x16x64_i8 v[114:117], v[186:189], v[196:199], v[114:117]
	v_mfma_i32_16x16x64_i8 v[102:105], v[168:171], v[204:207], v[102:105]
	v_mfma_i32_16x16x64_i8 v[98:101], v[186:189], v[204:207], v[98:101]
	v_mfma_i32_16x16x64_i8 v[86:89], v[168:171], v[212:215], v[86:89]
	v_mfma_i32_16x16x64_i8 v[82:85], v[186:189], v[212:215], v[82:85]
	v_mfma_i32_16x16x64_i8 v[70:73], v[168:171], v[220:223], v[70:73]
	v_mfma_i32_16x16x64_i8 v[66:69], v[186:189], v[220:223], v[66:69]
	v_mfma_i32_16x16x64_i8 v[118:121], v[182:185], v[200:203], v[118:121]
	v_mfma_i32_16x16x64_i8 v[114:117], v[190:193], v[200:203], v[114:117]
	v_mfma_i32_16x16x64_i8 v[102:105], v[182:185], v[208:211], v[102:105]
	v_mfma_i32_16x16x64_i8 v[98:101], v[190:193], v[208:211], v[98:101]
	v_mfma_i32_16x16x64_i8 v[86:89], v[182:185], v[216:219], v[86:89]
	v_mfma_i32_16x16x64_i8 v[82:85], v[190:193], v[216:219], v[82:85]
	v_mfma_i32_16x16x64_i8 v[70:73], v[182:185], v[224:227], v[70:73]
	v_mfma_i32_16x16x64_i8 v[66:69], v[190:193], v[224:227], v[66:69]
	s_setprio 0
	s_barrier
	s_add_i32 s36, s62, s5
	v_lshl_add_u64 v[228:229], s[40:41], 0, v[134:135]
	s_mov_b32 m0, s36
	ds_read_b128 v[196:199], v177 offset:16384
	ds_read_b128 v[200:203], v177 offset:17408
	ds_read_b128 v[204:207], v177 offset:18432
	ds_read_b128 v[208:211], v177 offset:19456
	ds_read_b128 v[212:215], v177 offset:20480
	ds_read_b128 v[216:219], v177 offset:21504
	ds_read_b128 v[220:223], v177 offset:22528
	ds_read_b128 v[224:227], v177 offset:23552
	global_load_lds_dwordx4 v[228:229], off
	s_add_i32 m0, s36, 0x2000
	s_add_u32 s36, s40, 0x40000
	v_lshl_add_u64 v[230:231], s[40:41], 0, v[132:133]
	s_addc_u32 s37, s41, 0
	s_add_i32 s68, s63, s5
	global_load_lds_dwordx4 v[230:231], off
	v_lshl_add_u64 v[232:233], s[36:37], 0, v[134:135]
	s_mov_b32 m0, s68
	s_nop 0
	global_load_lds_dwordx4 v[232:233], off
	v_lshl_add_u64 v[232:233], s[36:37], 0, v[132:133]
	s_add_i32 m0, s68, 0x2000
	s_and_b64 s[36:37], s[8:9], s[42:43]
	s_and_b64 s[36:37], s[36:37], exec
	s_cselect_b32 s36, s26, s34
	s_cselect_b32 s37, s27, s35
	s_add_u32 s36, s36, s70
	s_addc_u32 s37, s37, 0
	global_load_lds_dwordx4 v[232:233], off
	v_lshl_add_u64 v[232:233], s[36:37], 0, v[136:137]
	s_mov_b32 m0, s45
	v_lshl_add_u64 v[234:235], s[36:37], 0, v[138:139]
	global_load_lds_dwordx4 v[232:233], off
	s_mov_b32 m0, s46
	s_nop 0
	global_load_lds_dwordx4 v[234:235], off
	s_waitcnt vmcnt(8) lgkmcnt(0)
	s_barrier
; #define PG8_LDA(dst, b, h) do { _Pragma("unroll") for (int m = 0; m < 4; ++m) dst[m] = PG8_LD32(lds + PG8_SA(b, h) + aoff + m * 2048); } while (0)
; #define PG8_LDB(dst, b, h) do { _Pragma("unroll") for (int n = 0; n < 2; ++n) dst[n] = PG8_LD32(lds + PG8_SB(b, h) + boff + n * 2048); } while (0)
; #define PG8_WAIT_V(n) asm volatile("s_waitcnt vmcnt(" #n ")" ::: "memory")
; #define PG8_WAIT_L(n) asm volatile("s_waitcnt lgkmcnt(" #n ")" ::: "memory")
; #define PG8_BAR __builtin_amdgcn_s_barrier()
; #define PG8_SCHED __builtin_amdgcn_sched_barrier(0)
; #define PG8_STA(bufoff, nextflag, h, koff) do { if constexpr (Sched::GATHER) { unsigned _o[2]; _o[0] = (nextflag) ? nxtA[h][0] : curA[h][0]; _o[1] = (nextflag) ? nxtA[h][1] : curA[h][1]; PG8_STAGE(bufoff, Ab + (koff), _o); } \
;         else { PG8_STAGE(bufoff, ((nextflag) ? nA : cA) + (size_t)(h) * hstep + (koff), voffA); } } while (0)
; template <class Epi, class Sched, bool ALIGN_EPI, int DT>
; __device__ __forceinline__ void gemm_phase(LAS unsigned char* lds, const int KB, const Sched& S, const Epi& E) {
;     ...
;             PG8_WAIT_V(8); PG8_WAIT_L(0); PG8_BAR; PG8_MMA(1, 0, At, B0); PG8_MMA(1, 1, At, B1); PG8_BAR; PG8_SCHED;
;             PG8_LDB(B0, 1, 0); PG8_LDB(B1, 1, 1); PG8_SCHED; PG8_LDA(At, 1, 0); PG8_STA(PG8_SA(0, 1), last, 1, k2);
;             PG8_WAIT_V(8); PG8_WAIT_L(0); PG8_BAR; PG8_MMA(0, 0, At, B0); PG8_MMA(0, 1, At, B1); PG8_BAR; PG8_SCHED;
	s_setprio 1
	v_mfma_i32_16x16x64_i8 v[62:65], v[152:155], v[196:199], v[62:65]
	v_mfma_i32_16x16x64_i8 v[58:61], v[160:163], v[196:199], v[58:61]
	v_mfma_i32_16x16x64_i8 v[46:49], v[152:155], v[204:207], v[46:49]
	v_mfma_i32_16x16x64_i8 v[42:45], v[160:163], v[204:207], v[42:45]
	v_mfma_i32_16x16x64_i8 v[30:33], v[152:155], v[212:215], v[30:33]
	v_mfma_i32_16x16x64_i8 v[26:29], v[160:163], v[212:215], v[26:29]
	v_mfma_i32_16x16x64_i8 v[6:9], v[152:155], v[220:223], v[6:9]
	v_mfma_i32_16x16x64_i8 v[2:5], v[160:163], v[220:223], v[2:5]
	v_mfma_i32_16x16x64_i8 v[62:65], v[156:159], v[200:203], v[62:65]
	v_mfma_i32_16x16x64_i8 v[58:61], v[164:167], v[200:203], v[58:61]
	v_mfma_i32_16x16x64_i8 v[46:49], v[156:159], v[208:211], v[46:49]
	v_mfma_i32_16x16x64_i8 v[42:45], v[164:167], v[208:211], v[42:45]
	v_mfma_i32_16x16x64_i8 v[30:33], v[156:159], v[216:219], v[30:33]
	v_mfma_i32_16x16x64_i8 v[26:29], v[164:167], v[216:219], v[26:29]
	v_mfma_i32_16x16x64_i8 v[6:9], v[156:159], v[224:227], v[6:9]
	v_mfma_i32_16x16x64_i8 v[2:5], v[164:167], v[224:227], v[2:5]
	v_mfma_i32_16x16x64_i8 v[54:57], v[168:171], v[196:199], v[54:57]
	v_mfma_i32_16x16x64_i8 v[50:53], v[186:189], v[196:199], v[50:53]
	v_mfma_i32_16x16x64_i8 v[38:41], v[168:171], v[204:207], v[38:41]
	v_mfma_i32_16x16x64_i8 v[34:37], v[186:189], v[204:207], v[34:37]
	v_mfma_i32_16x16x64_i8 v[14:17], v[168:171], v[212:215], v[14:17]
	v_mfma_i32_16x16x64_i8 v[10:13], v[186:189], v[212:215], v[10:13]
	v_mfma_i32_16x16x64_i8 v[22:25], v[168:171], v[220:223], v[22:25]
	v_mfma_i32_16x16x64_i8 v[18:21], v[186:189], v[220:223], v[18:21]
	v_mfma_i32_16x16x64_i8 v[54:57], v[182:185], v[200:203], v[54:57]
	v_mfma_i32_16x16x64_i8 v[50:53], v[190:193], v[200:203], v[50:53]
	v_mfma_i32_16x16x64_i8 v[38:41], v[182:185], v[208:211], v[38:41]
	v_mfma_i32_16x16x64_i8 v[34:37], v[190:193], v[208:211], v[34:37]
	v_mfma_i32_16x16x64_i8 v[14:17], v[182:185], v[216:219], v[14:17]
	v_mfma_i32_16x16x64_i8 v[10:13], v[190:193], v[216:219], v[10:13]
	v_mfma_i32_16x16x64_i8 v[22:25], v[182:185], v[224:227], v[22:25]
	v_mfma_i32_16x16x64_i8 v[18:21], v[190:193], v[224:227], v[18:21]
	s_setprio 0
	s_barrier
	s_add_i32 s42, 0, 0x18000
	v_add_u32_e32 v1, s42, v173
	s_add_i32 s43, 0, 0x1c000
	ds_read_b128 v[152:155], v1
	ds_read_b128 v[156:159], v1 offset:1024
	ds_read_b128 v[160:163], v1 offset:2048
	ds_read_b128 v[164:167], v1 offset:3072
	v_add_u32_e32 v1, s43, v173
	ds_read_b128 v[168:171], v1
	ds_read_b128 v[182:185], v1 offset:1024
	ds_read_b128 v[186:189], v1 offset:2048
	ds_read_b128 v[190:193], v1 offset:3072
	s_add_u32 s36, s36, 0x40000
	s_addc_u32 s37, s37, 0
	s_mov_b32 m0, s47
	v_lshl_add_u64 v[236:237], s[36:37], 0, v[136:137]
	ds_read_b128 v[196:199], v177 offset:32768
	ds_read_b128 v[200:203], v177 offset:33792
	ds_read_b128 v[204:207], v177 offset:34816
	ds_read_b128 v[208:211], v177 offset:35840
	ds_read_b128 v[212:215], v177 offset:36864
	ds_read_b128 v[216:219], v177 offset:37888
	ds_read_b128 v[220:223], v177 offset:38912
	ds_read_b128 v[224:227], v177 offset:39936
	global_load_lds_dwordx4 v[236:237], off
	v_lshl_add_u64 v[236:237], s[36:37], 0, v[138:139]
	s_mov_b32 m0, s49
	s_nop 0
	global_load_lds_dwordx4 v[236:237], off
	s_waitcnt vmcnt(8) lgkmcnt(0)
	s_barrier
	s_setprio 1
	v_mfma_i32_16x16x64_i8 v[126:129], v[152:155], v[196:199], v[126:129]
	v_mfma_i32_16x16x64_i8 v[122:125], v[160:163], v[196:199], v[122:125]
	v_mfma_i32_16x16x64_i8 v[110:113], v[152:155], v[204:207], v[110:113]
	v_mfma_i32_16x16x64_i8 v[106:109], v[160:163], v[204:207], v[106:109]
	v_mfma_i32_16x16x64_i8 v[94:97], v[152:155], v[212:215], v[94:97]
	v_mfma_i32_16x16x64_i8 v[90:93], v[160:163], v[212:215], v[90:93]
	v_mfma_i32_16x16x64_i8 v[78:81], v[152:155], v[220:223], v[78:81]
	v_mfma_i32_16x16x64_i8 v[74:77], v[160:163], v[220:223], v[74:77]
	v_mfma_i32_16x16x64_i8 v[126:129], v[156:159], v[200:203], v[126:129]
	v_mfma_i32_16x16x64_i8 v[122:125], v[164:167], v[200:203], v[122:125]
	v_mfma_i32_16x16x64_i8 v[110:113], v[156:159], v[208:211], v[110:113]
	v_mfma_i32_16x16x64_i8 v[106:109], v[164:167], v[208:211], v[106:109]
	v_mfma_i32_16x16x64_i8 v[94:97], v[156:159], v[216:219], v[94:97]
	v_mfma_i32_16x16x64_i8 v[90:93], v[164:167], v[216:219], v[90:93]
	v_mfma_i32_16x16x64_i8 v[78:81], v[156:159], v[224:227], v[78:81]
	v_mfma_i32_16x16x64_i8 v[74:77], v[164:167], v[224:227], v[74:77]
	v_mfma_i32_16x16x64_i8 v[118:121], v[168:171], v[196:199], v[118:121]
	v_mfma_i32_16x16x64_i8 v[114:117], v[186:189], v[196:199], v[114:117]
	v_mfma_i32_16x16x64_i8 v[102:105], v[168:171], v[204:207], v[102:105]
	v_mfma_i32_16x16x64_i8 v[98:101], v[186:189], v[204:207], v[98:101]
	v_mfma_i32_16x16x64_i8 v[86:89], v[168:171], v[212:215], v[86:89]
	v_mfma_i32_16x16x64_i8 v[82:85], v[186:189], v[212:215], v[82:85]
	v_mfma_i32_16x16x64_i8 v[70:73], v[168:171], v[220:223], v[70:73]
	v_mfma_i32_16x16x64_i8 v[66:69], v[186:189], v[220:223], v[66:69]
	v_mfma_i32_16x16x64_i8 v[118:121], v[182:185], v[200:203], v[118:121]
	v_mfma_i32_16x16x64_i8 v[114:117], v[190:193], v[200:203], v[114:117]
	v_mfma_i32_16x16x64_i8 v[102:105], v[182:185], v[208:211], v[102:105]
	v_mfma_i32_16x16x64_i8 v[98:101], v[190:193], v[208:211], v[98:101]
	v_mfma_i32_16x16x64_i8 v[86:89], v[182:185], v[216:219], v[86:89]
	v_mfma_i32_16x16x64_i8 v[82:85], v[190:193], v[216:219], v[82:85]
	v_mfma_i32_16x16x64_i8 v[70:73], v[182:185], v[224:227], v[70:73]
	v_mfma_i32_16x16x64_i8 v[66:69], v[190:193], v[224:227], v[66:69]
	s_setprio 0
	s_barrier
; #define PG8_STAGE(bufoff, gbase, voff) do { _Pragma("unroll") for (int _i = 0; _i < 2; ++_i) \
;         __builtin_amdgcn_global_load_lds((const unsigned*)((const char*)(gbase) + (voff)[_i]), (LAS unsigned*)(lds + (bufoff) + ldsw + _i * 8192), 16, 0, 0); } while (0)
; #define PG8_LDA(dst, b, h) do { _Pragma("unroll") for (int m = 0; m < 4; ++m) dst[m] = PG8_LD32(lds + PG8_SA(b, h) + aoff + m * 2048); } while (0)
; #define PG8_WAIT_V(n) asm volatile("s_waitcnt vmcnt(" #n ")" ::: "memory")
; #define PG8_WAIT_L(n) asm volatile("s_waitcnt lgkmcnt(" #n ")" ::: "memory")
; #define PG8_BAR __builtin_amdgcn_s_barrier()
; #define PG8_SCHED __builtin_amdgcn_sched_barrier(0)
; #define PG8_STA(bufoff, nextflag, h, koff) do { if constexpr (Sched::GATHER) { unsigned _o[2]; _o[0] = (nextflag) ? nxtA[h][0] : curA[h][0]; _o[1] = (nextflag) ? nxtA[h][1] : curA[h][1]; PG8_STAGE(bufoff, Ab + (koff), _o); } \
;         else { PG8_STAGE(bufoff, ((nextflag) ? nA : cA) + (size_t)(h) * hstep + (koff), voffA); } } while (0)
; template <class Epi, class Sched, bool ALIGN_EPI, int DT>
; __device__ __forceinline__ void gemm_phase(LAS unsigned char* lds, const int KB, const Sched& S, const Epi& E) {
;     ...
;             PG8_LDA(At, 1, 1); PG8_STAGE(PG8_SB(1, 0), b3, voffB); PG8_STAGE(PG8_SB(1, 1), b3 + hstep, voffB); PG8_STA(PG8_SA(1, 0), last, 0, k3);
;             PG8_WAIT_V(8); PG8_WAIT_L(0); PG8_BAR; PG8_MMA(1, 0, At, B0); PG8_MMA(1, 1, At, B1); PG8_BAR; PG8_SCHED;
;         }
;         if constexpr (ALIGN_EPI) { if (wr == 0) PG8_BAR; }
	s_add_i32 s36, s42, s5
	v_lshl_add_u64 v[228:229], v[228:229], 0, s[18:19]
	s_mov_b32 m0, s36
	ds_read_b128 v[196:199], v177 offset:49152
	ds_read_b128 v[200:203], v177 offset:50176
	ds_read_b128 v[204:207], v177 offset:51200
	ds_read_b128 v[208:211], v177 offset:52224
	ds_read_b128 v[212:215], v177 offset:53248
	ds_read_b128 v[216:219], v177 offset:54272
	ds_read_b128 v[220:223], v177 offset:55296
	ds_read_b128 v[224:227], v177 offset:56320
	global_load_lds_dwordx4 v[228:229], off
	s_add_i32 m0, s36, 0x2000
	s_add_u32 s36, s40, 0x40080
	v_lshl_add_u64 v[228:229], v[230:231], 0, s[18:19]
	s_addc_u32 s37, s41, 0
	s_add_i32 s40, s43, s5
	global_load_lds_dwordx4 v[228:229], off
	v_lshl_add_u64 v[228:229], s[36:37], 0, v[134:135]
	s_mov_b32 m0, s40
	s_nop 0
	global_load_lds_dwordx4 v[228:229], off
	v_lshl_add_u64 v[228:229], s[36:37], 0, v[132:133]
	s_add_i32 m0, s40, 0x2000
	s_nop 0
	global_load_lds_dwordx4 v[228:229], off
	v_lshl_add_u64 v[228:229], v[232:233], 0, s[18:19]
	s_mov_b32 m0, s55
	s_nop 0
	global_load_lds_dwordx4 v[228:229], off
	v_lshl_add_u64 v[228:229], v[234:235], 0, s[18:19]
	s_mov_b32 m0, s56
	s_nop 0
	global_load_lds_dwordx4 v[228:229], off
	s_waitcnt vmcnt(8) lgkmcnt(0)
	s_barrier
	s_setprio 1
	v_mfma_i32_16x16x64_i8 v[62:65], v[152:155], v[196:199], v[62:65]
	v_mfma_i32_16x16x64_i8 v[58:61], v[160:163], v[196:199], v[58:61]
	v_mfma_i32_16x16x64_i8 v[46:49], v[152:155], v[204:207], v[46:49]
	v_mfma_i32_16x16x64_i8 v[42:45], v[160:163], v[204:207], v[42:45]
	v_mfma_i32_16x16x64_i8 v[30:33], v[152:155], v[212:215], v[30:33]
	v_mfma_i32_16x16x64_i8 v[26:29], v[160:163], v[212:215], v[26:29]
	v_mfma_i32_16x16x64_i8 v[6:9], v[152:155], v[220:223], v[6:9]
	v_mfma_i32_16x16x64_i8 v[2:5], v[160:163], v[220:223], v[2:5]
	v_mfma_i32_16x16x64_i8 v[62:65], v[156:159], v[200:203], v[62:65]
	v_mfma_i32_16x16x64_i8 v[58:61], v[164:167], v[200:203], v[58:61]
	v_mfma_i32_16x16x64_i8 v[46:49], v[156:159], v[208:211], v[46:49]
	v_mfma_i32_16x16x64_i8 v[42:45], v[164:167], v[208:211], v[42:45]
	v_mfma_i32_16x16x64_i8 v[30:33], v[156:159], v[216:219], v[30:33]
	v_mfma_i32_16x16x64_i8 v[26:29], v[164:167], v[216:219], v[26:29]
	v_mfma_i32_16x16x64_i8 v[6:9], v[156:159], v[224:227], v[6:9]
	v_mfma_i32_16x16x64_i8 v[2:5], v[164:167], v[224:227], v[2:5]
	v_mfma_i32_16x16x64_i8 v[54:57], v[168:171], v[196:199], v[54:57]
	v_mfma_i32_16x16x64_i8 v[50:53], v[186:189], v[196:199], v[50:53]
	v_mfma_i32_16x16x64_i8 v[38:41], v[168:171], v[204:207], v[38:41]
	v_mfma_i32_16x16x64_i8 v[34:37], v[186:189], v[204:207], v[34:37]
	v_mfma_i32_16x16x64_i8 v[14:17], v[168:171], v[212:215], v[14:17]
	v_mfma_i32_16x16x64_i8 v[10:13], v[186:189], v[212:215], v[10:13]
	v_mfma_i32_16x16x64_i8 v[22:25], v[168:171], v[220:223], v[22:25]
	v_mfma_i32_16x16x64_i8 v[18:21], v[186:189], v[220:223], v[18:21]
	v_mfma_i32_16x16x64_i8 v[54:57], v[182:185], v[200:203], v[54:57]
	v_mfma_i32_16x16x64_i8 v[50:53], v[190:193], v[200:203], v[50:53]
	v_mfma_i32_16x16x64_i8 v[38:41], v[182:185], v[208:211], v[38:41]
	v_mfma_i32_16x16x64_i8 v[34:37], v[190:193], v[208:211], v[34:37]
	v_mfma_i32_16x16x64_i8 v[14:17], v[182:185], v[216:219], v[14:17]
	v_mfma_i32_16x16x64_i8 v[10:13], v[190:193], v[216:219], v[10:13]
	v_mfma_i32_16x16x64_i8 v[22:25], v[182:185], v[224:227], v[22:25]
	v_mfma_i32_16x16x64_i8 v[18:21], v[190:193], v[224:227], v[18:21]
	s_setprio 0
	s_barrier
	s_add_i32 s67, s67, 2
	s_cmp_gt_u32 s67, 13
	s_mov_b64 s[36:37], s[38:39]
	s_cbranch_scc0 .LBB0_193
	s_and_b64 vcc, exec, s[20:21]
	s_cbranch_vccz .LBB0_196
	s_barrier

; #define PG8_STAGE(bufoff, gbase, voff) do { _Pragma("unroll") for (int _i = 0; _i < 2; ++_i) \
;         __builtin_amdgcn_global_load_lds((const unsigned*)((const char*)(gbase) + (voff)[_i]), (LAS unsigned*)(lds + (bufoff) + ldsw + _i * 8192), 16, 0, 0); } while (0)
; #define PG8_LDA(dst, b, h) do { _Pragma("unroll") for (int m = 0; m < 4; ++m) dst[m] = PG8_LD32(lds + PG8_SA(b, h) + aoff + m * 2048); } while (0)
; #define PG8_LDB(dst, b, h) do { _Pragma("unroll") for (int n = 0; n < 2; ++n) dst[n] = PG8_LD32(lds + PG8_SB(b, h) + boff + n * 2048); } while (0)
; #define PG8_WAIT_V(n) asm volatile("s_waitcnt vmcnt(" #n ")" ::: "memory")
; #define PG8_WAIT_L(n) asm volatile("s_waitcnt lgkmcnt(" #n ")" ::: "memory")
; #define PG8_BAR __builtin_amdgcn_s_barrier()
; #define PG8_SCHED __builtin_amdgcn_sched_barrier(0)
; #define PG8_STA(bufoff, nextflag, h, koff) do { if constexpr (Sched::GATHER) { unsigned _o[2]; _o[0] = (nextflag) ? nxtA[h][0] : curA[h][0]; _o[1] = (nextflag) ? nxtA[h][1] : curA[h][1]; PG8_STAGE(bufoff, Ab + (koff), _o); } \
;         else { PG8_STAGE(bufoff, ((nextflag) ? nA : cA) + (size_t)(h) * hstep + (koff), voffA); } } while (0)
; template <class Epi, class Sched, bool ALIGN_EPI, int DT>
; __device__ __forceinline__ void gemm_phase(LAS unsigned char* lds, const int KB, const Sched& S, const Epi& E) {
;     ...
;             PG8_LDB(B0, 0, 0); PG8_LDB(B1, 0, 1); PG8_SCHED; PG8_LDA(At, 0, 0); PG8_STA(PG8_SA(1, 1), false, 1, k1);
;             PG8_WAIT_V(8); PG8_WAIT_L(0); PG8_BAR; PG8_MMA(0, 0, At, B0); PG8_MMA(0, 1, At, B1); PG8_BAR; PG8_SCHED;
;             PG8_LDA(At, 0, 1); PG8_STAGE(PG8_SB(0, 0), b2, voffB); PG8_STAGE(PG8_SB(0, 1), b2 + hstep, voffB); PG8_STA(PG8_SA(0, 0), last, 0, k2);
;             PG8_WAIT_V(8); PG8_WAIT_L(0); PG8_BAR; PG8_MMA(1, 0, At, B0); PG8_MMA(1, 1, At, B1); PG8_BAR; PG8_SCHED;
.LBB0_1018:
	ds_read_b128 v[18:21], v193
	ds_read_b128 v[22:25], v193 offset:1024
	ds_read_b128 v[26:29], v193 offset:2048
	ds_read_b128 v[30:33], v193 offset:3072
	ds_read_b128 v[2:5], v195
	ds_read_b128 v[6:9], v195 offset:1024
	ds_read_b128 v[10:13], v195 offset:2048
	ds_read_b128 v[14:17], v195 offset:3072
	s_add_u32 s34, s38, 0x100
	s_addc_u32 s35, s39, 0
	s_add_u32 s68, s63, s38
	s_addc_u32 s69, s66, s39
	s_cmp_eq_u32 s67, 12
	s_cselect_b64 s[40:41], -1, 0
	s_and_b64 s[36:37], s[40:41], exec
	s_cselect_b32 s37, s21, s69
	s_cselect_b32 s36, s23, s68
	s_cselect_b32 s68, 0, s35
	s_cselect_b32 s69, 0, s34
	v_lshl_add_u64 v[222:223], v[178:179], 0, s[38:39]
	s_add_i32 m0, s29, 0xc000
	ds_read_b128 v[182:185], v196
	ds_read_b128 v[186:189], v196 offset:1024
	ds_read_b128 v[198:201], v196 offset:2048
	ds_read_b128 v[202:205], v196 offset:3072
	ds_read_b128 v[206:209], v196 offset:4096
	ds_read_b128 v[210:213], v196 offset:5120
	ds_read_b128 v[214:217], v196 offset:6144
	ds_read_b128 v[218:221], v196 offset:7168
	global_load_lds_dwordx4 v[222:223], off
	v_lshl_add_u64 v[222:223], v[180:181], 0, s[38:39]
	s_add_i32 m0, s29, 0xe000
	s_nop 0
	global_load_lds_dwordx4 v[222:223], off
	s_waitcnt vmcnt(8) lgkmcnt(0)
	s_barrier
	s_setprio 1
	v_mfma_scale_f32_16x16x128_f8f6f4 v[158:161], v[18:25], v[182:189], v[158:161], v190, v190 op_sel_hi:[0,0,0]
	v_mfma_scale_f32_16x16x128_f8f6f4 v[154:157], v[26:33], v[182:189], v[154:157], v190, v190 op_sel_hi:[0,0,0]
	v_mfma_scale_f32_16x16x128_f8f6f4 v[150:153], v[18:25], v[198:205], v[150:153], v190, v190 op_sel_hi:[0,0,0]
	v_mfma_scale_f32_16x16x128_f8f6f4 v[142:145], v[26:33], v[198:205], v[142:145], v190, v190 op_sel_hi:[0,0,0]
	v_mfma_scale_f32_16x16x128_f8f6f4 v[134:137], v[18:25], v[206:213], v[134:137], v190, v190 op_sel_hi:[0,0,0]
	v_mfma_scale_f32_16x16x128_f8f6f4 v[126:129], v[26:33], v[206:213], v[126:129], v190, v190 op_sel_hi:[0,0,0]
	v_mfma_scale_f32_16x16x128_f8f6f4 v[118:121], v[18:25], v[214:221], v[118:121], v190, v190 op_sel_hi:[0,0,0]
	v_mfma_scale_f32_16x16x128_f8f6f4 v[110:113], v[26:33], v[214:221], v[110:113], v190, v190 op_sel_hi:[0,0,0]
	v_mfma_scale_f32_16x16x128_f8f6f4 v[146:149], v[2:9], v[182:189], v[146:149], v190, v190 op_sel_hi:[0,0,0]
	v_mfma_scale_f32_16x16x128_f8f6f4 v[138:141], v[10:17], v[182:189], v[138:141], v190, v190 op_sel_hi:[0,0,0]
	v_mfma_scale_f32_16x16x128_f8f6f4 v[130:133], v[2:9], v[198:205], v[130:133], v190, v190 op_sel_hi:[0,0,0]
	v_mfma_scale_f32_16x16x128_f8f6f4 v[122:125], v[10:17], v[198:205], v[122:125], v190, v190 op_sel_hi:[0,0,0]
	v_mfma_scale_f32_16x16x128_f8f6f4 v[114:117], v[2:9], v[206:213], v[114:117], v190, v190 op_sel_hi:[0,0,0]
	v_mfma_scale_f32_16x16x128_f8f6f4 v[106:109], v[10:17], v[206:213], v[106:109], v190, v190 op_sel_hi:[0,0,0]
	v_mfma_scale_f32_16x16x128_f8f6f4 v[102:105], v[2:9], v[214:221], v[102:105], v190, v190 op_sel_hi:[0,0,0]
	v_mfma_scale_f32_16x16x128_f8f6f4 v[98:101], v[10:17], v[214:221], v[98:101], v190, v190 op_sel_hi:[0,0,0]
	s_setprio 0
	s_barrier
	s_add_i32 s38, s53, s42
	v_lshl_add_u64 v[182:183], s[36:37], 0, v[162:163]
	s_mov_b32 m0, s38
	ds_read_b128 v[198:201], v196 offset:16384
	ds_read_b128 v[202:205], v196 offset:17408
	ds_read_b128 v[206:209], v196 offset:18432
	ds_read_b128 v[210:213], v196 offset:19456
	ds_read_b128 v[214:217], v196 offset:20480
	ds_read_b128 v[218:221], v196 offset:21504
	ds_read_b128 v[222:225], v196 offset:22528
	ds_read_b128 v[226:229], v196 offset:23552
	global_load_lds_dwordx4 v[182:183], off
	s_add_i32 m0, s38, 0x2000
	s_add_u32 s38, s36, 0x40000
	v_lshl_add_u64 v[184:185], s[36:37], 0, v[164:165]
	s_addc_u32 s39, s37, 0
	s_add_i32 s70, s54, s42
	global_load_lds_dwordx4 v[184:185], off
	v_lshl_add_u64 v[186:187], s[38:39], 0, v[162:163]
	s_mov_b32 m0, s70
	s_nop 0
	global_load_lds_dwordx4 v[186:187], off
	v_lshl_add_u64 v[186:187], s[38:39], 0, v[164:165]
	s_add_i32 m0, s70, 0x2000
	s_and_b64 s[38:39], s[6:7], s[40:41]
	s_and_b64 s[38:39], s[38:39], exec
	s_cselect_b32 s38, s24, s30
	s_cselect_b32 s39, s25, s31
	s_add_u32 s38, s38, s69
	s_addc_u32 s39, s39, s68
	global_load_lds_dwordx4 v[186:187], off
	v_lshl_add_u64 v[186:187], s[38:39], 0, v[166:167]
	s_mov_b32 m0, s29
	v_lshl_add_u64 v[188:189], s[38:39], 0, v[168:169]
	global_load_lds_dwordx4 v[186:187], off
	s_mov_b32 m0, s43
	s_nop 0
	global_load_lds_dwordx4 v[188:189], off
	s_waitcnt vmcnt(8) lgkmcnt(0)
	s_barrier
	s_setprio 1
	v_mfma_scale_f32_16x16x128_f8f6f4 v[94:97], v[18:25], v[198:205], v[94:97], v190, v190 op_sel_hi:[0,0,0]
	v_mfma_scale_f32_16x16x128_f8f6f4 v[90:93], v[26:33], v[198:205], v[90:93], v190, v190 op_sel_hi:[0,0,0]
	v_mfma_scale_f32_16x16x128_f8f6f4 v[86:89], v[18:25], v[206:213], v[86:89], v190, v190 op_sel_hi:[0,0,0]
	v_mfma_scale_f32_16x16x128_f8f6f4 v[78:81], v[26:33], v[206:213], v[78:81], v190, v190 op_sel_hi:[0,0,0]
	v_mfma_scale_f32_16x16x128_f8f6f4 v[62:65], v[18:25], v[214:221], v[62:65], v190, v190 op_sel_hi:[0,0,0]
	v_mfma_scale_f32_16x16x128_f8f6f4 v[54:57], v[26:33], v[214:221], v[54:57], v190, v190 op_sel_hi:[0,0,0]
	v_mfma_scale_f32_16x16x128_f8f6f4 v[46:49], v[18:25], v[222:229], v[46:49], v190, v190 op_sel_hi:[0,0,0]
	v_mfma_scale_f32_16x16x128_f8f6f4 v[38:41], v[26:33], v[222:229], v[38:41], v190, v190 op_sel_hi:[0,0,0]
	v_mfma_scale_f32_16x16x128_f8f6f4 v[82:85], v[2:9], v[198:205], v[82:85], v190, v190 op_sel_hi:[0,0,0]
	v_mfma_scale_f32_16x16x128_f8f6f4 v[74:77], v[10:17], v[198:205], v[74:77], v190, v190 op_sel_hi:[0,0,0]
	v_mfma_scale_f32_16x16x128_f8f6f4 v[58:61], v[2:9], v[206:213], v[58:61], v190, v190 op_sel_hi:[0,0,0]
	v_mfma_scale_f32_16x16x128_f8f6f4 v[50:53], v[10:17], v[206:213], v[50:53], v190, v190 op_sel_hi:[0,0,0]
	v_mfma_scale_f32_16x16x128_f8f6f4 v[42:45], v[2:9], v[214:221], v[42:45], v190, v190 op_sel_hi:[0,0,0]
	v_mfma_scale_f32_16x16x128_f8f6f4 v[34:37], v[10:17], v[214:221], v[34:37], v190, v190 op_sel_hi:[0,0,0]
	v_mfma_scale_f32_16x16x128_f8f6f4 v[70:73], v[2:9], v[222:229], v[70:73], v190, v190 op_sel_hi:[0,0,0]
	v_mfma_scale_f32_16x16x128_f8f6f4 v[66:69], v[10:17], v[222:229], v[66:69], v190, v190 op_sel_hi:[0,0,0]
	s_setprio 0
	s_barrier
; #define PG8_STAGE(bufoff, gbase, voff) do { _Pragma("unroll") for (int _i = 0; _i < 2; ++_i) \
;         __builtin_amdgcn_global_load_lds((const unsigned*)((const char*)(gbase) + (voff)[_i]), (LAS unsigned*)(lds + (bufoff) + ldsw + _i * 8192), 16, 0, 0); } while (0)
; #define PG8_LDA(dst, b, h) do { _Pragma("unroll") for (int m = 0; m < 4; ++m) dst[m] = PG8_LD32(lds + PG8_SA(b, h) + aoff + m * 2048); } while (0)
; #define PG8_LDB(dst, b, h) do { _Pragma("unroll") for (int n = 0; n < 2; ++n) dst[n] = PG8_LD32(lds + PG8_SB(b, h) + boff + n * 2048); } while (0)
; #define PG8_WAIT_V(n) asm volatile("s_waitcnt vmcnt(" #n ")" ::: "memory")
; #define PG8_WAIT_L(n) asm volatile("s_waitcnt lgkmcnt(" #n ")" ::: "memory")
; #define PG8_BAR __builtin_amdgcn_s_barrier()
; #define PG8_SCHED __builtin_amdgcn_sched_barrier(0)
; #define PG8_STA(bufoff, nextflag, h, koff) do { if constexpr (Sched::GATHER) { unsigned _o[2]; _o[0] = (nextflag) ? nxtA[h][0] : curA[h][0]; _o[1] = (nextflag) ? nxtA[h][1] : curA[h][1]; PG8_STAGE(bufoff, Ab + (koff), _o); } \
;         else { PG8_STAGE(bufoff, ((nextflag) ? nA : cA) + (size_t)(h) * hstep + (koff), voffA); } } while (0)
; template <class Epi, class Sched, bool ALIGN_EPI, int DT>
; __device__ __forceinline__ void gemm_phase(LAS unsigned char* lds, const int KB, const Sched& S, const Epi& E) {
;     ...
;             PG8_LDB(B0, 1, 0); PG8_LDB(B1, 1, 1); PG8_SCHED; PG8_LDA(At, 1, 0); PG8_STA(PG8_SA(0, 1), last, 1, k2);
;             PG8_WAIT_V(8); PG8_WAIT_L(0); PG8_BAR; PG8_MMA(0, 0, At, B0); PG8_MMA(0, 1, At, B1); PG8_BAR; PG8_SCHED;
;             PG8_LDA(At, 1, 1); PG8_STAGE(PG8_SB(1, 0), b3, voffB); PG8_STAGE(PG8_SB(1, 1), b3 + hstep, voffB); PG8_STA(PG8_SA(1, 0), last, 0, k3);
;             PG8_WAIT_V(8); PG8_WAIT_L(0); PG8_BAR; PG8_MMA(1, 0, At, B0); PG8_MMA(1, 1, At, B1); PG8_BAR; PG8_SCHED;
;         }
;         if constexpr (ALIGN_EPI) { if (wr == 0) PG8_BAR; }
	s_add_i32 s40, 0, 0x18000
	s_add_i32 s41, 0, 0x1c000
	v_add_u32_e32 v14, s40, v191
	v_add_u32_e32 v30, s41, v191
	ds_read_b128 v[2:5], v14
	ds_read_b128 v[6:9], v14 offset:1024
	ds_read_b128 v[10:13], v14 offset:2048
	ds_read_b128 v[14:17], v14 offset:3072
	ds_read_b128 v[18:21], v30
	ds_read_b128 v[22:25], v30 offset:1024
	ds_read_b128 v[26:29], v30 offset:2048
	ds_read_b128 v[30:33], v30 offset:3072
	s_add_u32 s38, s38, 0x40000
	s_addc_u32 s39, s39, 0
	s_mov_b32 m0, s44
	v_lshl_add_u64 v[230:231], s[38:39], 0, v[166:167]
	ds_read_b128 v[198:201], v196 offset:32768
	ds_read_b128 v[202:205], v196 offset:33792
	ds_read_b128 v[206:209], v196 offset:34816
	ds_read_b128 v[210:213], v196 offset:35840
	ds_read_b128 v[214:217], v196 offset:36864
	ds_read_b128 v[218:221], v196 offset:37888
	ds_read_b128 v[222:225], v196 offset:38912
	ds_read_b128 v[226:229], v196 offset:39936
	global_load_lds_dwordx4 v[230:231], off
	v_lshl_add_u64 v[230:231], s[38:39], 0, v[168:169]
	s_mov_b32 m0, s45
	s_nop 0
	global_load_lds_dwordx4 v[230:231], off
	s_waitcnt vmcnt(8) lgkmcnt(0)
	s_barrier
	s_setprio 1
	v_mfma_scale_f32_16x16x128_f8f6f4 v[158:161], v[2:9], v[198:205], v[158:161], v190, v190 op_sel_hi:[0,0,0]
	v_mfma_scale_f32_16x16x128_f8f6f4 v[154:157], v[10:17], v[198:205], v[154:157], v190, v190 op_sel_hi:[0,0,0]
	v_mfma_scale_f32_16x16x128_f8f6f4 v[150:153], v[2:9], v[206:213], v[150:153], v190, v190 op_sel_hi:[0,0,0]
	v_mfma_scale_f32_16x16x128_f8f6f4 v[142:145], v[10:17], v[206:213], v[142:145], v190, v190 op_sel_hi:[0,0,0]
	v_mfma_scale_f32_16x16x128_f8f6f4 v[134:137], v[2:9], v[214:221], v[134:137], v190, v190 op_sel_hi:[0,0,0]
	v_mfma_scale_f32_16x16x128_f8f6f4 v[126:129], v[10:17], v[214:221], v[126:129], v190, v190 op_sel_hi:[0,0,0]
	v_mfma_scale_f32_16x16x128_f8f6f4 v[118:121], v[2:9], v[222:229], v[118:121], v190, v190 op_sel_hi:[0,0,0]
	v_mfma_scale_f32_16x16x128_f8f6f4 v[110:113], v[10:17], v[222:229], v[110:113], v190, v190 op_sel_hi:[0,0,0]
	v_mfma_scale_f32_16x16x128_f8f6f4 v[146:149], v[18:25], v[198:205], v[146:149], v190, v190 op_sel_hi:[0,0,0]
	v_mfma_scale_f32_16x16x128_f8f6f4 v[138:141], v[26:33], v[198:205], v[138:141], v190, v190 op_sel_hi:[0,0,0]
	v_mfma_scale_f32_16x16x128_f8f6f4 v[130:133], v[18:25], v[206:213], v[130:133], v190, v190 op_sel_hi:[0,0,0]
	v_mfma_scale_f32_16x16x128_f8f6f4 v[122:125], v[26:33], v[206:213], v[122:125], v190, v190 op_sel_hi:[0,0,0]
	v_mfma_scale_f32_16x16x128_f8f6f4 v[114:117], v[18:25], v[214:221], v[114:117], v190, v190 op_sel_hi:[0,0,0]
	v_mfma_scale_f32_16x16x128_f8f6f4 v[106:109], v[26:33], v[214:221], v[106:109], v190, v190 op_sel_hi:[0,0,0]
	v_mfma_scale_f32_16x16x128_f8f6f4 v[102:105], v[18:25], v[222:229], v[102:105], v190, v190 op_sel_hi:[0,0,0]
	v_mfma_scale_f32_16x16x128_f8f6f4 v[98:101], v[26:33], v[222:229], v[98:101], v190, v190 op_sel_hi:[0,0,0]
	s_setprio 0
	s_barrier
	s_add_i32 s38, s40, s42
	v_lshl_add_u64 v[182:183], v[182:183], 0, s[10:11]
	s_mov_b32 m0, s38
	ds_read_b128 v[198:201], v196 offset:49152
	ds_read_b128 v[202:205], v196 offset:50176
	ds_read_b128 v[206:209], v196 offset:51200
	ds_read_b128 v[210:213], v196 offset:52224
	ds_read_b128 v[214:217], v196 offset:53248
	ds_read_b128 v[218:221], v196 offset:54272
	ds_read_b128 v[222:225], v196 offset:55296
	ds_read_b128 v[226:229], v196 offset:56320
	global_load_lds_dwordx4 v[182:183], off
	s_add_i32 m0, s38, 0x2000
	s_add_u32 s36, s36, 0x40080
	v_lshl_add_u64 v[182:183], v[184:185], 0, s[10:11]
	s_addc_u32 s37, s37, 0
	s_add_i32 s38, s41, s42
	global_load_lds_dwordx4 v[182:183], off
	v_lshl_add_u64 v[182:183], s[36:37], 0, v[162:163]
	s_mov_b32 m0, s38
	s_nop 0
	global_load_lds_dwordx4 v[182:183], off
	v_lshl_add_u64 v[182:183], s[36:37], 0, v[164:165]
	s_add_i32 m0, s38, 0x2000
	s_nop 0
	global_load_lds_dwordx4 v[182:183], off
	v_lshl_add_u64 v[182:183], v[186:187], 0, s[10:11]
	s_mov_b32 m0, s47
	s_nop 0
	global_load_lds_dwordx4 v[182:183], off
	v_lshl_add_u64 v[182:183], v[188:189], 0, s[10:11]
	s_mov_b32 m0, s49
	s_nop 0
	global_load_lds_dwordx4 v[182:183], off
	s_waitcnt vmcnt(8) lgkmcnt(0)
	s_barrier
	s_setprio 1
	v_mfma_scale_f32_16x16x128_f8f6f4 v[94:97], v[2:9], v[198:205], v[94:97], v190, v190 op_sel_hi:[0,0,0]
	v_mfma_scale_f32_16x16x128_f8f6f4 v[90:93], v[10:17], v[198:205], v[90:93], v190, v190 op_sel_hi:[0,0,0]
	v_mfma_scale_f32_16x16x128_f8f6f4 v[86:89], v[2:9], v[206:213], v[86:89], v190, v190 op_sel_hi:[0,0,0]
	v_mfma_scale_f32_16x16x128_f8f6f4 v[78:81], v[10:17], v[206:213], v[78:81], v190, v190 op_sel_hi:[0,0,0]
	v_mfma_scale_f32_16x16x128_f8f6f4 v[62:65], v[2:9], v[214:221], v[62:65], v190, v190 op_sel_hi:[0,0,0]
	v_mfma_scale_f32_16x16x128_f8f6f4 v[54:57], v[10:17], v[214:221], v[54:57], v190, v190 op_sel_hi:[0,0,0]
	v_mfma_scale_f32_16x16x128_f8f6f4 v[46:49], v[2:9], v[222:229], v[46:49], v190, v190 op_sel_hi:[0,0,0]
	v_mfma_scale_f32_16x16x128_f8f6f4 v[38:41], v[10:17], v[222:229], v[38:41], v190, v190 op_sel_hi:[0,0,0]
	v_mfma_scale_f32_16x16x128_f8f6f4 v[82:85], v[18:25], v[198:205], v[82:85], v190, v190 op_sel_hi:[0,0,0]
	v_mfma_scale_f32_16x16x128_f8f6f4 v[74:77], v[26:33], v[198:205], v[74:77], v190, v190 op_sel_hi:[0,0,0]
	v_mfma_scale_f32_16x16x128_f8f6f4 v[58:61], v[18:25], v[206:213], v[58:61], v190, v190 op_sel_hi:[0,0,0]
	v_mfma_scale_f32_16x16x128_f8f6f4 v[50:53], v[26:33], v[206:213], v[50:53], v190, v190 op_sel_hi:[0,0,0]
	v_mfma_scale_f32_16x16x128_f8f6f4 v[42:45], v[18:25], v[214:221], v[42:45], v190, v190 op_sel_hi:[0,0,0]
	v_mfma_scale_f32_16x16x128_f8f6f4 v[34:37], v[26:33], v[214:221], v[34:37], v190, v190 op_sel_hi:[0,0,0]
	v_mfma_scale_f32_16x16x128_f8f6f4 v[70:73], v[18:25], v[222:229], v[70:73], v190, v190 op_sel_hi:[0,0,0]
	v_mfma_scale_f32_16x16x128_f8f6f4 v[66:69], v[26:33], v[222:229], v[66:69], v190, v190 op_sel_hi:[0,0,0]
	s_setprio 0
	s_barrier
	s_add_i32 s67, s67, 2
	s_cmp_gt_u32 s67, 13
	s_mov_b64 s[38:39], s[34:35]
	s_cbranch_scc0 .LBB0_1018
	s_and_b64 vcc, exec, s[12:13]
	s_cbranch_vccz .LBB0_1021
	s_barrier

; #define PG8_STAGE(bufoff, gbase, voff) do { _Pragma("unroll") for (int _i = 0; _i < 2; ++_i) \
;         __builtin_amdgcn_global_load_lds((const unsigned*)((const char*)(gbase) + (voff)[_i]), (LAS unsigned*)(lds + (bufoff) + ldsw + _i * 8192), 16, 0, 0); } while (0)
; #define PG8_LDA(dst, b, h) do { _Pragma("unroll") for (int m = 0; m < 4; ++m) dst[m] = PG8_LD32(lds + PG8_SA(b, h) + aoff + m * 2048); } while (0)
; #define PG8_LDB(dst, b, h) do { _Pragma("unroll") for (int n = 0; n < 2; ++n) dst[n] = PG8_LD32(lds + PG8_SB(b, h) + boff + n * 2048); } while (0)
; #define PG8_WAIT_V(n) asm volatile("s_waitcnt vmcnt(" #n ")" ::: "memory")
; #define PG8_WAIT_L(n) asm volatile("s_waitcnt lgkmcnt(" #n ")" ::: "memory")
; #define PG8_BAR __builtin_amdgcn_s_barrier()
; #define PG8_SCHED __builtin_amdgcn_sched_barrier(0)
; #define PG8_STA(bufoff, nextflag, h, koff) do { if constexpr (Sched::GATHER) { unsigned _o[2]; _o[0] = (nextflag) ? nxtA[h][0] : curA[h][0]; _o[1] = (nextflag) ? nxtA[h][1] : curA[h][1]; PG8_STAGE(bufoff, Ab + (koff), _o); } \
;         else { PG8_STAGE(bufoff, ((nextflag) ? nA : cA) + (size_t)(h) * hstep + (koff), voffA); } } while (0)
; template <class Epi, class Sched, bool ALIGN_EPI, int DT>
; __device__ __forceinline__ void gemm_phase(LAS unsigned char* lds, const int KB, const Sched& S, const Epi& E) {
;     ...
;             PG8_LDB(B0, 0, 0); PG8_LDB(B1, 0, 1); PG8_SCHED; PG8_LDA(At, 0, 0); PG8_STA(PG8_SA(1, 1), false, 1, k1);
;             PG8_WAIT_V(8); PG8_WAIT_L(0); PG8_BAR; PG8_MMA(0, 0, At, B0); PG8_MMA(0, 1, At, B1); PG8_BAR; PG8_SCHED;
;             PG8_LDA(At, 0, 1); PG8_STAGE(PG8_SB(0, 0), b2, voffB); PG8_STAGE(PG8_SB(0, 1), b2 + hstep, voffB); PG8_STA(PG8_SA(0, 0), last, 0, k2);
;             PG8_WAIT_V(8); PG8_WAIT_L(0); PG8_BAR; PG8_MMA(1, 0, At, B0); PG8_MMA(1, 1, At, B1); PG8_BAR; PG8_SCHED;
.LBB0_1154:
	ds_read_b128 v[70:73], v167
	ds_read_b128 v[156:159], v167 offset:1024
	ds_read_b128 v[160:163], v167 offset:2048
	ds_read_b128 v[172:175], v167 offset:3072
	ds_read_b128 v[176:179], v168
	ds_read_b128 v[180:183], v168 offset:1024
	ds_read_b128 v[184:187], v168 offset:2048
	ds_read_b128 v[188:191], v168 offset:3072
	s_add_u32 s30, s28, 0x100
	s_addc_u32 s31, s29, 0
	s_add_u32 s63, s56, s28
	s_addc_u32 s66, s57, s29
	s_cmp_eq_u32 s62, 12
	s_cselect_b64 s[36:37], -1, 0
	s_and_b64 s[34:35], s[36:37], exec
	s_cselect_b32 s67, 0, s30
	s_cselect_b32 s35, s17, s66
	s_cselect_b32 s34, s19, s63
	v_lshl_add_u64 v[192:193], v[66:67], 0, s[28:29]
	s_add_i32 m0, s25, 0xc000
	ds_read_b128 v[196:199], v169
	ds_read_b128 v[200:203], v169 offset:1024
	ds_read_b128 v[204:207], v169 offset:2048
	ds_read_b128 v[208:211], v169 offset:3072
	ds_read_b128 v[212:215], v169 offset:4096
	ds_read_b128 v[216:219], v169 offset:5120
	ds_read_b128 v[220:223], v169 offset:6144
	ds_read_b128 v[224:227], v169 offset:7168
	global_load_lds_dwordx4 v[192:193], off
	v_lshl_add_u64 v[192:193], v[68:69], 0, s[28:29]
	s_add_i32 m0, s25, 0xe000
	s_nop 0
	global_load_lds_dwordx4 v[192:193], off
	s_waitcnt vmcnt(8) lgkmcnt(0)
	s_barrier
	s_setprio 1
	v_mfma_i32_16x16x64_i8 v[134:137], v[70:73], v[196:199], v[134:137]
	v_mfma_i32_16x16x64_i8 v[126:129], v[160:163], v[196:199], v[126:129]
	v_mfma_i32_16x16x64_i8 v[118:121], v[70:73], v[204:207], v[118:121]
	v_mfma_i32_16x16x64_i8 v[110:113], v[160:163], v[204:207], v[110:113]
	v_mfma_i32_16x16x64_i8 v[102:105], v[70:73], v[212:215], v[102:105]
	v_mfma_i32_16x16x64_i8 v[94:97], v[160:163], v[212:215], v[94:97]
	v_mfma_i32_16x16x64_i8 v[86:89], v[70:73], v[220:223], v[86:89]
	v_mfma_i32_16x16x64_i8 v[78:81], v[160:163], v[220:223], v[78:81]
	v_mfma_i32_16x16x64_i8 v[134:137], v[156:159], v[200:203], v[134:137]
	v_mfma_i32_16x16x64_i8 v[126:129], v[172:175], v[200:203], v[126:129]
	v_mfma_i32_16x16x64_i8 v[118:121], v[156:159], v[208:211], v[118:121]
	v_mfma_i32_16x16x64_i8 v[110:113], v[172:175], v[208:211], v[110:113]
	v_mfma_i32_16x16x64_i8 v[102:105], v[156:159], v[216:219], v[102:105]
	v_mfma_i32_16x16x64_i8 v[94:97], v[172:175], v[216:219], v[94:97]
	v_mfma_i32_16x16x64_i8 v[86:89], v[156:159], v[224:227], v[86:89]
	v_mfma_i32_16x16x64_i8 v[78:81], v[172:175], v[224:227], v[78:81]
	v_mfma_i32_16x16x64_i8 v[130:133], v[176:179], v[196:199], v[130:133]
	v_mfma_i32_16x16x64_i8 v[122:125], v[184:187], v[196:199], v[122:125]
	v_mfma_i32_16x16x64_i8 v[114:117], v[176:179], v[204:207], v[114:117]
	v_mfma_i32_16x16x64_i8 v[106:109], v[184:187], v[204:207], v[106:109]
	v_mfma_i32_16x16x64_i8 v[98:101], v[176:179], v[212:215], v[98:101]
	v_mfma_i32_16x16x64_i8 v[90:93], v[184:187], v[212:215], v[90:93]
	v_mfma_i32_16x16x64_i8 v[82:85], v[176:179], v[220:223], v[82:85]
	v_mfma_i32_16x16x64_i8 v[74:77], v[184:187], v[220:223], v[74:77]
	v_mfma_i32_16x16x64_i8 v[130:133], v[180:183], v[200:203], v[130:133]
	v_mfma_i32_16x16x64_i8 v[122:125], v[188:191], v[200:203], v[122:125]
	v_mfma_i32_16x16x64_i8 v[114:117], v[180:183], v[208:211], v[114:117]
	v_mfma_i32_16x16x64_i8 v[106:109], v[188:191], v[208:211], v[106:109]
	v_mfma_i32_16x16x64_i8 v[98:101], v[180:183], v[216:219], v[98:101]
	v_mfma_i32_16x16x64_i8 v[90:93], v[188:191], v[216:219], v[90:93]
	v_mfma_i32_16x16x64_i8 v[82:85], v[180:183], v[224:227], v[82:85]
	v_mfma_i32_16x16x64_i8 v[74:77], v[188:191], v[224:227], v[74:77]
	s_setprio 0
	s_barrier
	s_add_i32 s28, s49, s38
	v_lshl_add_u64 v[192:193], s[34:35], 0, v[140:141]
	s_mov_b32 m0, s28
	ds_read_b128 v[196:199], v169 offset:16384
	ds_read_b128 v[200:203], v169 offset:17408
	ds_read_b128 v[204:207], v169 offset:18432
	ds_read_b128 v[208:211], v169 offset:19456
	ds_read_b128 v[212:215], v169 offset:20480
	ds_read_b128 v[216:219], v169 offset:21504
	ds_read_b128 v[220:223], v169 offset:22528
	ds_read_b128 v[224:227], v169 offset:23552
	global_load_lds_dwordx4 v[192:193], off
	s_add_i32 m0, s28, 0x2000
	s_add_u32 s28, s34, 0x40000
	v_lshl_add_u64 v[228:229], s[34:35], 0, v[138:139]
	s_addc_u32 s29, s35, 0
	s_add_i32 s63, s52, s38
	global_load_lds_dwordx4 v[228:229], off
	v_lshl_add_u64 v[230:231], s[28:29], 0, v[140:141]
	s_mov_b32 m0, s63
	s_nop 0
	global_load_lds_dwordx4 v[230:231], off
	v_lshl_add_u64 v[230:231], s[28:29], 0, v[138:139]
	s_add_i32 m0, s63, 0x2000
	s_and_b64 s[28:29], s[6:7], s[36:37]
	s_and_b64 s[28:29], s[28:29], exec
	s_cselect_b32 s28, s20, s26
	s_cselect_b32 s29, s21, s27
	s_add_u32 s28, s28, s67
	s_addc_u32 s29, s29, 0
	global_load_lds_dwordx4 v[230:231], off
	v_lshl_add_u64 v[230:231], s[28:29], 0, v[142:143]
	s_mov_b32 m0, s25
	v_lshl_add_u64 v[232:233], s[28:29], 0, v[144:145]
	global_load_lds_dwordx4 v[230:231], off
	s_mov_b32 m0, s41
	s_nop 0
	global_load_lds_dwordx4 v[232:233], off
	s_waitcnt vmcnt(8) lgkmcnt(0)
	s_barrier
; #define PG8_LDA(dst, b, h) do { _Pragma("unroll") for (int m = 0; m < 4; ++m) dst[m] = PG8_LD32(lds + PG8_SA(b, h) + aoff + m * 2048); } while (0)
; #define PG8_LDB(dst, b, h) do { _Pragma("unroll") for (int n = 0; n < 2; ++n) dst[n] = PG8_LD32(lds + PG8_SB(b, h) + boff + n * 2048); } while (0)
; #define PG8_WAIT_V(n) asm volatile("s_waitcnt vmcnt(" #n ")" ::: "memory")
; #define PG8_WAIT_L(n) asm volatile("s_waitcnt lgkmcnt(" #n ")" ::: "memory")
; #define PG8_BAR __builtin_amdgcn_s_barrier()
; #define PG8_SCHED __builtin_amdgcn_sched_barrier(0)
; #define PG8_STA(bufoff, nextflag, h, koff) do { if constexpr (Sched::GATHER) { unsigned _o[2]; _o[0] = (nextflag) ? nxtA[h][0] : curA[h][0]; _o[1] = (nextflag) ? nxtA[h][1] : curA[h][1]; PG8_STAGE(bufoff, Ab + (koff), _o); } \
;         else { PG8_STAGE(bufoff, ((nextflag) ? nA : cA) + (size_t)(h) * hstep + (koff), voffA); } } while (0)
; template <class Epi, class Sched, bool ALIGN_EPI, int DT>
; __device__ __forceinline__ void gemm_phase(LAS unsigned char* lds, const int KB, const Sched& S, const Epi& E) {
;     ...
;             PG8_WAIT_V(8); PG8_WAIT_L(0); PG8_BAR; PG8_MMA(1, 0, At, B0); PG8_MMA(1, 1, At, B1); PG8_BAR; PG8_SCHED;
;             PG8_LDB(B0, 1, 0); PG8_LDB(B1, 1, 1); PG8_SCHED; PG8_LDA(At, 1, 0); PG8_STA(PG8_SA(0, 1), last, 1, k2);
;             PG8_WAIT_V(8); PG8_WAIT_L(0); PG8_BAR; PG8_MMA(0, 0, At, B0); PG8_MMA(0, 1, At, B1); PG8_BAR; PG8_SCHED;
	s_setprio 1
	v_mfma_i32_16x16x64_i8 v[62:65], v[70:73], v[196:199], v[62:65]
	v_mfma_i32_16x16x64_i8 v[54:57], v[160:163], v[196:199], v[54:57]
	v_mfma_i32_16x16x64_i8 v[46:49], v[70:73], v[204:207], v[46:49]
	v_mfma_i32_16x16x64_i8 v[38:41], v[160:163], v[204:207], v[38:41]
	v_mfma_i32_16x16x64_i8 v[30:33], v[70:73], v[212:215], v[30:33]
	v_mfma_i32_16x16x64_i8 v[22:25], v[160:163], v[212:215], v[22:25]
	v_mfma_i32_16x16x64_i8 v[6:9], v[70:73], v[220:223], v[6:9]
	v_mfma_i32_16x16x64_i8 v[2:5], v[160:163], v[220:223], v[2:5]
	v_mfma_i32_16x16x64_i8 v[62:65], v[156:159], v[200:203], v[62:65]
	v_mfma_i32_16x16x64_i8 v[54:57], v[172:175], v[200:203], v[54:57]
	v_mfma_i32_16x16x64_i8 v[46:49], v[156:159], v[208:211], v[46:49]
	v_mfma_i32_16x16x64_i8 v[38:41], v[172:175], v[208:211], v[38:41]
	v_mfma_i32_16x16x64_i8 v[30:33], v[156:159], v[216:219], v[30:33]
	v_mfma_i32_16x16x64_i8 v[22:25], v[172:175], v[216:219], v[22:25]
	v_mfma_i32_16x16x64_i8 v[6:9], v[156:159], v[224:227], v[6:9]
	v_mfma_i32_16x16x64_i8 v[2:5], v[172:175], v[224:227], v[2:5]
	v_mfma_i32_16x16x64_i8 v[58:61], v[176:179], v[196:199], v[58:61]
	v_mfma_i32_16x16x64_i8 v[50:53], v[184:187], v[196:199], v[50:53]
	v_mfma_i32_16x16x64_i8 v[42:45], v[176:179], v[204:207], v[42:45]
	v_mfma_i32_16x16x64_i8 v[34:37], v[184:187], v[204:207], v[34:37]
	v_mfma_i32_16x16x64_i8 v[26:29], v[176:179], v[212:215], v[26:29]
	v_mfma_i32_16x16x64_i8 v[18:21], v[184:187], v[212:215], v[18:21]
	v_mfma_i32_16x16x64_i8 v[14:17], v[176:179], v[220:223], v[14:17]
	v_mfma_i32_16x16x64_i8 v[10:13], v[184:187], v[220:223], v[10:13]
	v_mfma_i32_16x16x64_i8 v[58:61], v[180:183], v[200:203], v[58:61]
	v_mfma_i32_16x16x64_i8 v[50:53], v[188:191], v[200:203], v[50:53]
	v_mfma_i32_16x16x64_i8 v[42:45], v[180:183], v[208:211], v[42:45]
	v_mfma_i32_16x16x64_i8 v[34:37], v[188:191], v[208:211], v[34:37]
	v_mfma_i32_16x16x64_i8 v[26:29], v[180:183], v[216:219], v[26:29]
	v_mfma_i32_16x16x64_i8 v[18:21], v[188:191], v[216:219], v[18:21]
	v_mfma_i32_16x16x64_i8 v[14:17], v[180:183], v[224:227], v[14:17]
	v_mfma_i32_16x16x64_i8 v[10:13], v[188:191], v[224:227], v[10:13]
	s_setprio 0
	s_barrier
	s_add_i32 s36, 0, 0x18000
	v_add_u32_e32 v1, s36, v165
	s_add_i32 s37, 0, 0x1c000
	ds_read_b128 v[70:73], v1
	ds_read_b128 v[156:159], v1 offset:1024
	ds_read_b128 v[160:163], v1 offset:2048
	ds_read_b128 v[172:175], v1 offset:3072
	v_add_u32_e32 v1, s37, v165
	ds_read_b128 v[176:179], v1
	ds_read_b128 v[180:183], v1 offset:1024
	ds_read_b128 v[184:187], v1 offset:2048
	ds_read_b128 v[188:191], v1 offset:3072
	s_add_u32 s28, s28, 0x40000
	s_addc_u32 s29, s29, 0
	s_mov_b32 m0, s42
	v_lshl_add_u64 v[234:235], s[28:29], 0, v[142:143]
	ds_read_b128 v[196:199], v169 offset:32768
	ds_read_b128 v[200:203], v169 offset:33792
	ds_read_b128 v[204:207], v169 offset:34816
	ds_read_b128 v[208:211], v169 offset:35840
	ds_read_b128 v[212:215], v169 offset:36864
	ds_read_b128 v[216:219], v169 offset:37888
	ds_read_b128 v[220:223], v169 offset:38912
	ds_read_b128 v[224:227], v169 offset:39936
	global_load_lds_dwordx4 v[234:235], off
	v_lshl_add_u64 v[234:235], s[28:29], 0, v[144:145]
	s_mov_b32 m0, s43
	s_nop 0
	global_load_lds_dwordx4 v[234:235], off
	s_waitcnt vmcnt(8) lgkmcnt(0)
	s_barrier
	s_setprio 1
	v_mfma_i32_16x16x64_i8 v[134:137], v[70:73], v[196:199], v[134:137]
	v_mfma_i32_16x16x64_i8 v[126:129], v[160:163], v[196:199], v[126:129]
	v_mfma_i32_16x16x64_i8 v[118:121], v[70:73], v[204:207], v[118:121]
	v_mfma_i32_16x16x64_i8 v[110:113], v[160:163], v[204:207], v[110:113]
	v_mfma_i32_16x16x64_i8 v[102:105], v[70:73], v[212:215], v[102:105]
	v_mfma_i32_16x16x64_i8 v[94:97], v[160:163], v[212:215], v[94:97]
	v_mfma_i32_16x16x64_i8 v[86:89], v[70:73], v[220:223], v[86:89]
	v_mfma_i32_16x16x64_i8 v[78:81], v[160:163], v[220:223], v[78:81]
	v_mfma_i32_16x16x64_i8 v[134:137], v[156:159], v[200:203], v[134:137]
	v_mfma_i32_16x16x64_i8 v[126:129], v[172:175], v[200:203], v[126:129]
	v_mfma_i32_16x16x64_i8 v[118:121], v[156:159], v[208:211], v[118:121]
	v_mfma_i32_16x16x64_i8 v[110:113], v[172:175], v[208:211], v[110:113]
	v_mfma_i32_16x16x64_i8 v[102:105], v[156:159], v[216:219], v[102:105]
	v_mfma_i32_16x16x64_i8 v[94:97], v[172:175], v[216:219], v[94:97]
	v_mfma_i32_16x16x64_i8 v[86:89], v[156:159], v[224:227], v[86:89]
	v_mfma_i32_16x16x64_i8 v[78:81], v[172:175], v[224:227], v[78:81]
	v_mfma_i32_16x16x64_i8 v[130:133], v[176:179], v[196:199], v[130:133]
	v_mfma_i32_16x16x64_i8 v[122:125], v[184:187], v[196:199], v[122:125]
	v_mfma_i32_16x16x64_i8 v[114:117], v[176:179], v[204:207], v[114:117]
	v_mfma_i32_16x16x64_i8 v[106:109], v[184:187], v[204:207], v[106:109]
	v_mfma_i32_16x16x64_i8 v[98:101], v[176:179], v[212:215], v[98:101]
	v_mfma_i32_16x16x64_i8 v[90:93], v[184:187], v[212:215], v[90:93]
	v_mfma_i32_16x16x64_i8 v[82:85], v[176:179], v[220:223], v[82:85]
	v_mfma_i32_16x16x64_i8 v[74:77], v[184:187], v[220:223], v[74:77]
	v_mfma_i32_16x16x64_i8 v[130:133], v[180:183], v[200:203], v[130:133]
	v_mfma_i32_16x16x64_i8 v[122:125], v[188:191], v[200:203], v[122:125]
	v_mfma_i32_16x16x64_i8 v[114:117], v[180:183], v[208:211], v[114:117]
	v_mfma_i32_16x16x64_i8 v[106:109], v[188:191], v[208:211], v[106:109]
	v_mfma_i32_16x16x64_i8 v[98:101], v[180:183], v[216:219], v[98:101]
	v_mfma_i32_16x16x64_i8 v[90:93], v[188:191], v[216:219], v[90:93]
	v_mfma_i32_16x16x64_i8 v[82:85], v[180:183], v[224:227], v[82:85]
	v_mfma_i32_16x16x64_i8 v[74:77], v[188:191], v[224:227], v[74:77]
	s_setprio 0
	s_barrier
; #define PG8_STAGE(bufoff, gbase, voff) do { _Pragma("unroll") for (int _i = 0; _i < 2; ++_i) \
;         __builtin_amdgcn_global_load_lds((const unsigned*)((const char*)(gbase) + (voff)[_i]), (LAS unsigned*)(lds + (bufoff) + ldsw + _i * 8192), 16, 0, 0); } while (0)
; #define PG8_LDA(dst, b, h) do { _Pragma("unroll") for (int m = 0; m < 4; ++m) dst[m] = PG8_LD32(lds + PG8_SA(b, h) + aoff + m * 2048); } while (0)
; #define PG8_WAIT_V(n) asm volatile("s_waitcnt vmcnt(" #n ")" ::: "memory")
; #define PG8_WAIT_L(n) asm volatile("s_waitcnt lgkmcnt(" #n ")" ::: "memory")
; #define PG8_BAR __builtin_amdgcn_s_barrier()
; #define PG8_SCHED __builtin_amdgcn_sched_barrier(0)
; #define PG8_STA(bufoff, nextflag, h, koff) do { if constexpr (Sched::GATHER) { unsigned _o[2]; _o[0] = (nextflag) ? nxtA[h][0] : curA[h][0]; _o[1] = (nextflag) ? nxtA[h][1] : curA[h][1]; PG8_STAGE(bufoff, Ab + (koff), _o); } \
;         else { PG8_STAGE(bufoff, ((nextflag) ? nA : cA) + (size_t)(h) * hstep + (koff), voffA); } } while (0)
; template <class Epi, class Sched, bool ALIGN_EPI, int DT>
; __device__ __forceinline__ void gemm_phase(LAS unsigned char* lds, const int KB, const Sched& S, const Epi& E) {
;     ...
;             PG8_LDA(At, 1, 1); PG8_STAGE(PG8_SB(1, 0), b3, voffB); PG8_STAGE(PG8_SB(1, 1), b3 + hstep, voffB); PG8_STA(PG8_SA(1, 0), last, 0, k3);
;             PG8_WAIT_V(8); PG8_WAIT_L(0); PG8_BAR; PG8_MMA(1, 0, At, B0); PG8_MMA(1, 1, At, B1); PG8_BAR; PG8_SCHED;
;         }
;         if constexpr (ALIGN_EPI) { if (wr == 0) PG8_BAR; }
	s_add_i32 s28, s36, s38
	v_lshl_add_u64 v[192:193], v[192:193], 0, s[12:13]
	s_mov_b32 m0, s28
	ds_read_b128 v[196:199], v169 offset:49152
	ds_read_b128 v[200:203], v169 offset:50176
	ds_read_b128 v[204:207], v169 offset:51200
	ds_read_b128 v[208:211], v169 offset:52224
	ds_read_b128 v[212:215], v169 offset:53248
	ds_read_b128 v[216:219], v169 offset:54272
	ds_read_b128 v[220:223], v169 offset:55296
	ds_read_b128 v[224:227], v169 offset:56320
	global_load_lds_dwordx4 v[192:193], off
	s_add_i32 m0, s28, 0x2000
	s_add_u32 s28, s34, 0x40080
	v_lshl_add_u64 v[192:193], v[228:229], 0, s[12:13]
	s_addc_u32 s29, s35, 0
	s_add_i32 s34, s37, s38
	global_load_lds_dwordx4 v[192:193], off
	v_lshl_add_u64 v[192:193], s[28:29], 0, v[140:141]
	s_mov_b32 m0, s34
	s_nop 0
	global_load_lds_dwordx4 v[192:193], off
	v_lshl_add_u64 v[192:193], s[28:29], 0, v[138:139]
	s_add_i32 m0, s34, 0x2000
	s_nop 0
	global_load_lds_dwordx4 v[192:193], off
	v_lshl_add_u64 v[192:193], v[230:231], 0, s[12:13]
	s_mov_b32 m0, s45
	s_nop 0
	global_load_lds_dwordx4 v[192:193], off
	v_lshl_add_u64 v[192:193], v[232:233], 0, s[12:13]
	s_mov_b32 m0, s46
	s_nop 0
	global_load_lds_dwordx4 v[192:193], off
	s_waitcnt vmcnt(8) lgkmcnt(0)
	s_barrier
	s_setprio 1
	v_mfma_i32_16x16x64_i8 v[62:65], v[70:73], v[196:199], v[62:65]
	v_mfma_i32_16x16x64_i8 v[54:57], v[160:163], v[196:199], v[54:57]
	v_mfma_i32_16x16x64_i8 v[46:49], v[70:73], v[204:207], v[46:49]
	v_mfma_i32_16x16x64_i8 v[38:41], v[160:163], v[204:207], v[38:41]
	v_mfma_i32_16x16x64_i8 v[30:33], v[70:73], v[212:215], v[30:33]
	v_mfma_i32_16x16x64_i8 v[22:25], v[160:163], v[212:215], v[22:25]
	v_mfma_i32_16x16x64_i8 v[6:9], v[70:73], v[220:223], v[6:9]
	v_mfma_i32_16x16x64_i8 v[2:5], v[160:163], v[220:223], v[2:5]
	v_mfma_i32_16x16x64_i8 v[62:65], v[156:159], v[200:203], v[62:65]
	v_mfma_i32_16x16x64_i8 v[54:57], v[172:175], v[200:203], v[54:57]
	v_mfma_i32_16x16x64_i8 v[46:49], v[156:159], v[208:211], v[46:49]
	v_mfma_i32_16x16x64_i8 v[38:41], v[172:175], v[208:211], v[38:41]
	v_mfma_i32_16x16x64_i8 v[30:33], v[156:159], v[216:219], v[30:33]
	v_mfma_i32_16x16x64_i8 v[22:25], v[172:175], v[216:219], v[22:25]
	v_mfma_i32_16x16x64_i8 v[6:9], v[156:159], v[224:227], v[6:9]
	v_mfma_i32_16x16x64_i8 v[2:5], v[172:175], v[224:227], v[2:5]
	v_mfma_i32_16x16x64_i8 v[58:61], v[176:179], v[196:199], v[58:61]
	v_mfma_i32_16x16x64_i8 v[50:53], v[184:187], v[196:199], v[50:53]
	v_mfma_i32_16x16x64_i8 v[42:45], v[176:179], v[204:207], v[42:45]
	v_mfma_i32_16x16x64_i8 v[34:37], v[184:187], v[204:207], v[34:37]
	v_mfma_i32_16x16x64_i8 v[26:29], v[176:179], v[212:215], v[26:29]
	v_mfma_i32_16x16x64_i8 v[18:21], v[184:187], v[212:215], v[18:21]
	v_mfma_i32_16x16x64_i8 v[14:17], v[176:179], v[220:223], v[14:17]
	v_mfma_i32_16x16x64_i8 v[10:13], v[184:187], v[220:223], v[10:13]
	v_mfma_i32_16x16x64_i8 v[58:61], v[180:183], v[200:203], v[58:61]
	v_mfma_i32_16x16x64_i8 v[50:53], v[188:191], v[200:203], v[50:53]
	v_mfma_i32_16x16x64_i8 v[42:45], v[180:183], v[208:211], v[42:45]
	v_mfma_i32_16x16x64_i8 v[34:37], v[188:191], v[208:211], v[34:37]
	v_mfma_i32_16x16x64_i8 v[26:29], v[180:183], v[216:219], v[26:29]
	v_mfma_i32_16x16x64_i8 v[18:21], v[188:191], v[216:219], v[18:21]
	v_mfma_i32_16x16x64_i8 v[14:17], v[180:183], v[224:227], v[14:17]
	v_mfma_i32_16x16x64_i8 v[10:13], v[188:191], v[224:227], v[10:13]
	s_setprio 0
	s_barrier
	s_add_i32 s62, s62, 2
	s_cmp_gt_u32 s62, 13
	s_mov_b64 s[28:29], s[30:31]
	s_cbranch_scc0 .LBB0_1154
	s_and_b64 vcc, exec, s[14:15]
	s_cbranch_vccz .LBB0_1157
	s_barrier

; #define PG8_STAGE(bufoff, gbase, voff) do { _Pragma("unroll") for (int _i = 0; _i < 2; ++_i) \
;         __builtin_amdgcn_global_load_lds((const unsigned*)((const char*)(gbase) + (voff)[_i]), (LAS unsigned*)(lds + (bufoff) + ldsw + _i * 8192), 16, 0, 0); } while (0)
; #define PG8_LDA(dst, b, h) do { _Pragma("unroll") for (int m = 0; m < 4; ++m) dst[m] = PG8_LD32(lds + PG8_SA(b, h) + aoff + m * 2048); } while (0)
; #define PG8_LDB(dst, b, h) do { _Pragma("unroll") for (int n = 0; n < 2; ++n) dst[n] = PG8_LD32(lds + PG8_SB(b, h) + boff + n * 2048); } while (0)
; #define PG8_WAIT_V(n) asm volatile("s_waitcnt vmcnt(" #n ")" ::: "memory")
; #define PG8_WAIT_L(n) asm volatile("s_waitcnt lgkmcnt(" #n ")" ::: "memory")
; #define PG8_BAR __builtin_amdgcn_s_barrier()
; #define PG8_SCHED __builtin_amdgcn_sched_barrier(0)
; #define PG8_STA(bufoff, nextflag, h, koff) do { if constexpr (Sched::GATHER) { unsigned _o[2]; _o[0] = (nextflag) ? nxtA[h][0] : curA[h][0]; _o[1] = (nextflag) ? nxtA[h][1] : curA[h][1]; PG8_STAGE(bufoff, Ab + (koff), _o); } \
;         else { PG8_STAGE(bufoff, ((nextflag) ? nA : cA) + (size_t)(h) * hstep + (koff), voffA); } } while (0)
; template <class Epi, class Sched, bool ALIGN_EPI, int DT>
; __device__ __forceinline__ void gemm_phase(LAS unsigned char* lds, const int KB, const Sched& S, const Epi& E) {
;     ...
;         for (int t = 0; t < nt; t += 2) {
;             const bool last = (t == nt - 2);
;             const size_t k1 = (size_t)(t + 1) * kstep, k2 = last ? 0 : (size_t)(t + 2) * kstep, k3 = k2 + kstep;
;             const char* b2 = last ? nB : cB + (size_t)(t + 2) * kstep; const char* b3 = b2 + kstep;
;             PG8_LDB(B0, 0, 0); PG8_LDB(B1, 0, 1); PG8_SCHED; PG8_LDA(At, 0, 0); PG8_STA(PG8_SA(1, 1), false, 1, k1);
;             PG8_WAIT_V(8); PG8_WAIT_L(0); PG8_BAR; PG8_MMA(0, 0, At, B0); PG8_MMA(0, 1, At, B1); PG8_BAR; PG8_SCHED;
;             PG8_LDA(At, 0, 1); PG8_STAGE(PG8_SB(0, 0), b2, voffB); PG8_STAGE(PG8_SB(0, 1), b2 + hstep, voffB); PG8_STA(PG8_SA(0, 0), last, 0, k2);
;             PG8_WAIT_V(8); PG8_WAIT_L(0); PG8_BAR; PG8_MMA(1, 0, At, B0); PG8_MMA(1, 1, At, B1); PG8_BAR; PG8_SCHED;
.LBB0_1237:
	ds_read_b128 v[18:21], v193
	ds_read_b128 v[22:25], v193 offset:1024
	ds_read_b128 v[26:29], v193 offset:2048
	ds_read_b128 v[30:33], v193 offset:3072
	ds_read_b128 v[2:5], v195
	ds_read_b128 v[6:9], v195 offset:1024
	ds_read_b128 v[10:13], v195 offset:2048
	ds_read_b128 v[14:17], v195 offset:3072
	s_add_u32 s26, s30, 0x100
	s_addc_u32 s27, s31, 0
	s_add_u32 s28, s56, s30
	s_addc_u32 s29, s57, s31
	s_add_i32 s68, s43, s34
	s_add_i32 m0, s35, 0xc000
	s_add_i32 s69, s35, 0xe000
	s_add_i32 s63, s68, 0x2000
	s_cmp_eq_u32 s62, 40
	s_cselect_b32 s29, s23, s29
	s_cselect_b32 s28, s22, s28
	s_cselect_b32 s66, 0, s27
	s_cselect_b32 s67, 0, s26
	v_lshl_add_u64 v[222:223], v[178:179], 0, s[30:31]
	ds_read_b128 v[182:185], v196
	ds_read_b128 v[186:189], v196 offset:1024
	ds_read_b128 v[198:201], v196 offset:2048
	ds_read_b128 v[202:205], v196 offset:3072
	ds_read_b128 v[206:209], v196 offset:4096
	ds_read_b128 v[210:213], v196 offset:5120
	ds_read_b128 v[214:217], v196 offset:6144
	ds_read_b128 v[218:221], v196 offset:7168
	global_load_lds_dwordx4 v[222:223], off
	v_lshl_add_u64 v[222:223], v[180:181], 0, s[30:31]
	s_mov_b32 m0, s69
	s_nop 0
	global_load_lds_dwordx4 v[222:223], off
	s_waitcnt vmcnt(8) lgkmcnt(0)
	s_barrier
	s_setprio 1
	v_mfma_scale_f32_16x16x128_f8f6f4 v[158:161], v[18:25], v[182:189], v[158:161], v190, v190 op_sel_hi:[0,0,0]
	v_mfma_scale_f32_16x16x128_f8f6f4 v[154:157], v[26:33], v[182:189], v[154:157], v190, v190 op_sel_hi:[0,0,0]
	v_mfma_scale_f32_16x16x128_f8f6f4 v[150:153], v[18:25], v[198:205], v[150:153], v190, v190 op_sel_hi:[0,0,0]
	v_mfma_scale_f32_16x16x128_f8f6f4 v[142:145], v[26:33], v[198:205], v[142:145], v190, v190 op_sel_hi:[0,0,0]
	v_mfma_scale_f32_16x16x128_f8f6f4 v[134:137], v[18:25], v[206:213], v[134:137], v190, v190 op_sel_hi:[0,0,0]
	v_mfma_scale_f32_16x16x128_f8f6f4 v[126:129], v[26:33], v[206:213], v[126:129], v190, v190 op_sel_hi:[0,0,0]
	v_mfma_scale_f32_16x16x128_f8f6f4 v[118:121], v[18:25], v[214:221], v[118:121], v190, v190 op_sel_hi:[0,0,0]
	v_mfma_scale_f32_16x16x128_f8f6f4 v[110:113], v[26:33], v[214:221], v[110:113], v190, v190 op_sel_hi:[0,0,0]
	v_mfma_scale_f32_16x16x128_f8f6f4 v[146:149], v[2:9], v[182:189], v[146:149], v190, v190 op_sel_hi:[0,0,0]
	v_mfma_scale_f32_16x16x128_f8f6f4 v[138:141], v[10:17], v[182:189], v[138:141], v190, v190 op_sel_hi:[0,0,0]
	v_mfma_scale_f32_16x16x128_f8f6f4 v[130:133], v[2:9], v[198:205], v[130:133], v190, v190 op_sel_hi:[0,0,0]
	v_mfma_scale_f32_16x16x128_f8f6f4 v[122:125], v[10:17], v[198:205], v[122:125], v190, v190 op_sel_hi:[0,0,0]
	v_mfma_scale_f32_16x16x128_f8f6f4 v[114:117], v[2:9], v[206:213], v[114:117], v190, v190 op_sel_hi:[0,0,0]
	v_mfma_scale_f32_16x16x128_f8f6f4 v[106:109], v[10:17], v[206:213], v[106:109], v190, v190 op_sel_hi:[0,0,0]
	v_mfma_scale_f32_16x16x128_f8f6f4 v[102:105], v[2:9], v[214:221], v[102:105], v190, v190 op_sel_hi:[0,0,0]
	v_mfma_scale_f32_16x16x128_f8f6f4 v[98:101], v[10:17], v[214:221], v[98:101], v190, v190 op_sel_hi:[0,0,0]
	s_setprio 0
	s_barrier
	s_mov_b32 m0, s68
	v_lshl_add_u64 v[184:185], s[28:29], 0, v[162:163]
	ds_read_b128 v[198:201], v196 offset:16384
	ds_read_b128 v[202:205], v196 offset:17408
	ds_read_b128 v[206:209], v196 offset:18432
	ds_read_b128 v[210:213], v196 offset:19456
	ds_read_b128 v[214:217], v196 offset:20480
	ds_read_b128 v[218:221], v196 offset:21504
	ds_read_b128 v[222:225], v196 offset:22528
	ds_read_b128 v[226:229], v196 offset:23552
	global_load_lds_dwordx4 v[184:185], off
	s_mov_b32 m0, s63
	s_cselect_b32 s63, s9, s25
	s_cselect_b32 s68, s8, s24
	s_add_u32 s30, s28, 0xb0000
	v_lshl_add_u64 v[182:183], s[28:29], 0, v[164:165]
	s_addc_u32 s31, s29, 0
	s_add_i32 s69, s44, s34
	global_load_lds_dwordx4 v[182:183], off
	v_lshl_add_u64 v[186:187], s[30:31], 0, v[162:163]
	s_mov_b32 m0, s69
	s_nop 0
	global_load_lds_dwordx4 v[186:187], off
	s_add_i32 m0, s69, 0x2000
	v_lshl_add_u64 v[186:187], s[30:31], 0, v[164:165]
	s_add_u32 s30, s68, s67
	s_addc_u32 s31, s63, s66
	global_load_lds_dwordx4 v[186:187], off
	v_lshl_add_u64 v[186:187], s[30:31], 0, v[166:167]
	s_mov_b32 m0, s35
	v_lshl_add_u64 v[188:189], s[30:31], 0, v[168:169]
	global_load_lds_dwordx4 v[186:187], off
	s_mov_b32 m0, s36
	s_nop 0
	global_load_lds_dwordx4 v[188:189], off
	s_waitcnt vmcnt(8) lgkmcnt(0)
	s_barrier
	s_setprio 1
	v_mfma_scale_f32_16x16x128_f8f6f4 v[94:97], v[18:25], v[198:205], v[94:97], v190, v190 op_sel_hi:[0,0,0]
	v_mfma_scale_f32_16x16x128_f8f6f4 v[90:93], v[26:33], v[198:205], v[90:93], v190, v190 op_sel_hi:[0,0,0]
	v_mfma_scale_f32_16x16x128_f8f6f4 v[86:89], v[18:25], v[206:213], v[86:89], v190, v190 op_sel_hi:[0,0,0]
	v_mfma_scale_f32_16x16x128_f8f6f4 v[78:81], v[26:33], v[206:213], v[78:81], v190, v190 op_sel_hi:[0,0,0]
	v_mfma_scale_f32_16x16x128_f8f6f4 v[62:65], v[18:25], v[214:221], v[62:65], v190, v190 op_sel_hi:[0,0,0]
	v_mfma_scale_f32_16x16x128_f8f6f4 v[54:57], v[26:33], v[214:221], v[54:57], v190, v190 op_sel_hi:[0,0,0]
	v_mfma_scale_f32_16x16x128_f8f6f4 v[46:49], v[18:25], v[222:229], v[46:49], v190, v190 op_sel_hi:[0,0,0]
	v_mfma_scale_f32_16x16x128_f8f6f4 v[38:41], v[26:33], v[222:229], v[38:41], v190, v190 op_sel_hi:[0,0,0]
	v_mfma_scale_f32_16x16x128_f8f6f4 v[82:85], v[2:9], v[198:205], v[82:85], v190, v190 op_sel_hi:[0,0,0]
	v_mfma_scale_f32_16x16x128_f8f6f4 v[74:77], v[10:17], v[198:205], v[74:77], v190, v190 op_sel_hi:[0,0,0]
	v_mfma_scale_f32_16x16x128_f8f6f4 v[58:61], v[2:9], v[206:213], v[58:61], v190, v190 op_sel_hi:[0,0,0]
	v_mfma_scale_f32_16x16x128_f8f6f4 v[50:53], v[10:17], v[206:213], v[50:53], v190, v190 op_sel_hi:[0,0,0]
	v_mfma_scale_f32_16x16x128_f8f6f4 v[42:45], v[2:9], v[214:221], v[42:45], v190, v190 op_sel_hi:[0,0,0]
	v_mfma_scale_f32_16x16x128_f8f6f4 v[34:37], v[10:17], v[214:221], v[34:37], v190, v190 op_sel_hi:[0,0,0]
	v_mfma_scale_f32_16x16x128_f8f6f4 v[70:73], v[2:9], v[222:229], v[70:73], v190, v190 op_sel_hi:[0,0,0]
	v_mfma_scale_f32_16x16x128_f8f6f4 v[66:69], v[10:17], v[222:229], v[66:69], v190, v190 op_sel_hi:[0,0,0]
	s_setprio 0
	s_barrier
; #define PG8_STAGE(bufoff, gbase, voff) do { _Pragma("unroll") for (int _i = 0; _i < 2; ++_i) \
;         __builtin_amdgcn_global_load_lds((const unsigned*)((const char*)(gbase) + (voff)[_i]), (LAS unsigned*)(lds + (bufoff) + ldsw + _i * 8192), 16, 0, 0); } while (0)
; #define PG8_LDA(dst, b, h) do { _Pragma("unroll") for (int m = 0; m < 4; ++m) dst[m] = PG8_LD32(lds + PG8_SA(b, h) + aoff + m * 2048); } while (0)
; #define PG8_LDB(dst, b, h) do { _Pragma("unroll") for (int n = 0; n < 2; ++n) dst[n] = PG8_LD32(lds + PG8_SB(b, h) + boff + n * 2048); } while (0)
; #define PG8_WAIT_V(n) asm volatile("s_waitcnt vmcnt(" #n ")" ::: "memory")
; #define PG8_WAIT_L(n) asm volatile("s_waitcnt lgkmcnt(" #n ")" ::: "memory")
; #define PG8_BAR __builtin_amdgcn_s_barrier()
; #define PG8_SCHED __builtin_amdgcn_sched_barrier(0)
; #define PG8_STA(bufoff, nextflag, h, koff) do { if constexpr (Sched::GATHER) { unsigned _o[2]; _o[0] = (nextflag) ? nxtA[h][0] : curA[h][0]; _o[1] = (nextflag) ? nxtA[h][1] : curA[h][1]; PG8_STAGE(bufoff, Ab + (koff), _o); } \
;         else { PG8_STAGE(bufoff, ((nextflag) ? nA : cA) + (size_t)(h) * hstep + (koff), voffA); } } while (0)
; template <class Epi, class Sched, bool ALIGN_EPI, int DT>
; __device__ __forceinline__ void gemm_phase(LAS unsigned char* lds, const int KB, const Sched& S, const Epi& E) {
;     ...
;             PG8_LDB(B0, 1, 0); PG8_LDB(B1, 1, 1); PG8_SCHED; PG8_LDA(At, 1, 0); PG8_STA(PG8_SA(0, 1), last, 1, k2);
;             PG8_WAIT_V(8); PG8_WAIT_L(0); PG8_BAR; PG8_MMA(0, 0, At, B0); PG8_MMA(0, 1, At, B1); PG8_BAR; PG8_SCHED;
;             PG8_LDA(At, 1, 1); PG8_STAGE(PG8_SB(1, 0), b3, voffB); PG8_STAGE(PG8_SB(1, 1), b3 + hstep, voffB); PG8_STA(PG8_SA(1, 0), last, 0, k3);
;             PG8_WAIT_V(8); PG8_WAIT_L(0); PG8_BAR; PG8_MMA(1, 0, At, B0); PG8_MMA(1, 1, At, B1); PG8_BAR; PG8_SCHED;
;         }
;         if constexpr (ALIGN_EPI) { if (wr == 0) PG8_BAR; }
	s_add_i32 s63, 0, 0x18000
	s_add_i32 s66, 0, 0x1c000
	v_add_u32_e32 v14, s63, v191
	v_add_u32_e32 v30, s66, v191
	ds_read_b128 v[2:5], v14
	ds_read_b128 v[6:9], v14 offset:1024
	ds_read_b128 v[10:13], v14 offset:2048
	ds_read_b128 v[14:17], v14 offset:3072
	ds_read_b128 v[18:21], v30
	ds_read_b128 v[22:25], v30 offset:1024
	ds_read_b128 v[26:29], v30 offset:2048
	ds_read_b128 v[30:33], v30 offset:3072
	s_add_u32 s30, s30, 0xb0000
	s_addc_u32 s31, s31, 0
	s_mov_b32 m0, s37
	v_lshl_add_u64 v[230:231], s[30:31], 0, v[166:167]
	ds_read_b128 v[198:201], v196 offset:32768
	ds_read_b128 v[202:205], v196 offset:33792
	ds_read_b128 v[206:209], v196 offset:34816
	ds_read_b128 v[210:213], v196 offset:35840
	ds_read_b128 v[214:217], v196 offset:36864
	ds_read_b128 v[218:221], v196 offset:37888
	ds_read_b128 v[222:225], v196 offset:38912
	ds_read_b128 v[226:229], v196 offset:39936
	global_load_lds_dwordx4 v[230:231], off
	v_lshl_add_u64 v[230:231], s[30:31], 0, v[168:169]
	s_mov_b32 m0, s38
	s_nop 0
	global_load_lds_dwordx4 v[230:231], off
	s_waitcnt vmcnt(8) lgkmcnt(0)
	s_barrier
	s_setprio 1
	v_mfma_scale_f32_16x16x128_f8f6f4 v[158:161], v[2:9], v[198:205], v[158:161], v190, v190 op_sel_hi:[0,0,0]
	v_mfma_scale_f32_16x16x128_f8f6f4 v[154:157], v[10:17], v[198:205], v[154:157], v190, v190 op_sel_hi:[0,0,0]
	v_mfma_scale_f32_16x16x128_f8f6f4 v[150:153], v[2:9], v[206:213], v[150:153], v190, v190 op_sel_hi:[0,0,0]
	v_mfma_scale_f32_16x16x128_f8f6f4 v[142:145], v[10:17], v[206:213], v[142:145], v190, v190 op_sel_hi:[0,0,0]
	v_mfma_scale_f32_16x16x128_f8f6f4 v[134:137], v[2:9], v[214:221], v[134:137], v190, v190 op_sel_hi:[0,0,0]
	v_mfma_scale_f32_16x16x128_f8f6f4 v[126:129], v[10:17], v[214:221], v[126:129], v190, v190 op_sel_hi:[0,0,0]
	v_mfma_scale_f32_16x16x128_f8f6f4 v[118:121], v[2:9], v[222:229], v[118:121], v190, v190 op_sel_hi:[0,0,0]
	v_mfma_scale_f32_16x16x128_f8f6f4 v[110:113], v[10:17], v[222:229], v[110:113], v190, v190 op_sel_hi:[0,0,0]
	v_mfma_scale_f32_16x16x128_f8f6f4 v[146:149], v[18:25], v[198:205], v[146:149], v190, v190 op_sel_hi:[0,0,0]
	v_mfma_scale_f32_16x16x128_f8f6f4 v[138:141], v[26:33], v[198:205], v[138:141], v190, v190 op_sel_hi:[0,0,0]
	v_mfma_scale_f32_16x16x128_f8f6f4 v[130:133], v[18:25], v[206:213], v[130:133], v190, v190 op_sel_hi:[0,0,0]
	v_mfma_scale_f32_16x16x128_f8f6f4 v[122:125], v[26:33], v[206:213], v[122:125], v190, v190 op_sel_hi:[0,0,0]
	v_mfma_scale_f32_16x16x128_f8f6f4 v[114:117], v[18:25], v[214:221], v[114:117], v190, v190 op_sel_hi:[0,0,0]
	v_mfma_scale_f32_16x16x128_f8f6f4 v[106:109], v[26:33], v[214:221], v[106:109], v190, v190 op_sel_hi:[0,0,0]
	v_mfma_scale_f32_16x16x128_f8f6f4 v[102:105], v[18:25], v[222:229], v[102:105], v190, v190 op_sel_hi:[0,0,0]
	v_mfma_scale_f32_16x16x128_f8f6f4 v[98:101], v[26:33], v[222:229], v[98:101], v190, v190 op_sel_hi:[0,0,0]
	s_setprio 0
	s_barrier
	s_add_i32 s30, s63, s34
	v_lshl_add_u64 v[184:185], v[184:185], 0, s[12:13]
	s_mov_b32 m0, s30
	ds_read_b128 v[198:201], v196 offset:49152
	ds_read_b128 v[202:205], v196 offset:50176
	ds_read_b128 v[206:209], v196 offset:51200
	ds_read_b128 v[210:213], v196 offset:52224
	ds_read_b128 v[214:217], v196 offset:53248
	ds_read_b128 v[218:221], v196 offset:54272
	ds_read_b128 v[222:225], v196 offset:55296
	ds_read_b128 v[226:229], v196 offset:56320
	global_load_lds_dwordx4 v[184:185], off
	s_add_i32 m0, s30, 0x2000
	s_add_u32 s28, s28, 0xb0080
	v_lshl_add_u64 v[182:183], v[182:183], 0, s[12:13]
	s_addc_u32 s29, s29, 0
	s_add_i32 s30, s66, s34
	global_load_lds_dwordx4 v[182:183], off
	v_lshl_add_u64 v[182:183], s[28:29], 0, v[162:163]
	s_mov_b32 m0, s30
	s_nop 0
	global_load_lds_dwordx4 v[182:183], off
	v_lshl_add_u64 v[182:183], s[28:29], 0, v[164:165]
	s_add_i32 m0, s30, 0x2000
	s_nop 0
	global_load_lds_dwordx4 v[182:183], off
	v_lshl_add_u64 v[182:183], v[186:187], 0, s[12:13]
	s_mov_b32 m0, s40
	s_nop 0
	global_load_lds_dwordx4 v[182:183], off
	v_lshl_add_u64 v[182:183], v[188:189], 0, s[12:13]
	s_mov_b32 m0, s41
	s_nop 0
	global_load_lds_dwordx4 v[182:183], off
	s_waitcnt vmcnt(8) lgkmcnt(0)
	s_barrier
	s_setprio 1
	v_mfma_scale_f32_16x16x128_f8f6f4 v[94:97], v[2:9], v[198:205], v[94:97], v190, v190 op_sel_hi:[0,0,0]
	v_mfma_scale_f32_16x16x128_f8f6f4 v[90:93], v[10:17], v[198:205], v[90:93], v190, v190 op_sel_hi:[0,0,0]
	v_mfma_scale_f32_16x16x128_f8f6f4 v[86:89], v[2:9], v[206:213], v[86:89], v190, v190 op_sel_hi:[0,0,0]
	v_mfma_scale_f32_16x16x128_f8f6f4 v[78:81], v[10:17], v[206:213], v[78:81], v190, v190 op_sel_hi:[0,0,0]
	v_mfma_scale_f32_16x16x128_f8f6f4 v[62:65], v[2:9], v[214:221], v[62:65], v190, v190 op_sel_hi:[0,0,0]
	v_mfma_scale_f32_16x16x128_f8f6f4 v[54:57], v[10:17], v[214:221], v[54:57], v190, v190 op_sel_hi:[0,0,0]
	v_mfma_scale_f32_16x16x128_f8f6f4 v[46:49], v[2:9], v[222:229], v[46:49], v190, v190 op_sel_hi:[0,0,0]
	v_mfma_scale_f32_16x16x128_f8f6f4 v[38:41], v[10:17], v[222:229], v[38:41], v190, v190 op_sel_hi:[0,0,0]
	v_mfma_scale_f32_16x16x128_f8f6f4 v[82:85], v[18:25], v[198:205], v[82:85], v190, v190 op_sel_hi:[0,0,0]
	v_mfma_scale_f32_16x16x128_f8f6f4 v[74:77], v[26:33], v[198:205], v[74:77], v190, v190 op_sel_hi:[0,0,0]
	v_mfma_scale_f32_16x16x128_f8f6f4 v[58:61], v[18:25], v[206:213], v[58:61], v190, v190 op_sel_hi:[0,0,0]
	v_mfma_scale_f32_16x16x128_f8f6f4 v[50:53], v[26:33], v[206:213], v[50:53], v190, v190 op_sel_hi:[0,0,0]
	v_mfma_scale_f32_16x16x128_f8f6f4 v[42:45], v[18:25], v[214:221], v[42:45], v190, v190 op_sel_hi:[0,0,0]
	v_mfma_scale_f32_16x16x128_f8f6f4 v[34:37], v[26:33], v[214:221], v[34:37], v190, v190 op_sel_hi:[0,0,0]
	v_mfma_scale_f32_16x16x128_f8f6f4 v[70:73], v[18:25], v[222:229], v[70:73], v190, v190 op_sel_hi:[0,0,0]
	v_mfma_scale_f32_16x16x128_f8f6f4 v[66:69], v[26:33], v[222:229], v[66:69], v190, v190 op_sel_hi:[0,0,0]
	s_setprio 0
	s_barrier
	s_add_i32 s62, s62, 2
	s_cmp_gt_u32 s62, 41
	s_mov_b64 s[30:31], s[26:27]
	s_cbranch_scc0 .LBB0_1237
	s_and_b64 vcc, exec, s[14:15]
	s_cbranch_vccz .LBB0_1240
	s_barrier

; #define PG8_STAGE(bufoff, gbase, voff) do { _Pragma("unroll") for (int _i = 0; _i < 2; ++_i) \
;         __builtin_amdgcn_global_load_lds((const unsigned*)((const char*)(gbase) + (voff)[_i]), (LAS unsigned*)(lds + (bufoff) + ldsw + _i * 8192), 16, 0, 0); } while (0)
; #define PG8_LDA(dst, b, h) do { _Pragma("unroll") for (int m = 0; m < 4; ++m) dst[m] = PG8_LD32(lds + PG8_SA(b, h) + aoff + m * 2048); } while (0)
; #define PG8_LDB(dst, b, h) do { _Pragma("unroll") for (int n = 0; n < 2; ++n) dst[n] = PG8_LD32(lds + PG8_SB(b, h) + boff + n * 2048); } while (0)
; #define PG8_WAIT_V(n) asm volatile("s_waitcnt vmcnt(" #n ")" ::: "memory")
; #define PG8_WAIT_L(n) asm volatile("s_waitcnt lgkmcnt(" #n ")" ::: "memory")
; #define PG8_BAR __builtin_amdgcn_s_barrier()
; #define PG8_SCHED __builtin_amdgcn_sched_barrier(0)
; #define PG8_STA(bufoff, nextflag, h, koff) do { if constexpr (Sched::GATHER) { unsigned _o[2]; _o[0] = (nextflag) ? nxtA[h][0] : curA[h][0]; _o[1] = (nextflag) ? nxtA[h][1] : curA[h][1]; PG8_STAGE(bufoff, Ab + (koff), _o); } \
;         else { PG8_STAGE(bufoff, ((nextflag) ? nA : cA) + (size_t)(h) * hstep + (koff), voffA); } } while (0)
; template <class Epi, class Sched, bool ALIGN_EPI, int DT>
; __device__ __forceinline__ void gemm_phase(LAS unsigned char* lds, const int KB, const Sched& S, const Epi& E) {
;     ...
;         for (int t = 0; t < nt; t += 2) {
;             const bool last = (t == nt - 2);
;             const size_t k1 = (size_t)(t + 1) * kstep, k2 = last ? 0 : (size_t)(t + 2) * kstep, k3 = k2 + kstep;
;             const char* b2 = last ? nB : cB + (size_t)(t + 2) * kstep; const char* b3 = b2 + kstep;
;             PG8_LDB(B0, 0, 0); PG8_LDB(B1, 0, 1); PG8_SCHED; PG8_LDA(At, 0, 0); PG8_STA(PG8_SA(1, 1), false, 1, k1);
;             PG8_WAIT_V(8); PG8_WAIT_L(0); PG8_BAR; PG8_MMA(0, 0, At, B0); PG8_MMA(0, 1, At, B1); PG8_BAR; PG8_SCHED;
;             PG8_LDA(At, 0, 1); PG8_STAGE(PG8_SB(0, 0), b2, voffB); PG8_STAGE(PG8_SB(0, 1), b2 + hstep, voffB); PG8_STA(PG8_SA(0, 0), last, 0, k2);
;             PG8_WAIT_V(8); PG8_WAIT_L(0); PG8_BAR; PG8_MMA(1, 0, At, B0); PG8_MMA(1, 1, At, B1); PG8_BAR; PG8_SCHED;
.LBB0_1385:
	ds_read_b128 v[152:155], v174
	ds_read_b128 v[156:159], v174 offset:1024
	ds_read_b128 v[160:163], v174 offset:2048
	ds_read_b128 v[164:167], v174 offset:3072
	ds_read_b128 v[168:171], v175
	ds_read_b128 v[180:183], v175 offset:1024
	ds_read_b128 v[184:187], v175 offset:2048
	ds_read_b128 v[188:191], v175 offset:3072
	s_add_u32 s38, s36, 0x100
	s_addc_u32 s39, s37, 0
	s_add_u32 s74, s25, s36
	s_addc_u32 s75, s70, s37
	s_cmp_eq_u32 s71, 12
	s_cselect_b64 s[42:43], -1, 0
	s_and_b64 s[40:41], s[42:43], exec
	s_cselect_b32 s76, 0, s38
	s_cselect_b32 s41, s0, s75
	s_cselect_b32 s40, s23, s74
	v_lshl_add_u64 v[192:193], v[148:149], 0, s[36:37]
	s_add_i32 m0, s47, 0xc000
	ds_read_b128 v[196:199], v176
	ds_read_b128 v[200:203], v176 offset:1024
	ds_read_b128 v[204:207], v176 offset:2048
	ds_read_b128 v[208:211], v176 offset:3072
	ds_read_b128 v[212:215], v176 offset:4096
	ds_read_b128 v[216:219], v176 offset:5120
	ds_read_b128 v[220:223], v176 offset:6144
	ds_read_b128 v[224:227], v176 offset:7168
	global_load_lds_dwordx4 v[192:193], off
	v_lshl_add_u64 v[192:193], v[150:151], 0, s[36:37]
	s_add_i32 m0, s47, 0xe000
	s_nop 0
	global_load_lds_dwordx4 v[192:193], off
	s_waitcnt vmcnt(8) lgkmcnt(0)
	s_barrier
	s_setprio 1
	v_mfma_i32_16x16x64_i8 v[126:129], v[152:155], v[196:199], v[126:129]
	v_mfma_i32_16x16x64_i8 v[122:125], v[160:163], v[196:199], v[122:125]
	v_mfma_i32_16x16x64_i8 v[110:113], v[152:155], v[204:207], v[110:113]
	v_mfma_i32_16x16x64_i8 v[106:109], v[160:163], v[204:207], v[106:109]
	v_mfma_i32_16x16x64_i8 v[94:97], v[152:155], v[212:215], v[94:97]
	v_mfma_i32_16x16x64_i8 v[90:93], v[160:163], v[212:215], v[90:93]
	v_mfma_i32_16x16x64_i8 v[78:81], v[152:155], v[220:223], v[78:81]
	v_mfma_i32_16x16x64_i8 v[74:77], v[160:163], v[220:223], v[74:77]
	v_mfma_i32_16x16x64_i8 v[126:129], v[156:159], v[200:203], v[126:129]
	v_mfma_i32_16x16x64_i8 v[122:125], v[164:167], v[200:203], v[122:125]
	v_mfma_i32_16x16x64_i8 v[110:113], v[156:159], v[208:211], v[110:113]
	v_mfma_i32_16x16x64_i8 v[106:109], v[164:167], v[208:211], v[106:109]
	v_mfma_i32_16x16x64_i8 v[94:97], v[156:159], v[216:219], v[94:97]
	v_mfma_i32_16x16x64_i8 v[90:93], v[164:167], v[216:219], v[90:93]
	v_mfma_i32_16x16x64_i8 v[78:81], v[156:159], v[224:227], v[78:81]
	v_mfma_i32_16x16x64_i8 v[74:77], v[164:167], v[224:227], v[74:77]
	v_mfma_i32_16x16x64_i8 v[118:121], v[168:171], v[196:199], v[118:121]
	v_mfma_i32_16x16x64_i8 v[114:117], v[184:187], v[196:199], v[114:117]
	v_mfma_i32_16x16x64_i8 v[102:105], v[168:171], v[204:207], v[102:105]
	v_mfma_i32_16x16x64_i8 v[98:101], v[184:187], v[204:207], v[98:101]
	v_mfma_i32_16x16x64_i8 v[86:89], v[168:171], v[212:215], v[86:89]
	v_mfma_i32_16x16x64_i8 v[82:85], v[184:187], v[212:215], v[82:85]
	v_mfma_i32_16x16x64_i8 v[70:73], v[168:171], v[220:223], v[70:73]
	v_mfma_i32_16x16x64_i8 v[66:69], v[184:187], v[220:223], v[66:69]
	v_mfma_i32_16x16x64_i8 v[118:121], v[180:183], v[200:203], v[118:121]
	v_mfma_i32_16x16x64_i8 v[114:117], v[188:191], v[200:203], v[114:117]
	v_mfma_i32_16x16x64_i8 v[102:105], v[180:183], v[208:211], v[102:105]
	v_mfma_i32_16x16x64_i8 v[98:101], v[188:191], v[208:211], v[98:101]
	v_mfma_i32_16x16x64_i8 v[86:89], v[180:183], v[216:219], v[86:89]
	v_mfma_i32_16x16x64_i8 v[82:85], v[188:191], v[216:219], v[82:85]
	v_mfma_i32_16x16x64_i8 v[70:73], v[180:183], v[224:227], v[70:73]
	v_mfma_i32_16x16x64_i8 v[66:69], v[188:191], v[224:227], v[66:69]
	s_setprio 0
	s_barrier
	s_add_i32 s36, s66, s44
	v_lshl_add_u64 v[192:193], s[40:41], 0, v[134:135]
	s_mov_b32 m0, s36
	ds_read_b128 v[196:199], v176 offset:16384
	ds_read_b128 v[200:203], v176 offset:17408
	ds_read_b128 v[204:207], v176 offset:18432
	ds_read_b128 v[208:211], v176 offset:19456
	ds_read_b128 v[212:215], v176 offset:20480
	ds_read_b128 v[216:219], v176 offset:21504
	ds_read_b128 v[220:223], v176 offset:22528
	ds_read_b128 v[224:227], v176 offset:23552
	global_load_lds_dwordx4 v[192:193], off
	s_add_i32 m0, s36, 0x2000
	s_add_u32 s36, s40, 0x40000
	v_lshl_add_u64 v[228:229], s[40:41], 0, v[132:133]
	s_addc_u32 s37, s41, 0
	s_add_i32 s74, s67, s44
	global_load_lds_dwordx4 v[228:229], off
	v_lshl_add_u64 v[230:231], s[36:37], 0, v[134:135]
	s_mov_b32 m0, s74
	s_nop 0
	global_load_lds_dwordx4 v[230:231], off
	v_lshl_add_u64 v[230:231], s[36:37], 0, v[132:133]
	s_add_i32 m0, s74, 0x2000
	s_and_b64 s[36:37], s[8:9], s[42:43]
	s_and_b64 s[36:37], s[36:37], exec
	s_cselect_b32 s36, s26, s34
	s_cselect_b32 s37, s27, s35
	s_add_u32 s36, s36, s76
	s_addc_u32 s37, s37, 0
	global_load_lds_dwordx4 v[230:231], off
	v_lshl_add_u64 v[230:231], s[36:37], 0, v[136:137]
	s_mov_b32 m0, s47
	v_lshl_add_u64 v[232:233], s[36:37], 0, v[138:139]
	global_load_lds_dwordx4 v[230:231], off
	s_mov_b32 m0, s49
	s_nop 0
	global_load_lds_dwordx4 v[232:233], off
	s_waitcnt vmcnt(8) lgkmcnt(0)
	s_barrier
; #define PG8_LDA(dst, b, h) do { _Pragma("unroll") for (int m = 0; m < 4; ++m) dst[m] = PG8_LD32(lds + PG8_SA(b, h) + aoff + m * 2048); } while (0)
; #define PG8_LDB(dst, b, h) do { _Pragma("unroll") for (int n = 0; n < 2; ++n) dst[n] = PG8_LD32(lds + PG8_SB(b, h) + boff + n * 2048); } while (0)
; #define PG8_WAIT_V(n) asm volatile("s_waitcnt vmcnt(" #n ")" ::: "memory")
; #define PG8_WAIT_L(n) asm volatile("s_waitcnt lgkmcnt(" #n ")" ::: "memory")
; #define PG8_BAR __builtin_amdgcn_s_barrier()
; #define PG8_SCHED __builtin_amdgcn_sched_barrier(0)
; #define PG8_STA(bufoff, nextflag, h, koff) do { if constexpr (Sched::GATHER) { unsigned _o[2]; _o[0] = (nextflag) ? nxtA[h][0] : curA[h][0]; _o[1] = (nextflag) ? nxtA[h][1] : curA[h][1]; PG8_STAGE(bufoff, Ab + (koff), _o); } \
;         else { PG8_STAGE(bufoff, ((nextflag) ? nA : cA) + (size_t)(h) * hstep + (koff), voffA); } } while (0)
; template <class Epi, class Sched, bool ALIGN_EPI, int DT>
; __device__ __forceinline__ void gemm_phase(LAS unsigned char* lds, const int KB, const Sched& S, const Epi& E) {
;     ...
;             PG8_WAIT_V(8); PG8_WAIT_L(0); PG8_BAR; PG8_MMA(1, 0, At, B0); PG8_MMA(1, 1, At, B1); PG8_BAR; PG8_SCHED;
;             PG8_LDB(B0, 1, 0); PG8_LDB(B1, 1, 1); PG8_SCHED; PG8_LDA(At, 1, 0); PG8_STA(PG8_SA(0, 1), last, 1, k2);
;             PG8_WAIT_V(8); PG8_WAIT_L(0); PG8_BAR; PG8_MMA(0, 0, At, B0); PG8_MMA(0, 1, At, B1); PG8_BAR; PG8_SCHED;
	s_setprio 1
	v_mfma_i32_16x16x64_i8 v[62:65], v[152:155], v[196:199], v[62:65]
	v_mfma_i32_16x16x64_i8 v[58:61], v[160:163], v[196:199], v[58:61]
	v_mfma_i32_16x16x64_i8 v[46:49], v[152:155], v[204:207], v[46:49]
	v_mfma_i32_16x16x64_i8 v[42:45], v[160:163], v[204:207], v[42:45]
	v_mfma_i32_16x16x64_i8 v[30:33], v[152:155], v[212:215], v[30:33]
	v_mfma_i32_16x16x64_i8 v[26:29], v[160:163], v[212:215], v[26:29]
	v_mfma_i32_16x16x64_i8 v[6:9], v[152:155], v[220:223], v[6:9]
	v_mfma_i32_16x16x64_i8 v[2:5], v[160:163], v[220:223], v[2:5]
	v_mfma_i32_16x16x64_i8 v[62:65], v[156:159], v[200:203], v[62:65]
	v_mfma_i32_16x16x64_i8 v[58:61], v[164:167], v[200:203], v[58:61]
	v_mfma_i32_16x16x64_i8 v[46:49], v[156:159], v[208:211], v[46:49]
	v_mfma_i32_16x16x64_i8 v[42:45], v[164:167], v[208:211], v[42:45]
	v_mfma_i32_16x16x64_i8 v[30:33], v[156:159], v[216:219], v[30:33]
	v_mfma_i32_16x16x64_i8 v[26:29], v[164:167], v[216:219], v[26:29]
	v_mfma_i32_16x16x64_i8 v[6:9], v[156:159], v[224:227], v[6:9]
	v_mfma_i32_16x16x64_i8 v[2:5], v[164:167], v[224:227], v[2:5]
	v_mfma_i32_16x16x64_i8 v[54:57], v[168:171], v[196:199], v[54:57]
	v_mfma_i32_16x16x64_i8 v[50:53], v[184:187], v[196:199], v[50:53]
	v_mfma_i32_16x16x64_i8 v[38:41], v[168:171], v[204:207], v[38:41]
	v_mfma_i32_16x16x64_i8 v[34:37], v[184:187], v[204:207], v[34:37]
	v_mfma_i32_16x16x64_i8 v[14:17], v[168:171], v[212:215], v[14:17]
	v_mfma_i32_16x16x64_i8 v[10:13], v[184:187], v[212:215], v[10:13]
	v_mfma_i32_16x16x64_i8 v[22:25], v[168:171], v[220:223], v[22:25]
	v_mfma_i32_16x16x64_i8 v[18:21], v[184:187], v[220:223], v[18:21]
	v_mfma_i32_16x16x64_i8 v[54:57], v[180:183], v[200:203], v[54:57]
	v_mfma_i32_16x16x64_i8 v[50:53], v[188:191], v[200:203], v[50:53]
	v_mfma_i32_16x16x64_i8 v[38:41], v[180:183], v[208:211], v[38:41]
	v_mfma_i32_16x16x64_i8 v[34:37], v[188:191], v[208:211], v[34:37]
	v_mfma_i32_16x16x64_i8 v[14:17], v[180:183], v[216:219], v[14:17]
	v_mfma_i32_16x16x64_i8 v[10:13], v[188:191], v[216:219], v[10:13]
	v_mfma_i32_16x16x64_i8 v[22:25], v[180:183], v[224:227], v[22:25]
	v_mfma_i32_16x16x64_i8 v[18:21], v[188:191], v[224:227], v[18:21]
	s_setprio 0
	s_barrier
	s_add_i32 s42, 0, 0x18000
	v_add_u32_e32 v1, s42, v172
	s_add_i32 s43, 0, 0x1c000
	ds_read_b128 v[152:155], v1
	ds_read_b128 v[156:159], v1 offset:1024
	ds_read_b128 v[160:163], v1 offset:2048
	ds_read_b128 v[164:167], v1 offset:3072
	v_add_u32_e32 v1, s43, v172
	ds_read_b128 v[168:171], v1
	ds_read_b128 v[180:183], v1 offset:1024
	ds_read_b128 v[184:187], v1 offset:2048
	ds_read_b128 v[188:191], v1 offset:3072
	s_add_u32 s36, s36, 0x40000
	s_addc_u32 s37, s37, 0
	s_mov_b32 m0, s52
	v_lshl_add_u64 v[234:235], s[36:37], 0, v[136:137]
	ds_read_b128 v[196:199], v176 offset:32768
	ds_read_b128 v[200:203], v176 offset:33792
	ds_read_b128 v[204:207], v176 offset:34816
	ds_read_b128 v[208:211], v176 offset:35840
	ds_read_b128 v[212:215], v176 offset:36864
	ds_read_b128 v[216:219], v176 offset:37888
	ds_read_b128 v[220:223], v176 offset:38912
	ds_read_b128 v[224:227], v176 offset:39936
	global_load_lds_dwordx4 v[234:235], off
	v_lshl_add_u64 v[234:235], s[36:37], 0, v[138:139]
	s_mov_b32 m0, s53
	s_nop 0
	global_load_lds_dwordx4 v[234:235], off
	s_waitcnt vmcnt(8) lgkmcnt(0)
	s_barrier
	s_setprio 1
	v_mfma_i32_16x16x64_i8 v[126:129], v[152:155], v[196:199], v[126:129]
	v_mfma_i32_16x16x64_i8 v[122:125], v[160:163], v[196:199], v[122:125]
	v_mfma_i32_16x16x64_i8 v[110:113], v[152:155], v[204:207], v[110:113]
	v_mfma_i32_16x16x64_i8 v[106:109], v[160:163], v[204:207], v[106:109]
	v_mfma_i32_16x16x64_i8 v[94:97], v[152:155], v[212:215], v[94:97]
	v_mfma_i32_16x16x64_i8 v[90:93], v[160:163], v[212:215], v[90:93]
	v_mfma_i32_16x16x64_i8 v[78:81], v[152:155], v[220:223], v[78:81]
	v_mfma_i32_16x16x64_i8 v[74:77], v[160:163], v[220:223], v[74:77]
	v_mfma_i32_16x16x64_i8 v[126:129], v[156:159], v[200:203], v[126:129]
	v_mfma_i32_16x16x64_i8 v[122:125], v[164:167], v[200:203], v[122:125]
	v_mfma_i32_16x16x64_i8 v[110:113], v[156:159], v[208:211], v[110:113]
	v_mfma_i32_16x16x64_i8 v[106:109], v[164:167], v[208:211], v[106:109]
	v_mfma_i32_16x16x64_i8 v[94:97], v[156:159], v[216:219], v[94:97]
	v_mfma_i32_16x16x64_i8 v[90:93], v[164:167], v[216:219], v[90:93]
	v_mfma_i32_16x16x64_i8 v[78:81], v[156:159], v[224:227], v[78:81]
	v_mfma_i32_16x16x64_i8 v[74:77], v[164:167], v[224:227], v[74:77]
	v_mfma_i32_16x16x64_i8 v[118:121], v[168:171], v[196:199], v[118:121]
	v_mfma_i32_16x16x64_i8 v[114:117], v[184:187], v[196:199], v[114:117]
	v_mfma_i32_16x16x64_i8 v[102:105], v[168:171], v[204:207], v[102:105]
	v_mfma_i32_16x16x64_i8 v[98:101], v[184:187], v[204:207], v[98:101]
	v_mfma_i32_16x16x64_i8 v[86:89], v[168:171], v[212:215], v[86:89]
	v_mfma_i32_16x16x64_i8 v[82:85], v[184:187], v[212:215], v[82:85]
	v_mfma_i32_16x16x64_i8 v[70:73], v[168:171], v[220:223], v[70:73]
	v_mfma_i32_16x16x64_i8 v[66:69], v[184:187], v[220:223], v[66:69]
	v_mfma_i32_16x16x64_i8 v[118:121], v[180:183], v[200:203], v[118:121]
	v_mfma_i32_16x16x64_i8 v[114:117], v[188:191], v[200:203], v[114:117]
	v_mfma_i32_16x16x64_i8 v[102:105], v[180:183], v[208:211], v[102:105]
	v_mfma_i32_16x16x64_i8 v[98:101], v[188:191], v[208:211], v[98:101]
	v_mfma_i32_16x16x64_i8 v[86:89], v[180:183], v[216:219], v[86:89]
	v_mfma_i32_16x16x64_i8 v[82:85], v[188:191], v[216:219], v[82:85]
	v_mfma_i32_16x16x64_i8 v[70:73], v[180:183], v[224:227], v[70:73]
	v_mfma_i32_16x16x64_i8 v[66:69], v[188:191], v[224:227], v[66:69]
	s_setprio 0
	s_barrier
; #define PG8_STAGE(bufoff, gbase, voff) do { _Pragma("unroll") for (int _i = 0; _i < 2; ++_i) \
;         __builtin_amdgcn_global_load_lds((const unsigned*)((const char*)(gbase) + (voff)[_i]), (LAS unsigned*)(lds + (bufoff) + ldsw + _i * 8192), 16, 0, 0); } while (0)
; #define PG8_LDA(dst, b, h) do { _Pragma("unroll") for (int m = 0; m < 4; ++m) dst[m] = PG8_LD32(lds + PG8_SA(b, h) + aoff + m * 2048); } while (0)
; #define PG8_WAIT_V(n) asm volatile("s_waitcnt vmcnt(" #n ")" ::: "memory")
; #define PG8_WAIT_L(n) asm volatile("s_waitcnt lgkmcnt(" #n ")" ::: "memory")
; #define PG8_BAR __builtin_amdgcn_s_barrier()
; #define PG8_SCHED __builtin_amdgcn_sched_barrier(0)
; #define PG8_STA(bufoff, nextflag, h, koff) do { if constexpr (Sched::GATHER) { unsigned _o[2]; _o[0] = (nextflag) ? nxtA[h][0] : curA[h][0]; _o[1] = (nextflag) ? nxtA[h][1] : curA[h][1]; PG8_STAGE(bufoff, Ab + (koff), _o); } \
;         else { PG8_STAGE(bufoff, ((nextflag) ? nA : cA) + (size_t)(h) * hstep + (koff), voffA); } } while (0)
; template <class Epi, class Sched, bool ALIGN_EPI, int DT>
; __device__ __forceinline__ void gemm_phase(LAS unsigned char* lds, const int KB, const Sched& S, const Epi& E) {
;     ...
;             PG8_LDA(At, 1, 1); PG8_STAGE(PG8_SB(1, 0), b3, voffB); PG8_STAGE(PG8_SB(1, 1), b3 + hstep, voffB); PG8_STA(PG8_SA(1, 0), last, 0, k3);
;             PG8_WAIT_V(8); PG8_WAIT_L(0); PG8_BAR; PG8_MMA(1, 0, At, B0); PG8_MMA(1, 1, At, B1); PG8_BAR; PG8_SCHED;
;         }
;         if constexpr (ALIGN_EPI) { if (wr == 0) PG8_BAR; }
	s_add_i32 s36, s42, s44
	v_lshl_add_u64 v[192:193], v[192:193], 0, s[18:19]
	s_mov_b32 m0, s36
	ds_read_b128 v[196:199], v176 offset:49152
	ds_read_b128 v[200:203], v176 offset:50176
	ds_read_b128 v[204:207], v176 offset:51200
	ds_read_b128 v[208:211], v176 offset:52224
	ds_read_b128 v[212:215], v176 offset:53248
	ds_read_b128 v[216:219], v176 offset:54272
	ds_read_b128 v[220:223], v176 offset:55296
	ds_read_b128 v[224:227], v176 offset:56320
	global_load_lds_dwordx4 v[192:193], off
	s_add_i32 m0, s36, 0x2000
	s_add_u32 s36, s40, 0x40080
	v_lshl_add_u64 v[192:193], v[228:229], 0, s[18:19]
	s_addc_u32 s37, s41, 0
	s_add_i32 s40, s43, s44
	global_load_lds_dwordx4 v[192:193], off
	v_lshl_add_u64 v[192:193], s[36:37], 0, v[134:135]
	s_mov_b32 m0, s40
	s_nop 0
	global_load_lds_dwordx4 v[192:193], off
	v_lshl_add_u64 v[192:193], s[36:37], 0, v[132:133]
	s_add_i32 m0, s40, 0x2000
	s_nop 0
	global_load_lds_dwordx4 v[192:193], off
	v_lshl_add_u64 v[192:193], v[230:231], 0, s[18:19]
	s_mov_b32 m0, s57
	s_nop 0
	global_load_lds_dwordx4 v[192:193], off
	v_lshl_add_u64 v[192:193], v[232:233], 0, s[18:19]
	s_mov_b32 m0, s62
	s_nop 0
	global_load_lds_dwordx4 v[192:193], off
	s_waitcnt vmcnt(8) lgkmcnt(0)
	s_barrier
	s_setprio 1
	v_mfma_i32_16x16x64_i8 v[62:65], v[152:155], v[196:199], v[62:65]
	v_mfma_i32_16x16x64_i8 v[58:61], v[160:163], v[196:199], v[58:61]
	v_mfma_i32_16x16x64_i8 v[46:49], v[152:155], v[204:207], v[46:49]
	v_mfma_i32_16x16x64_i8 v[42:45], v[160:163], v[204:207], v[42:45]
	v_mfma_i32_16x16x64_i8 v[30:33], v[152:155], v[212:215], v[30:33]
	v_mfma_i32_16x16x64_i8 v[26:29], v[160:163], v[212:215], v[26:29]
	v_mfma_i32_16x16x64_i8 v[6:9], v[152:155], v[220:223], v[6:9]
	v_mfma_i32_16x16x64_i8 v[2:5], v[160:163], v[220:223], v[2:5]
	v_mfma_i32_16x16x64_i8 v[62:65], v[156:159], v[200:203], v[62:65]
	v_mfma_i32_16x16x64_i8 v[58:61], v[164:167], v[200:203], v[58:61]
	v_mfma_i32_16x16x64_i8 v[46:49], v[156:159], v[208:211], v[46:49]
	v_mfma_i32_16x16x64_i8 v[42:45], v[164:167], v[208:211], v[42:45]
	v_mfma_i32_16x16x64_i8 v[30:33], v[156:159], v[216:219], v[30:33]
	v_mfma_i32_16x16x64_i8 v[26:29], v[164:167], v[216:219], v[26:29]
	v_mfma_i32_16x16x64_i8 v[6:9], v[156:159], v[224:227], v[6:9]
	v_mfma_i32_16x16x64_i8 v[2:5], v[164:167], v[224:227], v[2:5]
	v_mfma_i32_16x16x64_i8 v[54:57], v[168:171], v[196:199], v[54:57]
	v_mfma_i32_16x16x64_i8 v[50:53], v[184:187], v[196:199], v[50:53]
	v_mfma_i32_16x16x64_i8 v[38:41], v[168:171], v[204:207], v[38:41]
	v_mfma_i32_16x16x64_i8 v[34:37], v[184:187], v[204:207], v[34:37]
	v_mfma_i32_16x16x64_i8 v[14:17], v[168:171], v[212:215], v[14:17]
	v_mfma_i32_16x16x64_i8 v[10:13], v[184:187], v[212:215], v[10:13]
	v_mfma_i32_16x16x64_i8 v[22:25], v[168:171], v[220:223], v[22:25]
	v_mfma_i32_16x16x64_i8 v[18:21], v[184:187], v[220:223], v[18:21]
	v_mfma_i32_16x16x64_i8 v[54:57], v[180:183], v[200:203], v[54:57]
	v_mfma_i32_16x16x64_i8 v[50:53], v[188:191], v[200:203], v[50:53]
	v_mfma_i32_16x16x64_i8 v[38:41], v[180:183], v[208:211], v[38:41]
	v_mfma_i32_16x16x64_i8 v[34:37], v[188:191], v[208:211], v[34:37]
	v_mfma_i32_16x16x64_i8 v[14:17], v[180:183], v[216:219], v[14:17]
	v_mfma_i32_16x16x64_i8 v[10:13], v[188:191], v[216:219], v[10:13]
	v_mfma_i32_16x16x64_i8 v[22:25], v[180:183], v[224:227], v[22:25]
	v_mfma_i32_16x16x64_i8 v[18:21], v[188:191], v[224:227], v[18:21]
	s_setprio 0
	s_barrier
	s_add_i32 s71, s71, 2
	s_cmp_gt_u32 s71, 13
	s_mov_b64 s[36:37], s[38:39]
	s_cbranch_scc0 .LBB0_1385
	s_and_b64 vcc, exec, s[20:21]
	s_cbranch_vccz .LBB0_1388
	s_barrier

; #define PG8_STAGE(bufoff, gbase, voff) do { _Pragma("unroll") for (int _i = 0; _i < 2; ++_i) \
;         __builtin_amdgcn_global_load_lds((const unsigned*)((const char*)(gbase) + (voff)[_i]), (LAS unsigned*)(lds + (bufoff) + ldsw + _i * 8192), 16, 0, 0); } while (0)
; #define PG8_LDA(dst, b, h) do { _Pragma("unroll") for (int m = 0; m < 4; ++m) dst[m] = PG8_LD32(lds + PG8_SA(b, h) + aoff + m * 2048); } while (0)
; #define PG8_LDB(dst, b, h) do { _Pragma("unroll") for (int n = 0; n < 2; ++n) dst[n] = PG8_LD32(lds + PG8_SB(b, h) + boff + n * 2048); } while (0)
; #define PG8_WAIT_V(n) asm volatile("s_waitcnt vmcnt(" #n ")" ::: "memory")
; #define PG8_WAIT_L(n) asm volatile("s_waitcnt lgkmcnt(" #n ")" ::: "memory")
; #define PG8_BAR __builtin_amdgcn_s_barrier()
; #define PG8_SCHED __builtin_amdgcn_sched_barrier(0)
; #define PG8_STA(bufoff, nextflag, h, koff) do { if constexpr (Sched::GATHER) { unsigned _o[2]; _o[0] = (nextflag) ? nxtA[h][0] : curA[h][0]; _o[1] = (nextflag) ? nxtA[h][1] : curA[h][1]; PG8_STAGE(bufoff, Ab + (koff), _o); } \
;         else { PG8_STAGE(bufoff, ((nextflag) ? nA : cA) + (size_t)(h) * hstep + (koff), voffA); } } while (0)
; template <class Epi, class Sched, bool ALIGN_EPI, int DT>
; __device__ __forceinline__ void gemm_phase(LAS unsigned char* lds, const int KB, const Sched& S, const Epi& E) {
;     ...
;         for (int t = 0; t < nt; t += 2) {
;             const bool last = (t == nt - 2);
;             const size_t k1 = (size_t)(t + 1) * kstep, k2 = last ? 0 : (size_t)(t + 2) * kstep, k3 = k2 + kstep;
;             const char* b2 = last ? nB : cB + (size_t)(t + 2) * kstep; const char* b3 = b2 + kstep;
;             PG8_LDB(B0, 0, 0); PG8_LDB(B1, 0, 1); PG8_SCHED; PG8_LDA(At, 0, 0); PG8_STA(PG8_SA(1, 1), false, 1, k1);
;             PG8_WAIT_V(8); PG8_WAIT_L(0); PG8_BAR; PG8_MMA(0, 0, At, B0); PG8_MMA(0, 1, At, B1); PG8_BAR; PG8_SCHED;
;             PG8_LDA(At, 0, 1); PG8_STAGE(PG8_SB(0, 0), b2, voffB); PG8_STAGE(PG8_SB(0, 1), b2 + hstep, voffB); PG8_STA(PG8_SA(0, 0), last, 0, k2);
;             PG8_WAIT_V(8); PG8_WAIT_L(0); PG8_BAR; PG8_MMA(1, 0, At, B0); PG8_MMA(1, 1, At, B1); PG8_BAR; PG8_SCHED;
.LBB0_2108:
	ds_read_b128 v[18:21], v193
	ds_read_b128 v[22:25], v193 offset:1024
	ds_read_b128 v[26:29], v193 offset:2048
	ds_read_b128 v[30:33], v193 offset:3072
	ds_read_b128 v[2:5], v195
	ds_read_b128 v[6:9], v195 offset:1024
	ds_read_b128 v[10:13], v195 offset:2048
	ds_read_b128 v[14:17], v195 offset:3072
	s_add_u32 s38, s42, 0x100
	s_addc_u32 s39, s43, 0
	s_add_u32 s71, s68, s42
	s_addc_u32 s74, s69, s43
	s_cmp_eq_u32 s70, 12
	s_cselect_b64 s[44:45], -1, 0
	s_and_b64 s[40:41], s[44:45], exec
	s_cselect_b32 s41, s25, s74
	s_cselect_b32 s40, s27, s71
	s_cselect_b32 s71, 0, s39
	s_cselect_b32 s74, 0, s38
	v_lshl_add_u64 v[222:223], v[178:179], 0, s[42:43]
	s_add_i32 m0, s35, 0xc000
	ds_read_b128 v[182:185], v196
	ds_read_b128 v[186:189], v196 offset:1024
	ds_read_b128 v[198:201], v196 offset:2048
	ds_read_b128 v[202:205], v196 offset:3072
	ds_read_b128 v[206:209], v196 offset:4096
	ds_read_b128 v[210:213], v196 offset:5120
	ds_read_b128 v[214:217], v196 offset:6144
	ds_read_b128 v[218:221], v196 offset:7168
	global_load_lds_dwordx4 v[222:223], off
	v_lshl_add_u64 v[222:223], v[180:181], 0, s[42:43]
	s_add_i32 m0, s35, 0xe000
	s_nop 0
	global_load_lds_dwordx4 v[222:223], off
	s_waitcnt vmcnt(8) lgkmcnt(0)
	s_barrier
	s_setprio 1
	v_mfma_scale_f32_16x16x128_f8f6f4 v[158:161], v[18:25], v[182:189], v[158:161], v1, v1 op_sel_hi:[0,0,0]
	v_mfma_scale_f32_16x16x128_f8f6f4 v[154:157], v[26:33], v[182:189], v[154:157], v1, v1 op_sel_hi:[0,0,0]
	v_mfma_scale_f32_16x16x128_f8f6f4 v[150:153], v[18:25], v[198:205], v[150:153], v1, v1 op_sel_hi:[0,0,0]
	v_mfma_scale_f32_16x16x128_f8f6f4 v[142:145], v[26:33], v[198:205], v[142:145], v1, v1 op_sel_hi:[0,0,0]
	v_mfma_scale_f32_16x16x128_f8f6f4 v[134:137], v[18:25], v[206:213], v[134:137], v1, v1 op_sel_hi:[0,0,0]
	v_mfma_scale_f32_16x16x128_f8f6f4 v[126:129], v[26:33], v[206:213], v[126:129], v1, v1 op_sel_hi:[0,0,0]
	v_mfma_scale_f32_16x16x128_f8f6f4 v[118:121], v[18:25], v[214:221], v[118:121], v1, v1 op_sel_hi:[0,0,0]
	v_mfma_scale_f32_16x16x128_f8f6f4 v[110:113], v[26:33], v[214:221], v[110:113], v1, v1 op_sel_hi:[0,0,0]
	v_mfma_scale_f32_16x16x128_f8f6f4 v[146:149], v[2:9], v[182:189], v[146:149], v1, v1 op_sel_hi:[0,0,0]
	v_mfma_scale_f32_16x16x128_f8f6f4 v[138:141], v[10:17], v[182:189], v[138:141], v1, v1 op_sel_hi:[0,0,0]
	v_mfma_scale_f32_16x16x128_f8f6f4 v[130:133], v[2:9], v[198:205], v[130:133], v1, v1 op_sel_hi:[0,0,0]
	v_mfma_scale_f32_16x16x128_f8f6f4 v[122:125], v[10:17], v[198:205], v[122:125], v1, v1 op_sel_hi:[0,0,0]
	v_mfma_scale_f32_16x16x128_f8f6f4 v[114:117], v[2:9], v[206:213], v[114:117], v1, v1 op_sel_hi:[0,0,0]
	v_mfma_scale_f32_16x16x128_f8f6f4 v[106:109], v[10:17], v[206:213], v[106:109], v1, v1 op_sel_hi:[0,0,0]
	v_mfma_scale_f32_16x16x128_f8f6f4 v[102:105], v[2:9], v[214:221], v[102:105], v1, v1 op_sel_hi:[0,0,0]
	v_mfma_scale_f32_16x16x128_f8f6f4 v[98:101], v[10:17], v[214:221], v[98:101], v1, v1 op_sel_hi:[0,0,0]
	s_setprio 0
	s_barrier
	s_add_i32 s42, s57, s46
	v_lshl_add_u64 v[182:183], s[40:41], 0, v[162:163]
	s_mov_b32 m0, s42
	ds_read_b128 v[198:201], v196 offset:16384
	ds_read_b128 v[202:205], v196 offset:17408
	ds_read_b128 v[206:209], v196 offset:18432
	ds_read_b128 v[210:213], v196 offset:19456
	ds_read_b128 v[214:217], v196 offset:20480
	ds_read_b128 v[218:221], v196 offset:21504
	ds_read_b128 v[222:225], v196 offset:22528
	ds_read_b128 v[226:229], v196 offset:23552
	global_load_lds_dwordx4 v[182:183], off
	s_add_i32 m0, s42, 0x2000
	s_add_u32 s42, s40, 0x40000
	v_lshl_add_u64 v[184:185], s[40:41], 0, v[164:165]
	s_addc_u32 s43, s41, 0
	s_add_i32 s75, s62, s46
	global_load_lds_dwordx4 v[184:185], off
	v_lshl_add_u64 v[186:187], s[42:43], 0, v[162:163]
	s_mov_b32 m0, s75
	s_nop 0
	global_load_lds_dwordx4 v[186:187], off
	v_lshl_add_u64 v[186:187], s[42:43], 0, v[164:165]
	s_add_i32 m0, s75, 0x2000
	s_and_b64 s[42:43], s[6:7], s[44:45]
	s_and_b64 s[42:43], s[42:43], exec
	s_cselect_b32 s42, s28, s36
	s_cselect_b32 s43, s29, s37
	s_add_u32 s42, s42, s74
	s_addc_u32 s43, s43, s71
	global_load_lds_dwordx4 v[186:187], off
	v_lshl_add_u64 v[186:187], s[42:43], 0, v[166:167]
	s_mov_b32 m0, s35
	v_lshl_add_u64 v[188:189], s[42:43], 0, v[168:169]
	global_load_lds_dwordx4 v[186:187], off
	s_mov_b32 m0, s47
	s_nop 0
	global_load_lds_dwordx4 v[188:189], off
	s_waitcnt vmcnt(8) lgkmcnt(0)
	s_barrier
	s_setprio 1
	v_mfma_scale_f32_16x16x128_f8f6f4 v[94:97], v[18:25], v[198:205], v[94:97], v1, v1 op_sel_hi:[0,0,0]
	v_mfma_scale_f32_16x16x128_f8f6f4 v[90:93], v[26:33], v[198:205], v[90:93], v1, v1 op_sel_hi:[0,0,0]
	v_mfma_scale_f32_16x16x128_f8f6f4 v[86:89], v[18:25], v[206:213], v[86:89], v1, v1 op_sel_hi:[0,0,0]
	v_mfma_scale_f32_16x16x128_f8f6f4 v[78:81], v[26:33], v[206:213], v[78:81], v1, v1 op_sel_hi:[0,0,0]
	v_mfma_scale_f32_16x16x128_f8f6f4 v[62:65], v[18:25], v[214:221], v[62:65], v1, v1 op_sel_hi:[0,0,0]
	v_mfma_scale_f32_16x16x128_f8f6f4 v[54:57], v[26:33], v[214:221], v[54:57], v1, v1 op_sel_hi:[0,0,0]
	v_mfma_scale_f32_16x16x128_f8f6f4 v[46:49], v[18:25], v[222:229], v[46:49], v1, v1 op_sel_hi:[0,0,0]
	v_mfma_scale_f32_16x16x128_f8f6f4 v[38:41], v[26:33], v[222:229], v[38:41], v1, v1 op_sel_hi:[0,0,0]
	v_mfma_scale_f32_16x16x128_f8f6f4 v[82:85], v[2:9], v[198:205], v[82:85], v1, v1 op_sel_hi:[0,0,0]
	v_mfma_scale_f32_16x16x128_f8f6f4 v[74:77], v[10:17], v[198:205], v[74:77], v1, v1 op_sel_hi:[0,0,0]
	v_mfma_scale_f32_16x16x128_f8f6f4 v[58:61], v[2:9], v[206:213], v[58:61], v1, v1 op_sel_hi:[0,0,0]
	v_mfma_scale_f32_16x16x128_f8f6f4 v[50:53], v[10:17], v[206:213], v[50:53], v1, v1 op_sel_hi:[0,0,0]
	v_mfma_scale_f32_16x16x128_f8f6f4 v[42:45], v[2:9], v[214:221], v[42:45], v1, v1 op_sel_hi:[0,0,0]
	v_mfma_scale_f32_16x16x128_f8f6f4 v[34:37], v[10:17], v[214:221], v[34:37], v1, v1 op_sel_hi:[0,0,0]
	v_mfma_scale_f32_16x16x128_f8f6f4 v[70:73], v[2:9], v[222:229], v[70:73], v1, v1 op_sel_hi:[0,0,0]
	v_mfma_scale_f32_16x16x128_f8f6f4 v[66:69], v[10:17], v[222:229], v[66:69], v1, v1 op_sel_hi:[0,0,0]
	s_setprio 0
	s_barrier
; #define PG8_STAGE(bufoff, gbase, voff) do { _Pragma("unroll") for (int _i = 0; _i < 2; ++_i) \
;         __builtin_amdgcn_global_load_lds((const unsigned*)((const char*)(gbase) + (voff)[_i]), (LAS unsigned*)(lds + (bufoff) + ldsw + _i * 8192), 16, 0, 0); } while (0)
; #define PG8_LDA(dst, b, h) do { _Pragma("unroll") for (int m = 0; m < 4; ++m) dst[m] = PG8_LD32(lds + PG8_SA(b, h) + aoff + m * 2048); } while (0)
; #define PG8_LDB(dst, b, h) do { _Pragma("unroll") for (int n = 0; n < 2; ++n) dst[n] = PG8_LD32(lds + PG8_SB(b, h) + boff + n * 2048); } while (0)
; #define PG8_WAIT_V(n) asm volatile("s_waitcnt vmcnt(" #n ")" ::: "memory")
; #define PG8_WAIT_L(n) asm volatile("s_waitcnt lgkmcnt(" #n ")" ::: "memory")
; #define PG8_BAR __builtin_amdgcn_s_barrier()
; #define PG8_SCHED __builtin_amdgcn_sched_barrier(0)
; #define PG8_STA(bufoff, nextflag, h, koff) do { if constexpr (Sched::GATHER) { unsigned _o[2]; _o[0] = (nextflag) ? nxtA[h][0] : curA[h][0]; _o[1] = (nextflag) ? nxtA[h][1] : curA[h][1]; PG8_STAGE(bufoff, Ab + (koff), _o); } \
;         else { PG8_STAGE(bufoff, ((nextflag) ? nA : cA) + (size_t)(h) * hstep + (koff), voffA); } } while (0)
; template <class Epi, class Sched, bool ALIGN_EPI, int DT>
; __device__ __forceinline__ void gemm_phase(LAS unsigned char* lds, const int KB, const Sched& S, const Epi& E) {
;     ...
;             PG8_LDB(B0, 1, 0); PG8_LDB(B1, 1, 1); PG8_SCHED; PG8_LDA(At, 1, 0); PG8_STA(PG8_SA(0, 1), last, 1, k2);
;             PG8_WAIT_V(8); PG8_WAIT_L(0); PG8_BAR; PG8_MMA(0, 0, At, B0); PG8_MMA(0, 1, At, B1); PG8_BAR; PG8_SCHED;
;             PG8_LDA(At, 1, 1); PG8_STAGE(PG8_SB(1, 0), b3, voffB); PG8_STAGE(PG8_SB(1, 1), b3 + hstep, voffB); PG8_STA(PG8_SA(1, 0), last, 0, k3);
;             PG8_WAIT_V(8); PG8_WAIT_L(0); PG8_BAR; PG8_MMA(1, 0, At, B0); PG8_MMA(1, 1, At, B1); PG8_BAR; PG8_SCHED;
;         }
;         if constexpr (ALIGN_EPI) { if (wr == 0) PG8_BAR; }
	s_add_i32 s44, 0, 0x18000
	s_add_i32 s45, 0, 0x1c000
	v_add_u32_e32 v14, s44, v191
	v_add_u32_e32 v30, s45, v191
	ds_read_b128 v[2:5], v14
	ds_read_b128 v[6:9], v14 offset:1024
	ds_read_b128 v[10:13], v14 offset:2048
	ds_read_b128 v[14:17], v14 offset:3072
	ds_read_b128 v[18:21], v30
	ds_read_b128 v[22:25], v30 offset:1024
	ds_read_b128 v[26:29], v30 offset:2048
	ds_read_b128 v[30:33], v30 offset:3072
	s_add_u32 s42, s42, 0x40000
	s_addc_u32 s43, s43, 0
	s_mov_b32 m0, s49
	v_lshl_add_u64 v[230:231], s[42:43], 0, v[166:167]
	ds_read_b128 v[198:201], v196 offset:32768
	ds_read_b128 v[202:205], v196 offset:33792
	ds_read_b128 v[206:209], v196 offset:34816
	ds_read_b128 v[210:213], v196 offset:35840
	ds_read_b128 v[214:217], v196 offset:36864
	ds_read_b128 v[218:221], v196 offset:37888
	ds_read_b128 v[222:225], v196 offset:38912
	ds_read_b128 v[226:229], v196 offset:39936
	global_load_lds_dwordx4 v[230:231], off
	v_lshl_add_u64 v[230:231], s[42:43], 0, v[168:169]
	s_mov_b32 m0, s52
	s_nop 0
	global_load_lds_dwordx4 v[230:231], off
	s_waitcnt vmcnt(8) lgkmcnt(0)
	s_barrier
	s_setprio 1
	v_mfma_scale_f32_16x16x128_f8f6f4 v[158:161], v[2:9], v[198:205], v[158:161], v1, v1 op_sel_hi:[0,0,0]
	v_mfma_scale_f32_16x16x128_f8f6f4 v[154:157], v[10:17], v[198:205], v[154:157], v1, v1 op_sel_hi:[0,0,0]
	v_mfma_scale_f32_16x16x128_f8f6f4 v[150:153], v[2:9], v[206:213], v[150:153], v1, v1 op_sel_hi:[0,0,0]
	v_mfma_scale_f32_16x16x128_f8f6f4 v[142:145], v[10:17], v[206:213], v[142:145], v1, v1 op_sel_hi:[0,0,0]
	v_mfma_scale_f32_16x16x128_f8f6f4 v[134:137], v[2:9], v[214:221], v[134:137], v1, v1 op_sel_hi:[0,0,0]
	v_mfma_scale_f32_16x16x128_f8f6f4 v[126:129], v[10:17], v[214:221], v[126:129], v1, v1 op_sel_hi:[0,0,0]
	v_mfma_scale_f32_16x16x128_f8f6f4 v[118:121], v[2:9], v[222:229], v[118:121], v1, v1 op_sel_hi:[0,0,0]
	v_mfma_scale_f32_16x16x128_f8f6f4 v[110:113], v[10:17], v[222:229], v[110:113], v1, v1 op_sel_hi:[0,0,0]
	v_mfma_scale_f32_16x16x128_f8f6f4 v[146:149], v[18:25], v[198:205], v[146:149], v1, v1 op_sel_hi:[0,0,0]
	v_mfma_scale_f32_16x16x128_f8f6f4 v[138:141], v[26:33], v[198:205], v[138:141], v1, v1 op_sel_hi:[0,0,0]
	v_mfma_scale_f32_16x16x128_f8f6f4 v[130:133], v[18:25], v[206:213], v[130:133], v1, v1 op_sel_hi:[0,0,0]
	v_mfma_scale_f32_16x16x128_f8f6f4 v[122:125], v[26:33], v[206:213], v[122:125], v1, v1 op_sel_hi:[0,0,0]
	v_mfma_scale_f32_16x16x128_f8f6f4 v[114:117], v[18:25], v[214:221], v[114:117], v1, v1 op_sel_hi:[0,0,0]
	v_mfma_scale_f32_16x16x128_f8f6f4 v[106:109], v[26:33], v[214:221], v[106:109], v1, v1 op_sel_hi:[0,0,0]
	v_mfma_scale_f32_16x16x128_f8f6f4 v[102:105], v[18:25], v[222:229], v[102:105], v1, v1 op_sel_hi:[0,0,0]
	v_mfma_scale_f32_16x16x128_f8f6f4 v[98:101], v[26:33], v[222:229], v[98:101], v1, v1 op_sel_hi:[0,0,0]
	s_setprio 0
	s_barrier
	s_add_i32 s42, s44, s46
	v_lshl_add_u64 v[182:183], v[182:183], 0, s[10:11]
	s_mov_b32 m0, s42
	ds_read_b128 v[198:201], v196 offset:49152
	ds_read_b128 v[202:205], v196 offset:50176
	ds_read_b128 v[206:209], v196 offset:51200
	ds_read_b128 v[210:213], v196 offset:52224
	ds_read_b128 v[214:217], v196 offset:53248
	ds_read_b128 v[218:221], v196 offset:54272
	ds_read_b128 v[222:225], v196 offset:55296
	ds_read_b128 v[226:229], v196 offset:56320
	global_load_lds_dwordx4 v[182:183], off
	s_add_i32 m0, s42, 0x2000
	s_add_u32 s40, s40, 0x40080
	v_lshl_add_u64 v[182:183], v[184:185], 0, s[10:11]
	s_addc_u32 s41, s41, 0
	s_add_i32 s42, s45, s46
	global_load_lds_dwordx4 v[182:183], off
	v_lshl_add_u64 v[182:183], s[40:41], 0, v[162:163]
	s_mov_b32 m0, s42
	s_nop 0
	global_load_lds_dwordx4 v[182:183], off
	v_lshl_add_u64 v[182:183], s[40:41], 0, v[164:165]
	s_add_i32 m0, s42, 0x2000
	s_nop 0
	global_load_lds_dwordx4 v[182:183], off
	v_lshl_add_u64 v[182:183], v[186:187], 0, s[10:11]
	s_mov_b32 m0, s54
	s_nop 0
	global_load_lds_dwordx4 v[182:183], off
	v_lshl_add_u64 v[182:183], v[188:189], 0, s[10:11]
	s_mov_b32 m0, s55
	s_nop 0
	global_load_lds_dwordx4 v[182:183], off
	s_waitcnt vmcnt(8) lgkmcnt(0)
	s_barrier
	s_setprio 1
	v_mfma_scale_f32_16x16x128_f8f6f4 v[94:97], v[2:9], v[198:205], v[94:97], v1, v1 op_sel_hi:[0,0,0]
	v_mfma_scale_f32_16x16x128_f8f6f4 v[90:93], v[10:17], v[198:205], v[90:93], v1, v1 op_sel_hi:[0,0,0]
	v_mfma_scale_f32_16x16x128_f8f6f4 v[86:89], v[2:9], v[206:213], v[86:89], v1, v1 op_sel_hi:[0,0,0]
	v_mfma_scale_f32_16x16x128_f8f6f4 v[78:81], v[10:17], v[206:213], v[78:81], v1, v1 op_sel_hi:[0,0,0]
	v_mfma_scale_f32_16x16x128_f8f6f4 v[62:65], v[2:9], v[214:221], v[62:65], v1, v1 op_sel_hi:[0,0,0]
	v_mfma_scale_f32_16x16x128_f8f6f4 v[54:57], v[10:17], v[214:221], v[54:57], v1, v1 op_sel_hi:[0,0,0]
	v_mfma_scale_f32_16x16x128_f8f6f4 v[46:49], v[2:9], v[222:229], v[46:49], v1, v1 op_sel_hi:[0,0,0]
	v_mfma_scale_f32_16x16x128_f8f6f4 v[38:41], v[10:17], v[222:229], v[38:41], v1, v1 op_sel_hi:[0,0,0]
	v_mfma_scale_f32_16x16x128_f8f6f4 v[82:85], v[18:25], v[198:205], v[82:85], v1, v1 op_sel_hi:[0,0,0]
	v_mfma_scale_f32_16x16x128_f8f6f4 v[74:77], v[26:33], v[198:205], v[74:77], v1, v1 op_sel_hi:[0,0,0]
	v_mfma_scale_f32_16x16x128_f8f6f4 v[58:61], v[18:25], v[206:213], v[58:61], v1, v1 op_sel_hi:[0,0,0]
	v_mfma_scale_f32_16x16x128_f8f6f4 v[50:53], v[26:33], v[206:213], v[50:53], v1, v1 op_sel_hi:[0,0,0]
	v_mfma_scale_f32_16x16x128_f8f6f4 v[42:45], v[18:25], v[214:221], v[42:45], v1, v1 op_sel_hi:[0,0,0]
	v_mfma_scale_f32_16x16x128_f8f6f4 v[34:37], v[26:33], v[214:221], v[34:37], v1, v1 op_sel_hi:[0,0,0]
	v_mfma_scale_f32_16x16x128_f8f6f4 v[70:73], v[18:25], v[222:229], v[70:73], v1, v1 op_sel_hi:[0,0,0]
	v_mfma_scale_f32_16x16x128_f8f6f4 v[66:69], v[26:33], v[222:229], v[66:69], v1, v1 op_sel_hi:[0,0,0]
	s_setprio 0
	s_barrier
	s_add_i32 s70, s70, 2
	s_cmp_gt_u32 s70, 13
	s_mov_b64 s[42:43], s[38:39]
	s_cbranch_scc0 .LBB0_2108
	s_and_b64 vcc, exec, s[12:13]
	s_cbranch_vccz .LBB0_2111
	s_barrier

; #define PG8_STAGE(bufoff, gbase, voff) do { _Pragma("unroll") for (int _i = 0; _i < 2; ++_i) \
;         __builtin_amdgcn_global_load_lds((const unsigned*)((const char*)(gbase) + (voff)[_i]), (LAS unsigned*)(lds + (bufoff) + ldsw + _i * 8192), 16, 0, 0); } while (0)
; #define PG8_LDA(dst, b, h) do { _Pragma("unroll") for (int m = 0; m < 4; ++m) dst[m] = PG8_LD32(lds + PG8_SA(b, h) + aoff + m * 2048); } while (0)
; #define PG8_LDB(dst, b, h) do { _Pragma("unroll") for (int n = 0; n < 2; ++n) dst[n] = PG8_LD32(lds + PG8_SB(b, h) + boff + n * 2048); } while (0)
; #define PG8_WAIT_V(n) asm volatile("s_waitcnt vmcnt(" #n ")" ::: "memory")
; #define PG8_WAIT_L(n) asm volatile("s_waitcnt lgkmcnt(" #n ")" ::: "memory")
; #define PG8_BAR __builtin_amdgcn_s_barrier()
; #define PG8_SCHED __builtin_amdgcn_sched_barrier(0)
; #define PG8_STA(bufoff, nextflag, h, koff) do { if constexpr (Sched::GATHER) { unsigned _o[2]; _o[0] = (nextflag) ? nxtA[h][0] : curA[h][0]; _o[1] = (nextflag) ? nxtA[h][1] : curA[h][1]; PG8_STAGE(bufoff, Ab + (koff), _o); } \
;         else { PG8_STAGE(bufoff, ((nextflag) ? nA : cA) + (size_t)(h) * hstep + (koff), voffA); } } while (0)
; template <class Epi, class Sched, bool ALIGN_EPI, int DT>
; __device__ __forceinline__ void gemm_phase(LAS unsigned char* lds, const int KB, const Sched& S, const Epi& E) {
;     ...
;         for (int t = 0; t < nt; t += 2) {
;             const bool last = (t == nt - 2);
;             const size_t k1 = (size_t)(t + 1) * kstep, k2 = last ? 0 : (size_t)(t + 2) * kstep, k3 = k2 + kstep;
;             const char* b2 = last ? nB : cB + (size_t)(t + 2) * kstep; const char* b3 = b2 + kstep;
;             PG8_LDB(B0, 0, 0); PG8_LDB(B1, 0, 1); PG8_SCHED; PG8_LDA(At, 0, 0); PG8_STA(PG8_SA(1, 1), false, 1, k1);
;             PG8_WAIT_V(8); PG8_WAIT_L(0); PG8_BAR; PG8_MMA(0, 0, At, B0); PG8_MMA(0, 1, At, B1); PG8_BAR; PG8_SCHED;
;             PG8_LDA(At, 0, 1); PG8_STAGE(PG8_SB(0, 0), b2, voffB); PG8_STAGE(PG8_SB(0, 1), b2 + hstep, voffB); PG8_STA(PG8_SA(0, 0), last, 0, k2);
;             PG8_WAIT_V(8); PG8_WAIT_L(0); PG8_BAR; PG8_MMA(1, 0, At, B0); PG8_MMA(1, 1, At, B1); PG8_BAR; PG8_SCHED;
.LBB0_2294:
	v_add_u32_e32 v79, s65, v167
	ds_read_b128 v[142:145], v79
	ds_read_b128 v[156:159], v79 offset:1024
	ds_read_b128 v[178:181], v79 offset:2048
	ds_read_b128 v[182:185], v79 offset:3072
	v_add_u32_e32 v79, s66, v167
	ds_read_b128 v[186:189], v79
	ds_read_b128 v[190:193], v79 offset:1024
	ds_read_b128 v[196:199], v79 offset:2048
	ds_read_b128 v[200:203], v79 offset:3072
	s_add_u32 s40, s8, 0x100
	s_addc_u32 s41, s9, 0
	s_cmpk_eq_i32 s8, 0x700
	s_cselect_b64 vcc, -1, 0
	v_lshl_add_u64 v[160:161], v[88:89], 0, s[8:9]
	s_and_b64 s[76:77], vcc, exec
	v_cndmask_b32_e32 v161, v161, v155, vcc
	s_cselect_b32 s75, 0, s40
	v_cndmask_b32_e32 v160, v160, v154, vcc
	v_lshl_add_u64 v[236:237], v[140:141], 0, s[8:9]
	s_add_i32 m0, s42, 0xc000
	ds_read_b128 v[204:207], v169
	ds_read_b128 v[208:211], v169 offset:1024
	ds_read_b128 v[212:215], v169 offset:2048
	ds_read_b128 v[216:219], v169 offset:3072
	ds_read_b128 v[220:223], v169 offset:4096
	ds_read_b128 v[224:227], v169 offset:5120
	ds_read_b128 v[228:231], v169 offset:6144
	ds_read_b128 v[232:235], v169 offset:7168
	global_load_lds_dwordx4 v[236:237], off
	v_lshl_add_u64 v[236:237], v[138:139], 0, s[8:9]
	s_add_i32 m0, s42, 0xe000
	s_nop 0
	global_load_lds_dwordx4 v[236:237], off
	s_waitcnt vmcnt(8) lgkmcnt(0)
	s_barrier
	s_setprio 1
	v_mfma_i32_16x16x64_i8 v[134:137], v[142:145], v[204:207], v[134:137]
	v_mfma_i32_16x16x64_i8 v[126:129], v[178:181], v[204:207], v[126:129]
	v_mfma_i32_16x16x64_i8 v[118:121], v[142:145], v[212:215], v[118:121]
	v_mfma_i32_16x16x64_i8 v[110:113], v[178:181], v[212:215], v[110:113]
	v_mfma_i32_16x16x64_i8 v[102:105], v[142:145], v[220:223], v[102:105]
	v_mfma_i32_16x16x64_i8 v[94:97], v[178:181], v[220:223], v[94:97]
	v_mfma_i32_16x16x64_i8 v[82:85], v[142:145], v[228:231], v[82:85]
	v_mfma_i32_16x16x64_i8 v[70:73], v[178:181], v[228:231], v[70:73]
	v_mfma_i32_16x16x64_i8 v[134:137], v[156:159], v[208:211], v[134:137]
	v_mfma_i32_16x16x64_i8 v[126:129], v[182:185], v[208:211], v[126:129]
	v_mfma_i32_16x16x64_i8 v[118:121], v[156:159], v[216:219], v[118:121]
	v_mfma_i32_16x16x64_i8 v[110:113], v[182:185], v[216:219], v[110:113]
	v_mfma_i32_16x16x64_i8 v[102:105], v[156:159], v[224:227], v[102:105]
	v_mfma_i32_16x16x64_i8 v[94:97], v[182:185], v[224:227], v[94:97]
	v_mfma_i32_16x16x64_i8 v[82:85], v[156:159], v[232:235], v[82:85]
	v_mfma_i32_16x16x64_i8 v[70:73], v[182:185], v[232:235], v[70:73]
	v_mfma_i32_16x16x64_i8 v[130:133], v[186:189], v[204:207], v[130:133]
	v_mfma_i32_16x16x64_i8 v[122:125], v[196:199], v[204:207], v[122:125]
	v_mfma_i32_16x16x64_i8 v[114:117], v[186:189], v[212:215], v[114:117]
	v_mfma_i32_16x16x64_i8 v[106:109], v[196:199], v[212:215], v[106:109]
	v_mfma_i32_16x16x64_i8 v[98:101], v[186:189], v[220:223], v[98:101]
	v_mfma_i32_16x16x64_i8 v[90:93], v[196:199], v[220:223], v[90:93]
	v_mfma_i32_16x16x64_i8 v[74:77], v[186:189], v[228:231], v[74:77]
	v_mfma_i32_16x16x64_i8 v[66:69], v[196:199], v[228:231], v[66:69]
	v_mfma_i32_16x16x64_i8 v[130:133], v[190:193], v[208:211], v[130:133]
	v_mfma_i32_16x16x64_i8 v[122:125], v[200:203], v[208:211], v[122:125]
	v_mfma_i32_16x16x64_i8 v[114:117], v[190:193], v[216:219], v[114:117]
	v_mfma_i32_16x16x64_i8 v[106:109], v[200:203], v[216:219], v[106:109]
	v_mfma_i32_16x16x64_i8 v[98:101], v[190:193], v[224:227], v[98:101]
	v_mfma_i32_16x16x64_i8 v[90:93], v[200:203], v[224:227], v[90:93]
	v_mfma_i32_16x16x64_i8 v[74:77], v[190:193], v[232:235], v[74:77]
	v_mfma_i32_16x16x64_i8 v[66:69], v[200:203], v[232:235], v[66:69]
	s_setprio 0
	s_barrier
	s_add_i32 s8, s65, s33
	v_lshl_add_u64 v[236:237], v[160:161], 0, v[148:149]
	s_mov_b32 m0, s8
	ds_read_b128 v[204:207], v169 offset:16384
	ds_read_b128 v[208:211], v169 offset:17408
	ds_read_b128 v[212:215], v169 offset:18432
	ds_read_b128 v[216:219], v169 offset:19456
	ds_read_b128 v[220:223], v169 offset:20480
	ds_read_b128 v[224:227], v169 offset:21504
	ds_read_b128 v[228:231], v169 offset:22528
	ds_read_b128 v[232:235], v169 offset:23552
	global_load_lds_dwordx4 v[236:237], off
	v_lshl_add_u64 v[238:239], v[160:161], 0, v[150:151]
	s_add_i32 m0, s8, 0x2000
	v_lshl_add_u64 v[240:241], v[160:161], 0, s[10:11]
	s_add_i32 s8, s66, s33
	global_load_lds_dwordx4 v[238:239], off
	v_lshl_add_u64 v[242:243], v[240:241], 0, v[148:149]
	s_mov_b32 m0, s8
	v_lshl_add_u64 v[240:241], v[240:241], 0, v[150:151]
	global_load_lds_dwordx4 v[242:243], off
	s_add_i32 m0, s8, 0x2000
	s_add_u32 s8, s60, s75
	global_load_lds_dwordx4 v[240:241], off
	v_cndmask_b32_e32 v146, v81, v173, vcc
	s_addc_u32 s9, s61, 0
	s_mov_b32 m0, s42
	v_cndmask_b32_e32 v240, v80, v174, vcc
	global_load_lds_dwordx4 v146, s[8:9]
	s_mov_b32 m0, s43
	v_mov_b32_e32 v241, v147
	global_load_lds_dwordx4 v240, s[8:9]
	s_waitcnt vmcnt(8)
	s_waitcnt lgkmcnt(0)
	v_lshl_add_u64 v[242:243], s[8:9], 0, v[146:147]
	v_lshl_add_u64 v[240:241], s[8:9], 0, v[240:241]
	s_barrier
; #define PG8_LDA(dst, b, h) do { _Pragma("unroll") for (int m = 0; m < 4; ++m) dst[m] = PG8_LD32(lds + PG8_SA(b, h) + aoff + m * 2048); } while (0)
; #define PG8_LDB(dst, b, h) do { _Pragma("unroll") for (int n = 0; n < 2; ++n) dst[n] = PG8_LD32(lds + PG8_SB(b, h) + boff + n * 2048); } while (0)
; #define PG8_WAIT_V(n) asm volatile("s_waitcnt vmcnt(" #n ")" ::: "memory")
; #define PG8_WAIT_L(n) asm volatile("s_waitcnt lgkmcnt(" #n ")" ::: "memory")
; #define PG8_BAR __builtin_amdgcn_s_barrier()
; #define PG8_SCHED __builtin_amdgcn_sched_barrier(0)
; #define PG8_STA(bufoff, nextflag, h, koff) do { if constexpr (Sched::GATHER) { unsigned _o[2]; _o[0] = (nextflag) ? nxtA[h][0] : curA[h][0]; _o[1] = (nextflag) ? nxtA[h][1] : curA[h][1]; PG8_STAGE(bufoff, Ab + (koff), _o); } \
;         else { PG8_STAGE(bufoff, ((nextflag) ? nA : cA) + (size_t)(h) * hstep + (koff), voffA); } } while (0)
; template <class Epi, class Sched, bool ALIGN_EPI, int DT>
; __device__ __forceinline__ void gemm_phase(LAS unsigned char* lds, const int KB, const Sched& S, const Epi& E) {
;     ...
;             PG8_WAIT_V(8); PG8_WAIT_L(0); PG8_BAR; PG8_MMA(1, 0, At, B0); PG8_MMA(1, 1, At, B1); PG8_BAR; PG8_SCHED;
;             PG8_LDB(B0, 1, 0); PG8_LDB(B1, 1, 1); PG8_SCHED; PG8_LDA(At, 1, 0); PG8_STA(PG8_SA(0, 1), last, 1, k2);
;             PG8_WAIT_V(8); PG8_WAIT_L(0); PG8_BAR; PG8_MMA(0, 0, At, B0); PG8_MMA(0, 1, At, B1); PG8_BAR; PG8_SCHED;
	s_setprio 1
	v_mfma_i32_16x16x64_i8 v[54:57], v[142:145], v[204:207], v[54:57]
	v_mfma_i32_16x16x64_i8 v[50:53], v[178:181], v[204:207], v[50:53]
	v_mfma_i32_16x16x64_i8 v[42:45], v[142:145], v[212:215], v[42:45]
	v_mfma_i32_16x16x64_i8 v[34:37], v[178:181], v[212:215], v[34:37]
	v_mfma_i32_16x16x64_i8 v[26:29], v[142:145], v[220:223], v[26:29]
	v_mfma_i32_16x16x64_i8 v[18:21], v[178:181], v[220:223], v[18:21]
	v_mfma_i32_16x16x64_i8 v[10:13], v[142:145], v[228:231], v[10:13]
	v_mfma_i32_16x16x64_i8 v[2:5], v[178:181], v[228:231], v[2:5]
	v_mfma_i32_16x16x64_i8 v[54:57], v[156:159], v[208:211], v[54:57]
	v_mfma_i32_16x16x64_i8 v[50:53], v[182:185], v[208:211], v[50:53]
	v_mfma_i32_16x16x64_i8 v[42:45], v[156:159], v[216:219], v[42:45]
	v_mfma_i32_16x16x64_i8 v[34:37], v[182:185], v[216:219], v[34:37]
	v_mfma_i32_16x16x64_i8 v[26:29], v[156:159], v[224:227], v[26:29]
	v_mfma_i32_16x16x64_i8 v[18:21], v[182:185], v[224:227], v[18:21]
	v_mfma_i32_16x16x64_i8 v[10:13], v[156:159], v[232:235], v[10:13]
	v_mfma_i32_16x16x64_i8 v[2:5], v[182:185], v[232:235], v[2:5]
	v_mfma_i32_16x16x64_i8 v[62:65], v[186:189], v[204:207], v[62:65]
	v_mfma_i32_16x16x64_i8 v[58:61], v[196:199], v[204:207], v[58:61]
	v_mfma_i32_16x16x64_i8 v[46:49], v[186:189], v[212:215], v[46:49]
	v_mfma_i32_16x16x64_i8 v[38:41], v[196:199], v[212:215], v[38:41]
	v_mfma_i32_16x16x64_i8 v[30:33], v[186:189], v[220:223], v[30:33]
	v_mfma_i32_16x16x64_i8 v[22:25], v[196:199], v[220:223], v[22:25]
	v_mfma_i32_16x16x64_i8 v[14:17], v[186:189], v[228:231], v[14:17]
	v_mfma_i32_16x16x64_i8 v[6:9], v[196:199], v[228:231], v[6:9]
	v_mfma_i32_16x16x64_i8 v[62:65], v[190:193], v[208:211], v[62:65]
	v_mfma_i32_16x16x64_i8 v[58:61], v[200:203], v[208:211], v[58:61]
	v_mfma_i32_16x16x64_i8 v[46:49], v[190:193], v[216:219], v[46:49]
	v_mfma_i32_16x16x64_i8 v[38:41], v[200:203], v[216:219], v[38:41]
	v_mfma_i32_16x16x64_i8 v[30:33], v[190:193], v[224:227], v[30:33]
	v_mfma_i32_16x16x64_i8 v[22:25], v[200:203], v[224:227], v[22:25]
	v_mfma_i32_16x16x64_i8 v[14:17], v[190:193], v[232:235], v[14:17]
	v_mfma_i32_16x16x64_i8 v[6:9], v[200:203], v[232:235], v[6:9]
	s_setprio 0
	s_barrier
	s_add_i32 s75, 0, 0x18000
	v_add_u32_e32 v79, s75, v167
	s_add_i32 s76, 0, 0x1c000
	ds_read_b128 v[142:145], v79
	ds_read_b128 v[156:159], v79 offset:1024
	ds_read_b128 v[178:181], v79 offset:2048
	ds_read_b128 v[182:185], v79 offset:3072
	v_add_u32_e32 v79, s76, v167
	ds_read_b128 v[186:189], v79
	ds_read_b128 v[190:193], v79 offset:1024
	ds_read_b128 v[196:199], v79 offset:2048
	ds_read_b128 v[200:203], v79 offset:3072
	s_mov_b32 m0, s44
	v_cndmask_b32_e32 v79, v78, v175, vcc
	ds_read_b128 v[204:207], v169 offset:32768
	ds_read_b128 v[208:211], v169 offset:33792
	ds_read_b128 v[212:215], v169 offset:34816
	ds_read_b128 v[216:219], v169 offset:35840
	ds_read_b128 v[220:223], v169 offset:36864
	ds_read_b128 v[224:227], v169 offset:37888
	ds_read_b128 v[228:231], v169 offset:38912
	ds_read_b128 v[232:235], v169 offset:39936
	v_cndmask_b32_e32 v87, v86, v176, vcc
	global_load_lds_dwordx4 v79, s[8:9]
	s_mov_b32 m0, s45
	s_nop 0
	global_load_lds_dwordx4 v87, s[8:9]
	s_waitcnt vmcnt(8) lgkmcnt(0)
	s_barrier
	s_setprio 1
	v_mfma_i32_16x16x64_i8 v[134:137], v[142:145], v[204:207], v[134:137]
	v_mfma_i32_16x16x64_i8 v[126:129], v[178:181], v[204:207], v[126:129]
	v_mfma_i32_16x16x64_i8 v[118:121], v[142:145], v[212:215], v[118:121]
	v_mfma_i32_16x16x64_i8 v[110:113], v[178:181], v[212:215], v[110:113]
	v_mfma_i32_16x16x64_i8 v[102:105], v[142:145], v[220:223], v[102:105]
	v_mfma_i32_16x16x64_i8 v[94:97], v[178:181], v[220:223], v[94:97]
	v_mfma_i32_16x16x64_i8 v[82:85], v[142:145], v[228:231], v[82:85]
	v_mfma_i32_16x16x64_i8 v[70:73], v[178:181], v[228:231], v[70:73]
	v_mfma_i32_16x16x64_i8 v[134:137], v[156:159], v[208:211], v[134:137]
	v_mfma_i32_16x16x64_i8 v[126:129], v[182:185], v[208:211], v[126:129]
	v_mfma_i32_16x16x64_i8 v[118:121], v[156:159], v[216:219], v[118:121]
	v_mfma_i32_16x16x64_i8 v[110:113], v[182:185], v[216:219], v[110:113]
	v_mfma_i32_16x16x64_i8 v[102:105], v[156:159], v[224:227], v[102:105]
	v_mfma_i32_16x16x64_i8 v[94:97], v[182:185], v[224:227], v[94:97]
	v_mfma_i32_16x16x64_i8 v[82:85], v[156:159], v[232:235], v[82:85]
	v_mfma_i32_16x16x64_i8 v[70:73], v[182:185], v[232:235], v[70:73]
	v_mfma_i32_16x16x64_i8 v[130:133], v[186:189], v[204:207], v[130:133]
	v_mfma_i32_16x16x64_i8 v[122:125], v[196:199], v[204:207], v[122:125]
	v_mfma_i32_16x16x64_i8 v[114:117], v[186:189], v[212:215], v[114:117]
	v_mfma_i32_16x16x64_i8 v[106:109], v[196:199], v[212:215], v[106:109]
	v_mfma_i32_16x16x64_i8 v[98:101], v[186:189], v[220:223], v[98:101]
	v_mfma_i32_16x16x64_i8 v[90:93], v[196:199], v[220:223], v[90:93]
	v_mfma_i32_16x16x64_i8 v[74:77], v[186:189], v[228:231], v[74:77]
	v_mfma_i32_16x16x64_i8 v[66:69], v[196:199], v[228:231], v[66:69]
	v_mfma_i32_16x16x64_i8 v[130:133], v[190:193], v[208:211], v[130:133]
	v_mfma_i32_16x16x64_i8 v[122:125], v[200:203], v[208:211], v[122:125]
	v_mfma_i32_16x16x64_i8 v[114:117], v[190:193], v[216:219], v[114:117]
	v_mfma_i32_16x16x64_i8 v[106:109], v[200:203], v[216:219], v[106:109]
	v_mfma_i32_16x16x64_i8 v[98:101], v[190:193], v[224:227], v[98:101]
	v_mfma_i32_16x16x64_i8 v[90:93], v[200:203], v[224:227], v[90:93]
	v_mfma_i32_16x16x64_i8 v[74:77], v[190:193], v[232:235], v[74:77]
	v_mfma_i32_16x16x64_i8 v[66:69], v[200:203], v[232:235], v[66:69]
	s_setprio 0
	s_barrier
; #define PG8_STAGE(bufoff, gbase, voff) do { _Pragma("unroll") for (int _i = 0; _i < 2; ++_i) \
;         __builtin_amdgcn_global_load_lds((const unsigned*)((const char*)(gbase) + (voff)[_i]), (LAS unsigned*)(lds + (bufoff) + ldsw + _i * 8192), 16, 0, 0); } while (0)
; #define PG8_LDA(dst, b, h) do { _Pragma("unroll") for (int m = 0; m < 4; ++m) dst[m] = PG8_LD32(lds + PG8_SA(b, h) + aoff + m * 2048); } while (0)
; #define PG8_WAIT_V(n) asm volatile("s_waitcnt vmcnt(" #n ")" ::: "memory")
; #define PG8_WAIT_L(n) asm volatile("s_waitcnt lgkmcnt(" #n ")" ::: "memory")
; #define PG8_BAR __builtin_amdgcn_s_barrier()
; #define PG8_SCHED __builtin_amdgcn_sched_barrier(0)
; #define PG8_STA(bufoff, nextflag, h, koff) do { if constexpr (Sched::GATHER) { unsigned _o[2]; _o[0] = (nextflag) ? nxtA[h][0] : curA[h][0]; _o[1] = (nextflag) ? nxtA[h][1] : curA[h][1]; PG8_STAGE(bufoff, Ab + (koff), _o); } \
;         else { PG8_STAGE(bufoff, ((nextflag) ? nA : cA) + (size_t)(h) * hstep + (koff), voffA); } } while (0)
; template <class Epi, class Sched, bool ALIGN_EPI, int DT>
; __device__ __forceinline__ void gemm_phase(LAS unsigned char* lds, const int KB, const Sched& S, const Epi& E) {
;     ...
;             PG8_LDA(At, 1, 1); PG8_STAGE(PG8_SB(1, 0), b3, voffB); PG8_STAGE(PG8_SB(1, 1), b3 + hstep, voffB); PG8_STA(PG8_SA(1, 0), last, 0, k3);
;             PG8_WAIT_V(8); PG8_WAIT_L(0); PG8_BAR; PG8_MMA(1, 0, At, B0); PG8_MMA(1, 1, At, B1); PG8_BAR; PG8_SCHED;
;         }
;         if constexpr (ALIGN_EPI) { if (wr == 0) PG8_BAR; }
	s_add_i32 s8, s75, s33
	v_lshl_add_u64 v[236:237], v[236:237], 0, s[20:21]
	s_mov_b32 m0, s8
	ds_read_b128 v[204:207], v169 offset:49152
	ds_read_b128 v[208:211], v169 offset:50176
	ds_read_b128 v[212:215], v169 offset:51200
	ds_read_b128 v[216:219], v169 offset:52224
	ds_read_b128 v[220:223], v169 offset:53248
	ds_read_b128 v[224:227], v169 offset:54272
	ds_read_b128 v[228:231], v169 offset:55296
	ds_read_b128 v[232:235], v169 offset:56320
	global_load_lds_dwordx4 v[236:237], off
	v_lshl_add_u64 v[236:237], v[238:239], 0, s[20:21]
	s_add_i32 m0, s8, 0x2000
	v_lshl_add_u64 v[160:161], v[160:161], 0, s[24:25]
	s_add_i32 s8, s76, s33
	global_load_lds_dwordx4 v[236:237], off
	v_lshl_add_u64 v[236:237], v[160:161], 0, v[148:149]
	s_mov_b32 m0, s8
	v_lshl_add_u64 v[160:161], v[160:161], 0, v[150:151]
	global_load_lds_dwordx4 v[236:237], off
	s_add_i32 m0, s8, 0x2000
	s_nop 0
	global_load_lds_dwordx4 v[160:161], off
	v_lshl_add_u64 v[160:161], v[242:243], 0, s[20:21]
	s_mov_b32 m0, s46
	s_nop 0
	global_load_lds_dwordx4 v[160:161], off
	v_lshl_add_u64 v[160:161], v[240:241], 0, s[20:21]
	s_mov_b32 m0, s47
	s_nop 0
	global_load_lds_dwordx4 v[160:161], off
	s_waitcnt vmcnt(8) lgkmcnt(0)
	s_barrier
	s_setprio 1
	v_mfma_i32_16x16x64_i8 v[54:57], v[142:145], v[204:207], v[54:57]
	v_mfma_i32_16x16x64_i8 v[50:53], v[178:181], v[204:207], v[50:53]
	v_mfma_i32_16x16x64_i8 v[42:45], v[142:145], v[212:215], v[42:45]
	v_mfma_i32_16x16x64_i8 v[34:37], v[178:181], v[212:215], v[34:37]
	v_mfma_i32_16x16x64_i8 v[26:29], v[142:145], v[220:223], v[26:29]
	v_mfma_i32_16x16x64_i8 v[18:21], v[178:181], v[220:223], v[18:21]
	v_mfma_i32_16x16x64_i8 v[10:13], v[142:145], v[228:231], v[10:13]
	v_mfma_i32_16x16x64_i8 v[2:5], v[178:181], v[228:231], v[2:5]
	v_mfma_i32_16x16x64_i8 v[54:57], v[156:159], v[208:211], v[54:57]
	v_mfma_i32_16x16x64_i8 v[50:53], v[182:185], v[208:211], v[50:53]
	v_mfma_i32_16x16x64_i8 v[42:45], v[156:159], v[216:219], v[42:45]
	v_mfma_i32_16x16x64_i8 v[34:37], v[182:185], v[216:219], v[34:37]
	v_mfma_i32_16x16x64_i8 v[26:29], v[156:159], v[224:227], v[26:29]
	v_mfma_i32_16x16x64_i8 v[18:21], v[182:185], v[224:227], v[18:21]
	v_mfma_i32_16x16x64_i8 v[10:13], v[156:159], v[232:235], v[10:13]
	v_mfma_i32_16x16x64_i8 v[2:5], v[182:185], v[232:235], v[2:5]
	v_mfma_i32_16x16x64_i8 v[62:65], v[186:189], v[204:207], v[62:65]
	v_mfma_i32_16x16x64_i8 v[58:61], v[196:199], v[204:207], v[58:61]
	v_mfma_i32_16x16x64_i8 v[46:49], v[186:189], v[212:215], v[46:49]
	v_mfma_i32_16x16x64_i8 v[38:41], v[196:199], v[212:215], v[38:41]
	v_mfma_i32_16x16x64_i8 v[30:33], v[186:189], v[220:223], v[30:33]
	v_mfma_i32_16x16x64_i8 v[22:25], v[196:199], v[220:223], v[22:25]
	v_mfma_i32_16x16x64_i8 v[14:17], v[186:189], v[228:231], v[14:17]
	v_mfma_i32_16x16x64_i8 v[6:9], v[196:199], v[228:231], v[6:9]
	v_mfma_i32_16x16x64_i8 v[62:65], v[190:193], v[208:211], v[62:65]
	v_mfma_i32_16x16x64_i8 v[58:61], v[200:203], v[208:211], v[58:61]
	v_mfma_i32_16x16x64_i8 v[46:49], v[190:193], v[216:219], v[46:49]
	v_mfma_i32_16x16x64_i8 v[38:41], v[200:203], v[216:219], v[38:41]
	v_mfma_i32_16x16x64_i8 v[30:33], v[190:193], v[224:227], v[30:33]
	v_mfma_i32_16x16x64_i8 v[22:25], v[200:203], v[224:227], v[22:25]
	v_mfma_i32_16x16x64_i8 v[14:17], v[190:193], v[232:235], v[14:17]
	v_mfma_i32_16x16x64_i8 v[6:9], v[200:203], v[232:235], v[6:9]
	s_setprio 0
	s_barrier
	s_add_i32 s37, s37, 2
	s_cmp_gt_u32 s37, 13
	s_mov_b64 s[8:9], s[40:41]
	s_cbranch_scc0 .LBB0_2294
	s_and_b64 vcc, exec, s[26:27]
	s_cbranch_vccz .LBB0_2297
	s_barrier

; #define PG8_STAGE(bufoff, gbase, voff) do { _Pragma("unroll") for (int _i = 0; _i < 2; ++_i) \
;         __builtin_amdgcn_global_load_lds((const unsigned*)((const char*)(gbase) + (voff)[_i]), (LAS unsigned*)(lds + (bufoff) + ldsw + _i * 8192), 16, 0, 0); } while (0)
; #define PG8_LDA(dst, b, h) do { _Pragma("unroll") for (int m = 0; m < 4; ++m) dst[m] = PG8_LD32(lds + PG8_SA(b, h) + aoff + m * 2048); } while (0)
; #define PG8_LDB(dst, b, h) do { _Pragma("unroll") for (int n = 0; n < 2; ++n) dst[n] = PG8_LD32(lds + PG8_SB(b, h) + boff + n * 2048); } while (0)
; #define PG8_WAIT_V(n) asm volatile("s_waitcnt vmcnt(" #n ")" ::: "memory")
; #define PG8_WAIT_L(n) asm volatile("s_waitcnt lgkmcnt(" #n ")" ::: "memory")
; #define PG8_BAR __builtin_amdgcn_s_barrier()
; #define PG8_SCHED __builtin_amdgcn_sched_barrier(0)
; #define PG8_STA(bufoff, nextflag, h, koff) do { if constexpr (Sched::GATHER) { unsigned _o[2]; _o[0] = (nextflag) ? nxtA[h][0] : curA[h][0]; _o[1] = (nextflag) ? nxtA[h][1] : curA[h][1]; PG8_STAGE(bufoff, Ab + (koff), _o); } \
;         else { PG8_STAGE(bufoff, ((nextflag) ? nA : cA) + (size_t)(h) * hstep + (koff), voffA); } } while (0)
; template <class Epi, class Sched, bool ALIGN_EPI, int DT>
; __device__ __forceinline__ void gemm_phase(LAS unsigned char* lds, const int KB, const Sched& S, const Epi& E) {
;     ...
;         for (int t = 0; t < nt; t += 2) {
;             const bool last = (t == nt - 2);
;             const size_t k1 = (size_t)(t + 1) * kstep, k2 = last ? 0 : (size_t)(t + 2) * kstep, k3 = k2 + kstep;
;             const char* b2 = last ? nB : cB + (size_t)(t + 2) * kstep; const char* b3 = b2 + kstep;
;             PG8_LDB(B0, 0, 0); PG8_LDB(B1, 0, 1); PG8_SCHED; PG8_LDA(At, 0, 0); PG8_STA(PG8_SA(1, 1), false, 1, k1);
;             PG8_WAIT_V(8); PG8_WAIT_L(0); PG8_BAR; PG8_MMA(0, 0, At, B0); PG8_MMA(0, 1, At, B1); PG8_BAR; PG8_SCHED;
;             PG8_LDA(At, 0, 1); PG8_STAGE(PG8_SB(0, 0), b2, voffB); PG8_STAGE(PG8_SB(0, 1), b2 + hstep, voffB); PG8_STA(PG8_SA(0, 0), last, 0, k2);
;             PG8_WAIT_V(8); PG8_WAIT_L(0); PG8_BAR; PG8_MMA(1, 0, At, B0); PG8_MMA(1, 1, At, B1); PG8_BAR; PG8_SCHED;
.LBB0_2387:
	ds_read_b128 v[18:21], v198
	ds_read_b128 v[22:25], v198 offset:1024
	ds_read_b128 v[26:29], v198 offset:2048
	ds_read_b128 v[30:33], v198 offset:3072
	ds_read_b128 v[2:5], v199
	ds_read_b128 v[6:9], v199 offset:1024
	ds_read_b128 v[10:13], v199 offset:2048
	ds_read_b128 v[14:17], v199 offset:3072
	s_add_u32 s42, s44, 0x100
	s_addc_u32 s43, s45, 0
	s_add_i32 s76, s63, s4
	s_add_i32 m0, s33, 0xc000
	s_add_i32 s77, s33, 0xe000
	s_add_i32 s74, s76, 0x2000
	s_cmp_eq_u32 s71, 18
	v_lshl_add_u64 v[184:185], v[178:179], 0, s[44:45]
	s_cselect_b64 vcc, -1, 0
	s_cselect_b32 s75, 0, s42
	v_cndmask_b32_e32 v185, v185, v177, vcc
	v_cndmask_b32_e32 v184, v184, v176, vcc
	v_lshl_add_u64 v[226:227], v[180:181], 0, s[44:45]
	ds_read_b128 v[186:189], v200
	ds_read_b128 v[190:193], v200 offset:1024
	ds_read_b128 v[202:205], v200 offset:2048
	ds_read_b128 v[206:209], v200 offset:3072
	ds_read_b128 v[210:213], v200 offset:4096
	ds_read_b128 v[214:217], v200 offset:5120
	ds_read_b128 v[218:221], v200 offset:6144
	ds_read_b128 v[222:225], v200 offset:7168
	global_load_lds_dwordx4 v[226:227], off
	v_lshl_add_u64 v[226:227], v[182:183], 0, s[44:45]
	s_mov_b32 m0, s77
	s_nop 0
	global_load_lds_dwordx4 v[226:227], off
	s_waitcnt vmcnt(8) lgkmcnt(0)
	s_barrier
	s_setprio 1
	v_mfma_scale_f32_16x16x128_f8f6f4 v[158:161], v[18:25], v[186:193], v[158:161], v1, v1 op_sel_hi:[0,0,0]
	v_mfma_scale_f32_16x16x128_f8f6f4 v[154:157], v[26:33], v[186:193], v[154:157], v1, v1 op_sel_hi:[0,0,0]
	v_mfma_scale_f32_16x16x128_f8f6f4 v[150:153], v[18:25], v[202:209], v[150:153], v1, v1 op_sel_hi:[0,0,0]
	v_mfma_scale_f32_16x16x128_f8f6f4 v[142:145], v[26:33], v[202:209], v[142:145], v1, v1 op_sel_hi:[0,0,0]
	v_mfma_scale_f32_16x16x128_f8f6f4 v[134:137], v[18:25], v[210:217], v[134:137], v1, v1 op_sel_hi:[0,0,0]
	v_mfma_scale_f32_16x16x128_f8f6f4 v[126:129], v[26:33], v[210:217], v[126:129], v1, v1 op_sel_hi:[0,0,0]
	v_mfma_scale_f32_16x16x128_f8f6f4 v[118:121], v[18:25], v[218:225], v[118:121], v1, v1 op_sel_hi:[0,0,0]
	v_mfma_scale_f32_16x16x128_f8f6f4 v[110:113], v[26:33], v[218:225], v[110:113], v1, v1 op_sel_hi:[0,0,0]
	v_mfma_scale_f32_16x16x128_f8f6f4 v[146:149], v[2:9], v[186:193], v[146:149], v1, v1 op_sel_hi:[0,0,0]
	v_mfma_scale_f32_16x16x128_f8f6f4 v[138:141], v[10:17], v[186:193], v[138:141], v1, v1 op_sel_hi:[0,0,0]
	v_mfma_scale_f32_16x16x128_f8f6f4 v[130:133], v[2:9], v[202:209], v[130:133], v1, v1 op_sel_hi:[0,0,0]
	v_mfma_scale_f32_16x16x128_f8f6f4 v[122:125], v[10:17], v[202:209], v[122:125], v1, v1 op_sel_hi:[0,0,0]
	v_mfma_scale_f32_16x16x128_f8f6f4 v[114:117], v[2:9], v[210:217], v[114:117], v1, v1 op_sel_hi:[0,0,0]
	v_mfma_scale_f32_16x16x128_f8f6f4 v[106:109], v[10:17], v[210:217], v[106:109], v1, v1 op_sel_hi:[0,0,0]
	v_mfma_scale_f32_16x16x128_f8f6f4 v[102:105], v[2:9], v[218:225], v[102:105], v1, v1 op_sel_hi:[0,0,0]
	v_mfma_scale_f32_16x16x128_f8f6f4 v[98:101], v[10:17], v[218:225], v[98:101], v1, v1 op_sel_hi:[0,0,0]
	s_setprio 0
	s_barrier
	s_mov_b32 m0, s76
	v_lshl_add_u64 v[188:189], v[184:185], 0, v[170:171]
	ds_read_b128 v[202:205], v200 offset:16384
	ds_read_b128 v[206:209], v200 offset:17408
	ds_read_b128 v[210:213], v200 offset:18432
	ds_read_b128 v[214:217], v200 offset:19456
	ds_read_b128 v[218:221], v200 offset:20480
	ds_read_b128 v[222:225], v200 offset:21504
	ds_read_b128 v[226:229], v200 offset:22528
	ds_read_b128 v[230:233], v200 offset:23552
	global_load_lds_dwordx4 v[188:189], off
	v_lshl_add_u64 v[186:187], v[184:185], 0, v[164:165]
	s_mov_b32 m0, s74
	s_cselect_b32 s45, s9, s41
	s_cselect_b32 s44, s8, s40
	v_lshl_add_u64 v[190:191], v[184:185], 0, s[12:13]
	s_add_i32 s74, s64, s4
	global_load_lds_dwordx4 v[186:187], off
	v_lshl_add_u64 v[192:193], v[190:191], 0, v[170:171]
	s_mov_b32 m0, s74
	v_lshl_add_u64 v[190:191], v[190:191], 0, v[164:165]
	global_load_lds_dwordx4 v[192:193], off
	s_add_i32 m0, s74, 0x2000
	s_add_u32 s44, s44, s75
	s_addc_u32 s45, s45, 0
	global_load_lds_dwordx4 v[190:191], off
	v_lshl_add_u64 v[190:191], s[44:45], 0, v[166:167]
	s_mov_b32 m0, s33
	v_lshl_add_u64 v[192:193], s[44:45], 0, v[168:169]
	global_load_lds_dwordx4 v[190:191], off
	s_mov_b32 m0, s39
	s_nop 0
	global_load_lds_dwordx4 v[192:193], off
	s_waitcnt vmcnt(8) lgkmcnt(0)
	s_barrier
	s_setprio 1
	v_mfma_scale_f32_16x16x128_f8f6f4 v[94:97], v[18:25], v[202:209], v[94:97], v1, v1 op_sel_hi:[0,0,0]
	v_mfma_scale_f32_16x16x128_f8f6f4 v[90:93], v[26:33], v[202:209], v[90:93], v1, v1 op_sel_hi:[0,0,0]
	v_mfma_scale_f32_16x16x128_f8f6f4 v[86:89], v[18:25], v[210:217], v[86:89], v1, v1 op_sel_hi:[0,0,0]
	v_mfma_scale_f32_16x16x128_f8f6f4 v[78:81], v[26:33], v[210:217], v[78:81], v1, v1 op_sel_hi:[0,0,0]
	v_mfma_scale_f32_16x16x128_f8f6f4 v[62:65], v[18:25], v[218:225], v[62:65], v1, v1 op_sel_hi:[0,0,0]
	v_mfma_scale_f32_16x16x128_f8f6f4 v[54:57], v[26:33], v[218:225], v[54:57], v1, v1 op_sel_hi:[0,0,0]
	v_mfma_scale_f32_16x16x128_f8f6f4 v[46:49], v[18:25], v[226:233], v[46:49], v1, v1 op_sel_hi:[0,0,0]
	v_mfma_scale_f32_16x16x128_f8f6f4 v[38:41], v[26:33], v[226:233], v[38:41], v1, v1 op_sel_hi:[0,0,0]
	v_mfma_scale_f32_16x16x128_f8f6f4 v[82:85], v[2:9], v[202:209], v[82:85], v1, v1 op_sel_hi:[0,0,0]
	v_mfma_scale_f32_16x16x128_f8f6f4 v[74:77], v[10:17], v[202:209], v[74:77], v1, v1 op_sel_hi:[0,0,0]
	v_mfma_scale_f32_16x16x128_f8f6f4 v[58:61], v[2:9], v[210:217], v[58:61], v1, v1 op_sel_hi:[0,0,0]
	v_mfma_scale_f32_16x16x128_f8f6f4 v[50:53], v[10:17], v[210:217], v[50:53], v1, v1 op_sel_hi:[0,0,0]
	v_mfma_scale_f32_16x16x128_f8f6f4 v[42:45], v[2:9], v[218:225], v[42:45], v1, v1 op_sel_hi:[0,0,0]
	v_mfma_scale_f32_16x16x128_f8f6f4 v[34:37], v[10:17], v[218:225], v[34:37], v1, v1 op_sel_hi:[0,0,0]
	v_mfma_scale_f32_16x16x128_f8f6f4 v[70:73], v[2:9], v[226:233], v[70:73], v1, v1 op_sel_hi:[0,0,0]
	v_mfma_scale_f32_16x16x128_f8f6f4 v[66:69], v[10:17], v[226:233], v[66:69], v1, v1 op_sel_hi:[0,0,0]
	s_setprio 0
	s_barrier
; #define PG8_STAGE(bufoff, gbase, voff) do { _Pragma("unroll") for (int _i = 0; _i < 2; ++_i) \
;         __builtin_amdgcn_global_load_lds((const unsigned*)((const char*)(gbase) + (voff)[_i]), (LAS unsigned*)(lds + (bufoff) + ldsw + _i * 8192), 16, 0, 0); } while (0)
; #define PG8_LDA(dst, b, h) do { _Pragma("unroll") for (int m = 0; m < 4; ++m) dst[m] = PG8_LD32(lds + PG8_SA(b, h) + aoff + m * 2048); } while (0)
; #define PG8_LDB(dst, b, h) do { _Pragma("unroll") for (int n = 0; n < 2; ++n) dst[n] = PG8_LD32(lds + PG8_SB(b, h) + boff + n * 2048); } while (0)
; #define PG8_WAIT_V(n) asm volatile("s_waitcnt vmcnt(" #n ")" ::: "memory")
; #define PG8_WAIT_L(n) asm volatile("s_waitcnt lgkmcnt(" #n ")" ::: "memory")
; #define PG8_BAR __builtin_amdgcn_s_barrier()
; #define PG8_SCHED __builtin_amdgcn_sched_barrier(0)
; #define PG8_STA(bufoff, nextflag, h, koff) do { if constexpr (Sched::GATHER) { unsigned _o[2]; _o[0] = (nextflag) ? nxtA[h][0] : curA[h][0]; _o[1] = (nextflag) ? nxtA[h][1] : curA[h][1]; PG8_STAGE(bufoff, Ab + (koff), _o); } \
;         else { PG8_STAGE(bufoff, ((nextflag) ? nA : cA) + (size_t)(h) * hstep + (koff), voffA); } } while (0)
; template <class Epi, class Sched, bool ALIGN_EPI, int DT>
; __device__ __forceinline__ void gemm_phase(LAS unsigned char* lds, const int KB, const Sched& S, const Epi& E) {
;     ...
;             PG8_LDB(B0, 1, 0); PG8_LDB(B1, 1, 1); PG8_SCHED; PG8_LDA(At, 1, 0); PG8_STA(PG8_SA(0, 1), last, 1, k2);
;             PG8_WAIT_V(8); PG8_WAIT_L(0); PG8_BAR; PG8_MMA(0, 0, At, B0); PG8_MMA(0, 1, At, B1); PG8_BAR; PG8_SCHED;
;             PG8_LDA(At, 1, 1); PG8_STAGE(PG8_SB(1, 0), b3, voffB); PG8_STAGE(PG8_SB(1, 1), b3 + hstep, voffB); PG8_STA(PG8_SA(1, 0), last, 0, k3);
;             PG8_WAIT_V(8); PG8_WAIT_L(0); PG8_BAR; PG8_MMA(1, 0, At, B0); PG8_MMA(1, 1, At, B1); PG8_BAR; PG8_SCHED;
;         }
;         if constexpr (ALIGN_EPI) { if (wr == 0) PG8_BAR; }
	s_add_i32 s74, 0, 0x18000
	s_add_i32 s75, 0, 0x1c000
	v_add_u32_e32 v14, s74, v196
	v_add_u32_e32 v30, s75, v196
	ds_read_b128 v[2:5], v14
	ds_read_b128 v[6:9], v14 offset:1024
	ds_read_b128 v[10:13], v14 offset:2048
	ds_read_b128 v[14:17], v14 offset:3072
	ds_read_b128 v[18:21], v30
	ds_read_b128 v[22:25], v30 offset:1024
	ds_read_b128 v[26:29], v30 offset:2048
	ds_read_b128 v[30:33], v30 offset:3072
	s_add_u32 s44, s44, 0x58000
	s_addc_u32 s45, s45, 0
	s_mov_b32 m0, s46
	v_lshl_add_u64 v[234:235], s[44:45], 0, v[166:167]
	ds_read_b128 v[202:205], v200 offset:32768
	ds_read_b128 v[206:209], v200 offset:33792
	ds_read_b128 v[210:213], v200 offset:34816
	ds_read_b128 v[214:217], v200 offset:35840
	ds_read_b128 v[218:221], v200 offset:36864
	ds_read_b128 v[222:225], v200 offset:37888
	ds_read_b128 v[226:229], v200 offset:38912
	ds_read_b128 v[230:233], v200 offset:39936
	global_load_lds_dwordx4 v[234:235], off
	v_lshl_add_u64 v[234:235], s[44:45], 0, v[168:169]
	s_mov_b32 m0, s47
	s_nop 0
	global_load_lds_dwordx4 v[234:235], off
	s_waitcnt vmcnt(8) lgkmcnt(0)
	s_barrier
	s_setprio 1
	v_mfma_scale_f32_16x16x128_f8f6f4 v[158:161], v[2:9], v[202:209], v[158:161], v1, v1 op_sel_hi:[0,0,0]
	v_mfma_scale_f32_16x16x128_f8f6f4 v[154:157], v[10:17], v[202:209], v[154:157], v1, v1 op_sel_hi:[0,0,0]
	v_mfma_scale_f32_16x16x128_f8f6f4 v[150:153], v[2:9], v[210:217], v[150:153], v1, v1 op_sel_hi:[0,0,0]
	v_mfma_scale_f32_16x16x128_f8f6f4 v[142:145], v[10:17], v[210:217], v[142:145], v1, v1 op_sel_hi:[0,0,0]
	v_mfma_scale_f32_16x16x128_f8f6f4 v[134:137], v[2:9], v[218:225], v[134:137], v1, v1 op_sel_hi:[0,0,0]
	v_mfma_scale_f32_16x16x128_f8f6f4 v[126:129], v[10:17], v[218:225], v[126:129], v1, v1 op_sel_hi:[0,0,0]
	v_mfma_scale_f32_16x16x128_f8f6f4 v[118:121], v[2:9], v[226:233], v[118:121], v1, v1 op_sel_hi:[0,0,0]
	v_mfma_scale_f32_16x16x128_f8f6f4 v[110:113], v[10:17], v[226:233], v[110:113], v1, v1 op_sel_hi:[0,0,0]
	v_mfma_scale_f32_16x16x128_f8f6f4 v[146:149], v[18:25], v[202:209], v[146:149], v1, v1 op_sel_hi:[0,0,0]
	v_mfma_scale_f32_16x16x128_f8f6f4 v[138:141], v[26:33], v[202:209], v[138:141], v1, v1 op_sel_hi:[0,0,0]
	v_mfma_scale_f32_16x16x128_f8f6f4 v[130:133], v[18:25], v[210:217], v[130:133], v1, v1 op_sel_hi:[0,0,0]
	v_mfma_scale_f32_16x16x128_f8f6f4 v[122:125], v[26:33], v[210:217], v[122:125], v1, v1 op_sel_hi:[0,0,0]
	v_mfma_scale_f32_16x16x128_f8f6f4 v[114:117], v[18:25], v[218:225], v[114:117], v1, v1 op_sel_hi:[0,0,0]
	v_mfma_scale_f32_16x16x128_f8f6f4 v[106:109], v[26:33], v[218:225], v[106:109], v1, v1 op_sel_hi:[0,0,0]
	v_mfma_scale_f32_16x16x128_f8f6f4 v[102:105], v[18:25], v[226:233], v[102:105], v1, v1 op_sel_hi:[0,0,0]
	v_mfma_scale_f32_16x16x128_f8f6f4 v[98:101], v[26:33], v[226:233], v[98:101], v1, v1 op_sel_hi:[0,0,0]
	s_setprio 0
	s_barrier
	s_add_i32 s44, s74, s4
	v_lshl_add_u64 v[188:189], v[188:189], 0, s[16:17]
	s_mov_b32 m0, s44
	ds_read_b128 v[202:205], v200 offset:49152
	ds_read_b128 v[206:209], v200 offset:50176
	ds_read_b128 v[210:213], v200 offset:51200
	ds_read_b128 v[214:217], v200 offset:52224
	ds_read_b128 v[218:221], v200 offset:53248
	ds_read_b128 v[222:225], v200 offset:54272
	ds_read_b128 v[226:229], v200 offset:55296
	ds_read_b128 v[230:233], v200 offset:56320
	global_load_lds_dwordx4 v[188:189], off
	v_lshl_add_u64 v[186:187], v[186:187], 0, s[16:17]
	s_add_i32 m0, s44, 0x2000
	v_lshl_add_u64 v[184:185], v[184:185], 0, s[18:19]
	s_add_i32 s44, s75, s4
	global_load_lds_dwordx4 v[186:187], off
	v_lshl_add_u64 v[186:187], v[184:185], 0, v[170:171]
	s_mov_b32 m0, s44
	v_lshl_add_u64 v[184:185], v[184:185], 0, v[164:165]
	global_load_lds_dwordx4 v[186:187], off
	s_add_i32 m0, s44, 0x2000
	s_nop 0
	global_load_lds_dwordx4 v[184:185], off
	v_lshl_add_u64 v[184:185], v[190:191], 0, s[16:17]
	s_mov_b32 m0, s52
	s_nop 0
	global_load_lds_dwordx4 v[184:185], off
	v_lshl_add_u64 v[184:185], v[192:193], 0, s[16:17]
	s_mov_b32 m0, s53
	s_nop 0
	global_load_lds_dwordx4 v[184:185], off
	s_waitcnt vmcnt(8) lgkmcnt(0)
	s_barrier
	s_setprio 1
	v_mfma_scale_f32_16x16x128_f8f6f4 v[94:97], v[2:9], v[202:209], v[94:97], v1, v1 op_sel_hi:[0,0,0]
	v_mfma_scale_f32_16x16x128_f8f6f4 v[90:93], v[10:17], v[202:209], v[90:93], v1, v1 op_sel_hi:[0,0,0]
	v_mfma_scale_f32_16x16x128_f8f6f4 v[86:89], v[2:9], v[210:217], v[86:89], v1, v1 op_sel_hi:[0,0,0]
	v_mfma_scale_f32_16x16x128_f8f6f4 v[78:81], v[10:17], v[210:217], v[78:81], v1, v1 op_sel_hi:[0,0,0]
	v_mfma_scale_f32_16x16x128_f8f6f4 v[62:65], v[2:9], v[218:225], v[62:65], v1, v1 op_sel_hi:[0,0,0]
	v_mfma_scale_f32_16x16x128_f8f6f4 v[54:57], v[10:17], v[218:225], v[54:57], v1, v1 op_sel_hi:[0,0,0]
	v_mfma_scale_f32_16x16x128_f8f6f4 v[46:49], v[2:9], v[226:233], v[46:49], v1, v1 op_sel_hi:[0,0,0]
	v_mfma_scale_f32_16x16x128_f8f6f4 v[38:41], v[10:17], v[226:233], v[38:41], v1, v1 op_sel_hi:[0,0,0]
	v_mfma_scale_f32_16x16x128_f8f6f4 v[82:85], v[18:25], v[202:209], v[82:85], v1, v1 op_sel_hi:[0,0,0]
	v_mfma_scale_f32_16x16x128_f8f6f4 v[74:77], v[26:33], v[202:209], v[74:77], v1, v1 op_sel_hi:[0,0,0]
	v_mfma_scale_f32_16x16x128_f8f6f4 v[58:61], v[18:25], v[210:217], v[58:61], v1, v1 op_sel_hi:[0,0,0]
	v_mfma_scale_f32_16x16x128_f8f6f4 v[50:53], v[26:33], v[210:217], v[50:53], v1, v1 op_sel_hi:[0,0,0]
	v_mfma_scale_f32_16x16x128_f8f6f4 v[42:45], v[18:25], v[218:225], v[42:45], v1, v1 op_sel_hi:[0,0,0]
	v_mfma_scale_f32_16x16x128_f8f6f4 v[34:37], v[26:33], v[218:225], v[34:37], v1, v1 op_sel_hi:[0,0,0]
	v_mfma_scale_f32_16x16x128_f8f6f4 v[70:73], v[18:25], v[226:233], v[70:73], v1, v1 op_sel_hi:[0,0,0]
	v_mfma_scale_f32_16x16x128_f8f6f4 v[66:69], v[26:33], v[226:233], v[66:69], v1, v1 op_sel_hi:[0,0,0]
	s_setprio 0
	s_barrier
	s_add_i32 s71, s71, 2
	s_cmp_gt_u32 s71, 19
	s_mov_b64 s[44:45], s[42:43]
	s_cbranch_scc0 .LBB0_2387
	s_and_b64 vcc, exec, s[20:21]
	s_cbranch_vccz .LBB0_2390
	s_barrier
